# static priority: waves 4-7 run at s_setprio 1 for the whole kernel, all per-segment s_setprio toggles removed
# baseline (speedup 1.0000x reference)
_Z8skel_fwd4Args:
	v_cmp_lt_u32_e32 vcc, 255, v0
	s_cbranch_vccz .Lprio_skip
	s_setprio 1
.Lprio_skip:
	s_load_dword s54, s[0:1], 0x118
	s_mov_b64 s[86:87], s[0:1]
	s_add_u32 s0, s86, 0x118
	s_addc_u32 s1, s87, 0
	s_mov_b32 s85, s2
	v_writelane_b32 v252, s0, 0
	s_mov_b32 s30, s2
	s_nop 0
	v_writelane_b32 v252, s1, 1
	s_waitcnt lgkmcnt(0)
	s_and_b32 s0, s54, 7
	s_cmp_lg_u32 s0, 0
	s_cbranch_scc1 .LBB0_2
	s_ashr_i32 s1, s85, 31
	s_lshr_b32 s1, s1, 29
	s_add_i32 s1, s85, s1
	s_and_b32 s2, s1, -8
	s_ashr_i32 s0, s54, 3
	s_sub_i32 s2, s85, s2
	s_mul_i32 s0, s0, s2
	s_ashr_i32 s1, s1, 3
	s_add_i32 s30, s0, s1

.LBB0_210:
	s_ashr_i32 s49, s48, 31
	s_lshl_b64 s[4:5], s[48:49], 19
	s_add_u32 s50, s6, s4
	s_addc_u32 s51, s7, s5
	s_and_b64 s[4:5], s[38:39], exec
	s_cselect_b32 s49, s51, s41
	s_cselect_b32 s64, s50, s40
	s_ashr_i32 s45, s44, 31
	s_lshl_b64 s[4:5], s[44:45], 19
	s_add_u32 s52, s8, s4
	s_addc_u32 s53, s9, s5
	s_and_b64 s[4:5], s[38:39], exec
	s_cselect_b32 s45, s53, s43
	s_cselect_b32 s65, s52, s42
	s_add_u32 s70, s64, 0x80
	s_addc_u32 s71, s49, 0
	s_add_u32 s4, s40, 0x40080
	s_addc_u32 s5, s41, 0
	s_add_u32 s78, s42, 0x100
	v_lshl_add_u64 v[144:145], s[4:5], 0, v[140:141]
	v_lshl_add_u64 v[146:147], s[4:5], 0, v[142:143]
	s_addc_u32 s79, s43, 0
	s_mov_b32 s80, -2
	s_mov_b64 s[42:43], 0
	s_waitcnt lgkmcnt(0)
	s_add_u32 s4, s40, s42
	s_addc_u32 s5, s41, s43
	s_add_u32 s81, s4, 0x100
	s_addc_u32 s82, s5, 0
	s_add_u32 s60, s78, s42
	s_addc_u32 s61, s79, s43
	s_add_u32 s4, s4, 0x180
	s_addc_u32 s5, s5, 0
	s_add_i32 s83, 0, 0x10000
	s_add_i32 s84, 0, 0x14000
	v_add_u32_e32 v2, s83, v151
	s_waitcnt vmcnt(0)
	ds_read_b128 v[154:157], v2
	ds_read_b128 v[158:161], v2 offset:1024
	ds_read_b128 v[162:165], v2 offset:2048
	ds_read_b128 v[166:169], v2 offset:3072
	v_add_u32_e32 v2, s84, v151
	ds_read_b128 v[170:173], v2
	ds_read_b128 v[174:177], v2 offset:1024
	ds_read_b128 v[178:181], v2 offset:2048
	ds_read_b128 v[182:185], v2 offset:3072
	s_cmpk_eq_i32 s42, 0x700
	s_cselect_b32 s13, s71, s5
	s_cselect_b32 s12, s70, s4
	s_cselect_b32 s61, s45, s61
	s_cselect_b32 s60, s65, s60
	s_cselect_b32 s5, s49, s82
	s_cselect_b32 s4, s64, s81
	v_lshl_add_u64 v[148:149], v[144:145], 0, s[42:43]
	s_add_i32 m0, s17, 0xc000
	ds_read_b128 v[186:189], v153
	ds_read_b128 v[190:193], v153 offset:1024
	ds_read_b128 v[204:207], v153 offset:2048
	ds_read_b128 v[208:211], v153 offset:3072
	ds_read_b128 v[212:215], v153 offset:4096
	ds_read_b128 v[216:219], v153 offset:5120
	ds_read_b128 v[220:223], v153 offset:6144
	ds_read_b128 v[224:227], v153 offset:7168
	global_load_lds_dwordx4 v[148:149], off
	v_lshl_add_u64 v[148:149], v[146:147], 0, s[42:43]
	s_add_i32 m0, s17, 0xe000
	s_nop 0
	global_load_lds_dwordx4 v[148:149], off
	s_waitcnt vmcnt(8)
	s_waitcnt lgkmcnt(0)
	s_barrier
	v_mfma_f32_16x16x32_bf16 v[128:131], v[154:157], v[186:189], 0
	v_mfma_f32_16x16x32_bf16 v[124:127], v[162:165], v[186:189], 0
	v_mfma_f32_16x16x32_bf16 v[112:115], v[154:157], v[204:207], 0
	v_mfma_f32_16x16x32_bf16 v[108:111], v[162:165], v[204:207], 0
	v_mfma_f32_16x16x32_bf16 v[96:99], v[154:157], v[212:215], 0
	v_mfma_f32_16x16x32_bf16 v[92:95], v[162:165], v[212:215], 0
	v_mfma_f32_16x16x32_bf16 v[80:83], v[154:157], v[220:223], 0
	v_mfma_f32_16x16x32_bf16 v[76:79], v[162:165], v[220:223], 0
	v_mfma_f32_16x16x32_bf16 v[128:131], v[158:161], v[190:193], v[128:131]
	v_mfma_f32_16x16x32_bf16 v[124:127], v[166:169], v[190:193], v[124:127]
	v_mfma_f32_16x16x32_bf16 v[112:115], v[158:161], v[208:211], v[112:115]
	v_mfma_f32_16x16x32_bf16 v[108:111], v[166:169], v[208:211], v[108:111]
	v_mfma_f32_16x16x32_bf16 v[96:99], v[158:161], v[216:219], v[96:99]
	v_mfma_f32_16x16x32_bf16 v[92:95], v[166:169], v[216:219], v[92:95]
	v_mfma_f32_16x16x32_bf16 v[80:83], v[158:161], v[224:227], v[80:83]
	v_mfma_f32_16x16x32_bf16 v[76:79], v[166:169], v[224:227], v[76:79]
	v_mfma_f32_16x16x32_bf16 v[120:123], v[170:173], v[186:189], 0
	v_mfma_f32_16x16x32_bf16 v[116:119], v[178:181], v[186:189], 0
	v_mfma_f32_16x16x32_bf16 v[104:107], v[170:173], v[204:207], 0
	v_mfma_f32_16x16x32_bf16 v[100:103], v[178:181], v[204:207], 0
	v_mfma_f32_16x16x32_bf16 v[88:91], v[170:173], v[212:215], 0
	v_mfma_f32_16x16x32_bf16 v[84:87], v[178:181], v[212:215], 0
	v_mfma_f32_16x16x32_bf16 v[72:75], v[170:173], v[220:223], 0
	v_mfma_f32_16x16x32_bf16 v[68:71], v[178:181], v[220:223], 0
	v_mfma_f32_16x16x32_bf16 v[120:123], v[174:177], v[190:193], v[120:123]
	v_mfma_f32_16x16x32_bf16 v[116:119], v[182:185], v[190:193], v[116:119]
	v_mfma_f32_16x16x32_bf16 v[104:107], v[174:177], v[208:211], v[104:107]
	v_mfma_f32_16x16x32_bf16 v[100:103], v[182:185], v[208:211], v[100:103]
	v_mfma_f32_16x16x32_bf16 v[88:91], v[174:177], v[216:219], v[88:91]
	v_mfma_f32_16x16x32_bf16 v[84:87], v[182:185], v[216:219], v[84:87]
	v_mfma_f32_16x16x32_bf16 v[72:75], v[174:177], v[224:227], v[72:75]
	v_mfma_f32_16x16x32_bf16 v[68:71], v[182:185], v[224:227], v[68:71]
	s_barrier
	s_add_i32 s81, s83, s16
	v_lshl_add_u64 v[148:149], s[60:61], 0, v[136:137]
	s_mov_b32 m0, s81
	ds_read_b128 v[186:189], v153 offset:16384
	ds_read_b128 v[190:193], v153 offset:17408
	ds_read_b128 v[204:207], v153 offset:18432
	ds_read_b128 v[208:211], v153 offset:19456
	ds_read_b128 v[212:215], v153 offset:20480
	ds_read_b128 v[216:219], v153 offset:21504
	ds_read_b128 v[220:223], v153 offset:22528
	ds_read_b128 v[224:227], v153 offset:23552
	global_load_lds_dwordx4 v[148:149], off
	s_add_i32 m0, s81, 0x2000
	s_add_u32 s82, s60, 0x40000
	v_lshl_add_u64 v[194:195], s[60:61], 0, v[132:133]
	s_addc_u32 s83, s61, 0
	s_add_i32 s81, s84, s16
	global_load_lds_dwordx4 v[194:195], off
	v_lshl_add_u64 v[196:197], s[82:83], 0, v[136:137]
	s_mov_b32 m0, s81
	s_nop 0
	global_load_lds_dwordx4 v[196:197], off
	v_lshl_add_u64 v[196:197], s[82:83], 0, v[132:133]
	s_add_i32 m0, s81, 0x2000
	s_nop 0
	global_load_lds_dwordx4 v[196:197], off
	v_lshl_add_u64 v[196:197], s[4:5], 0, v[138:139]
	s_mov_b32 m0, s17
	s_nop 0
	global_load_lds_dwordx4 v[196:197], off
	v_lshl_add_u64 v[196:197], s[4:5], 0, v[134:135]
	s_mov_b32 m0, s46
	s_nop 0
	global_load_lds_dwordx4 v[196:197], off
	s_waitcnt vmcnt(8)
	s_waitcnt lgkmcnt(0)
	s_barrier
	v_mfma_f32_16x16x32_bf16 v[64:67], v[154:157], v[186:189], 0
	v_mfma_f32_16x16x32_bf16 v[60:63], v[162:165], v[186:189], 0
	v_mfma_f32_16x16x32_bf16 v[48:51], v[154:157], v[204:207], 0
	v_mfma_f32_16x16x32_bf16 v[44:47], v[162:165], v[204:207], 0
	v_mfma_f32_16x16x32_bf16 v[32:35], v[154:157], v[212:215], 0
	v_mfma_f32_16x16x32_bf16 v[28:31], v[162:165], v[212:215], 0
	v_mfma_f32_16x16x32_bf16 v[16:19], v[154:157], v[220:223], 0
	v_mfma_f32_16x16x32_bf16 v[12:15], v[162:165], v[220:223], 0
	v_mfma_f32_16x16x32_bf16 v[64:67], v[158:161], v[190:193], v[64:67]
	v_mfma_f32_16x16x32_bf16 v[60:63], v[166:169], v[190:193], v[60:63]
	v_mfma_f32_16x16x32_bf16 v[48:51], v[158:161], v[208:211], v[48:51]
	v_mfma_f32_16x16x32_bf16 v[44:47], v[166:169], v[208:211], v[44:47]
	v_mfma_f32_16x16x32_bf16 v[32:35], v[158:161], v[216:219], v[32:35]
	v_mfma_f32_16x16x32_bf16 v[28:31], v[166:169], v[216:219], v[28:31]
	v_mfma_f32_16x16x32_bf16 v[16:19], v[158:161], v[224:227], v[16:19]
	v_mfma_f32_16x16x32_bf16 v[12:15], v[166:169], v[224:227], v[12:15]
	v_mfma_f32_16x16x32_bf16 v[56:59], v[170:173], v[186:189], 0
	v_mfma_f32_16x16x32_bf16 v[52:55], v[178:181], v[186:189], 0
	v_mfma_f32_16x16x32_bf16 v[40:43], v[170:173], v[204:207], 0
	v_mfma_f32_16x16x32_bf16 v[36:39], v[178:181], v[204:207], 0
	v_mfma_f32_16x16x32_bf16 v[24:27], v[170:173], v[212:215], 0
	v_mfma_f32_16x16x32_bf16 v[20:23], v[178:181], v[212:215], 0
	v_mfma_f32_16x16x32_bf16 v[8:11], v[170:173], v[220:223], 0
	v_mfma_f32_16x16x32_bf16 v[4:7], v[178:181], v[220:223], 0
	v_mfma_f32_16x16x32_bf16 v[56:59], v[174:177], v[190:193], v[56:59]
	v_mfma_f32_16x16x32_bf16 v[52:55], v[182:185], v[190:193], v[52:55]
	v_mfma_f32_16x16x32_bf16 v[40:43], v[174:177], v[208:211], v[40:43]
	v_mfma_f32_16x16x32_bf16 v[36:39], v[182:185], v[208:211], v[36:39]
	v_mfma_f32_16x16x32_bf16 v[24:27], v[174:177], v[216:219], v[24:27]
	v_mfma_f32_16x16x32_bf16 v[20:23], v[182:185], v[216:219], v[20:23]
	v_mfma_f32_16x16x32_bf16 v[8:11], v[174:177], v[224:227], v[8:11]
	v_mfma_f32_16x16x32_bf16 v[4:7], v[182:185], v[224:227], v[4:7]
	s_barrier
	s_add_i32 s81, 0, 0x18000
	v_add_u32_e32 v2, s81, v151
	s_add_i32 s82, 0, 0x1c000
	ds_read_b128 v[154:157], v2
	ds_read_b128 v[158:161], v2 offset:1024
	ds_read_b128 v[162:165], v2 offset:2048
	ds_read_b128 v[166:169], v2 offset:3072
	v_add_u32_e32 v2, s82, v151
	ds_read_b128 v[170:173], v2
	ds_read_b128 v[174:177], v2 offset:1024
	ds_read_b128 v[178:181], v2 offset:2048
	ds_read_b128 v[182:185], v2 offset:3072
	s_add_u32 s4, s4, 0x40000
	s_addc_u32 s5, s5, 0
	s_mov_b32 m0, s47
	v_lshl_add_u64 v[196:197], s[4:5], 0, v[138:139]
	ds_read_b128 v[186:189], v153 offset:32768
	ds_read_b128 v[190:193], v153 offset:33792
	ds_read_b128 v[204:207], v153 offset:34816
	ds_read_b128 v[208:211], v153 offset:35840
	ds_read_b128 v[212:215], v153 offset:36864
	ds_read_b128 v[216:219], v153 offset:37888
	ds_read_b128 v[220:223], v153 offset:38912
	ds_read_b128 v[224:227], v153 offset:39936
	global_load_lds_dwordx4 v[196:197], off
	v_lshl_add_u64 v[196:197], s[4:5], 0, v[134:135]
	s_mov_b32 m0, s58
	s_nop 0
	global_load_lds_dwordx4 v[196:197], off
	s_waitcnt vmcnt(8)
	s_waitcnt lgkmcnt(0)
	s_barrier
	v_mfma_f32_16x16x32_bf16 v[128:131], v[154:157], v[186:189], v[128:131]
	v_mfma_f32_16x16x32_bf16 v[124:127], v[162:165], v[186:189], v[124:127]
	v_mfma_f32_16x16x32_bf16 v[112:115], v[154:157], v[204:207], v[112:115]
	v_mfma_f32_16x16x32_bf16 v[108:111], v[162:165], v[204:207], v[108:111]
	v_mfma_f32_16x16x32_bf16 v[96:99], v[154:157], v[212:215], v[96:99]
	v_mfma_f32_16x16x32_bf16 v[92:95], v[162:165], v[212:215], v[92:95]
	v_mfma_f32_16x16x32_bf16 v[80:83], v[154:157], v[220:223], v[80:83]
	v_mfma_f32_16x16x32_bf16 v[76:79], v[162:165], v[220:223], v[76:79]
	v_mfma_f32_16x16x32_bf16 v[128:131], v[158:161], v[190:193], v[128:131]
	v_mfma_f32_16x16x32_bf16 v[124:127], v[166:169], v[190:193], v[124:127]
	v_mfma_f32_16x16x32_bf16 v[112:115], v[158:161], v[208:211], v[112:115]
	v_mfma_f32_16x16x32_bf16 v[108:111], v[166:169], v[208:211], v[108:111]
	v_mfma_f32_16x16x32_bf16 v[96:99], v[158:161], v[216:219], v[96:99]
	v_mfma_f32_16x16x32_bf16 v[92:95], v[166:169], v[216:219], v[92:95]
	v_mfma_f32_16x16x32_bf16 v[80:83], v[158:161], v[224:227], v[80:83]
	v_mfma_f32_16x16x32_bf16 v[76:79], v[166:169], v[224:227], v[76:79]
	v_mfma_f32_16x16x32_bf16 v[120:123], v[170:173], v[186:189], v[120:123]
	v_mfma_f32_16x16x32_bf16 v[116:119], v[178:181], v[186:189], v[116:119]
	v_mfma_f32_16x16x32_bf16 v[104:107], v[170:173], v[204:207], v[104:107]
	v_mfma_f32_16x16x32_bf16 v[100:103], v[178:181], v[204:207], v[100:103]
	v_mfma_f32_16x16x32_bf16 v[88:91], v[170:173], v[212:215], v[88:91]
	v_mfma_f32_16x16x32_bf16 v[84:87], v[178:181], v[212:215], v[84:87]
	v_mfma_f32_16x16x32_bf16 v[72:75], v[170:173], v[220:223], v[72:75]
	v_mfma_f32_16x16x32_bf16 v[68:71], v[178:181], v[220:223], v[68:71]
	v_mfma_f32_16x16x32_bf16 v[120:123], v[174:177], v[190:193], v[120:123]
	v_mfma_f32_16x16x32_bf16 v[116:119], v[182:185], v[190:193], v[116:119]
	v_mfma_f32_16x16x32_bf16 v[104:107], v[174:177], v[208:211], v[104:107]
	v_mfma_f32_16x16x32_bf16 v[100:103], v[182:185], v[208:211], v[100:103]
	v_mfma_f32_16x16x32_bf16 v[88:91], v[174:177], v[216:219], v[88:91]
	v_mfma_f32_16x16x32_bf16 v[84:87], v[182:185], v[216:219], v[84:87]
	v_mfma_f32_16x16x32_bf16 v[72:75], v[174:177], v[224:227], v[72:75]
	v_mfma_f32_16x16x32_bf16 v[68:71], v[182:185], v[224:227], v[68:71]
	s_barrier
	s_add_i32 s4, s81, s16
	v_lshl_add_u64 v[148:149], v[148:149], 0, s[34:35]
	s_mov_b32 m0, s4
	ds_read_b128 v[186:189], v153 offset:49152
	ds_read_b128 v[190:193], v153 offset:50176
	ds_read_b128 v[204:207], v153 offset:51200
	ds_read_b128 v[208:211], v153 offset:52224
	ds_read_b128 v[212:215], v153 offset:53248
	ds_read_b128 v[216:219], v153 offset:54272
	ds_read_b128 v[220:223], v153 offset:55296
	ds_read_b128 v[224:227], v153 offset:56320
	global_load_lds_dwordx4 v[148:149], off
	s_add_i32 m0, s4, 0x2000
	s_add_u32 s4, s60, 0x40080
	v_lshl_add_u64 v[148:149], v[194:195], 0, s[34:35]
	s_addc_u32 s5, s61, 0
	s_add_i32 s60, s82, s16
	global_load_lds_dwordx4 v[148:149], off
	v_lshl_add_u64 v[148:149], s[4:5], 0, v[136:137]
	s_mov_b32 m0, s60
	s_nop 0
	global_load_lds_dwordx4 v[148:149], off
	v_lshl_add_u64 v[148:149], s[4:5], 0, v[132:133]
	s_add_i32 m0, s60, 0x2000
	s_nop 0
	global_load_lds_dwordx4 v[148:149], off
	v_lshl_add_u64 v[148:149], s[12:13], 0, v[138:139]
	s_mov_b32 m0, s74
	s_nop 0
	global_load_lds_dwordx4 v[148:149], off
	v_lshl_add_u64 v[148:149], s[12:13], 0, v[134:135]
	s_mov_b32 m0, s75
	s_nop 0
	global_load_lds_dwordx4 v[148:149], off
	s_waitcnt vmcnt(8)
	s_waitcnt lgkmcnt(0)
	s_barrier
	v_mfma_f32_16x16x32_bf16 v[64:67], v[154:157], v[186:189], v[64:67]
	v_mfma_f32_16x16x32_bf16 v[60:63], v[162:165], v[186:189], v[60:63]
	v_mfma_f32_16x16x32_bf16 v[48:51], v[154:157], v[204:207], v[48:51]
	v_mfma_f32_16x16x32_bf16 v[44:47], v[162:165], v[204:207], v[44:47]
	v_mfma_f32_16x16x32_bf16 v[32:35], v[154:157], v[212:215], v[32:35]
	v_mfma_f32_16x16x32_bf16 v[28:31], v[162:165], v[212:215], v[28:31]
	v_mfma_f32_16x16x32_bf16 v[16:19], v[154:157], v[220:223], v[16:19]
	v_mfma_f32_16x16x32_bf16 v[12:15], v[162:165], v[220:223], v[12:15]
	v_mfma_f32_16x16x32_bf16 v[64:67], v[158:161], v[190:193], v[64:67]
	v_mfma_f32_16x16x32_bf16 v[60:63], v[166:169], v[190:193], v[60:63]
	v_mfma_f32_16x16x32_bf16 v[48:51], v[158:161], v[208:211], v[48:51]
	v_mfma_f32_16x16x32_bf16 v[44:47], v[166:169], v[208:211], v[44:47]
	v_mfma_f32_16x16x32_bf16 v[32:35], v[158:161], v[216:219], v[32:35]
	v_mfma_f32_16x16x32_bf16 v[28:31], v[166:169], v[216:219], v[28:31]
	v_mfma_f32_16x16x32_bf16 v[16:19], v[158:161], v[224:227], v[16:19]
	v_mfma_f32_16x16x32_bf16 v[12:15], v[166:169], v[224:227], v[12:15]
	v_mfma_f32_16x16x32_bf16 v[56:59], v[170:173], v[186:189], v[56:59]
	v_mfma_f32_16x16x32_bf16 v[52:55], v[178:181], v[186:189], v[52:55]
	v_mfma_f32_16x16x32_bf16 v[40:43], v[170:173], v[204:207], v[40:43]
	v_mfma_f32_16x16x32_bf16 v[36:39], v[178:181], v[204:207], v[36:39]
	v_mfma_f32_16x16x32_bf16 v[24:27], v[170:173], v[212:215], v[24:27]
	v_mfma_f32_16x16x32_bf16 v[20:23], v[178:181], v[212:215], v[20:23]
	v_mfma_f32_16x16x32_bf16 v[8:11], v[170:173], v[220:223], v[8:11]
	v_mfma_f32_16x16x32_bf16 v[4:7], v[178:181], v[220:223], v[4:7]
	v_mfma_f32_16x16x32_bf16 v[56:59], v[174:177], v[190:193], v[56:59]
	v_mfma_f32_16x16x32_bf16 v[52:55], v[182:185], v[190:193], v[52:55]
	v_mfma_f32_16x16x32_bf16 v[40:43], v[174:177], v[208:211], v[40:43]
	v_mfma_f32_16x16x32_bf16 v[36:39], v[182:185], v[208:211], v[36:39]
	v_mfma_f32_16x16x32_bf16 v[24:27], v[174:177], v[216:219], v[24:27]
	v_mfma_f32_16x16x32_bf16 v[20:23], v[182:185], v[216:219], v[20:23]
	v_mfma_f32_16x16x32_bf16 v[8:11], v[174:177], v[224:227], v[8:11]
	v_mfma_f32_16x16x32_bf16 v[4:7], v[182:185], v[224:227], v[4:7]
	s_barrier
	s_add_i32 s80, s80, 2
	s_add_u32 s42, s42, 0x100
	s_addc_u32 s43, s43, 0
	s_cmp_gt_u32 s80, 13
.LBB0_211:
	s_add_u32 s4, s40, s42
	s_addc_u32 s5, s41, s43
	s_add_u32 s81, s4, 0x100
	s_addc_u32 s82, s5, 0
	s_add_u32 s60, s78, s42
	s_addc_u32 s61, s79, s43
	s_add_u32 s4, s4, 0x180
	s_addc_u32 s5, s5, 0
	s_add_i32 s83, 0, 0x10000
	s_add_i32 s84, 0, 0x14000
	v_add_u32_e32 v2, s83, v151
	s_waitcnt vmcnt(0)
	ds_read_b128 v[154:157], v2
	ds_read_b128 v[158:161], v2 offset:1024
	ds_read_b128 v[162:165], v2 offset:2048
	ds_read_b128 v[166:169], v2 offset:3072
	v_add_u32_e32 v2, s84, v151
	ds_read_b128 v[170:173], v2
	ds_read_b128 v[174:177], v2 offset:1024
	ds_read_b128 v[178:181], v2 offset:2048
	ds_read_b128 v[182:185], v2 offset:3072
	s_cmpk_eq_i32 s42, 0x700
	s_cselect_b32 s13, s71, s5
	s_cselect_b32 s12, s70, s4
	s_cselect_b32 s61, s45, s61
	s_cselect_b32 s60, s65, s60
	s_cselect_b32 s5, s49, s82
	s_cselect_b32 s4, s64, s81
	v_lshl_add_u64 v[148:149], v[144:145], 0, s[42:43]
	s_add_i32 m0, s17, 0xc000
	ds_read_b128 v[186:189], v153
	ds_read_b128 v[190:193], v153 offset:1024
	ds_read_b128 v[204:207], v153 offset:2048
	ds_read_b128 v[208:211], v153 offset:3072
	ds_read_b128 v[212:215], v153 offset:4096
	ds_read_b128 v[216:219], v153 offset:5120
	ds_read_b128 v[220:223], v153 offset:6144
	ds_read_b128 v[224:227], v153 offset:7168
	global_load_lds_dwordx4 v[148:149], off
	v_lshl_add_u64 v[148:149], v[146:147], 0, s[42:43]
	s_add_i32 m0, s17, 0xe000
	s_nop 0
	global_load_lds_dwordx4 v[148:149], off
	s_waitcnt vmcnt(8)
	s_waitcnt lgkmcnt(0)
	s_barrier
	v_mfma_f32_16x16x32_bf16 v[128:131], v[154:157], v[186:189], v[128:131]
	v_mfma_f32_16x16x32_bf16 v[124:127], v[162:165], v[186:189], v[124:127]
	v_mfma_f32_16x16x32_bf16 v[112:115], v[154:157], v[204:207], v[112:115]
	v_mfma_f32_16x16x32_bf16 v[108:111], v[162:165], v[204:207], v[108:111]
	v_mfma_f32_16x16x32_bf16 v[96:99], v[154:157], v[212:215], v[96:99]
	v_mfma_f32_16x16x32_bf16 v[92:95], v[162:165], v[212:215], v[92:95]
	v_mfma_f32_16x16x32_bf16 v[80:83], v[154:157], v[220:223], v[80:83]
	v_mfma_f32_16x16x32_bf16 v[76:79], v[162:165], v[220:223], v[76:79]
	v_mfma_f32_16x16x32_bf16 v[128:131], v[158:161], v[190:193], v[128:131]
	v_mfma_f32_16x16x32_bf16 v[124:127], v[166:169], v[190:193], v[124:127]
	v_mfma_f32_16x16x32_bf16 v[112:115], v[158:161], v[208:211], v[112:115]
	v_mfma_f32_16x16x32_bf16 v[108:111], v[166:169], v[208:211], v[108:111]
	v_mfma_f32_16x16x32_bf16 v[96:99], v[158:161], v[216:219], v[96:99]
	v_mfma_f32_16x16x32_bf16 v[92:95], v[166:169], v[216:219], v[92:95]
	v_mfma_f32_16x16x32_bf16 v[80:83], v[158:161], v[224:227], v[80:83]
	v_mfma_f32_16x16x32_bf16 v[76:79], v[166:169], v[224:227], v[76:79]
	v_mfma_f32_16x16x32_bf16 v[120:123], v[170:173], v[186:189], v[120:123]
	v_mfma_f32_16x16x32_bf16 v[116:119], v[178:181], v[186:189], v[116:119]
	v_mfma_f32_16x16x32_bf16 v[104:107], v[170:173], v[204:207], v[104:107]
	v_mfma_f32_16x16x32_bf16 v[100:103], v[178:181], v[204:207], v[100:103]
	v_mfma_f32_16x16x32_bf16 v[88:91], v[170:173], v[212:215], v[88:91]
	v_mfma_f32_16x16x32_bf16 v[84:87], v[178:181], v[212:215], v[84:87]
	v_mfma_f32_16x16x32_bf16 v[72:75], v[170:173], v[220:223], v[72:75]
	v_mfma_f32_16x16x32_bf16 v[68:71], v[178:181], v[220:223], v[68:71]
	v_mfma_f32_16x16x32_bf16 v[120:123], v[174:177], v[190:193], v[120:123]
	v_mfma_f32_16x16x32_bf16 v[116:119], v[182:185], v[190:193], v[116:119]
	v_mfma_f32_16x16x32_bf16 v[104:107], v[174:177], v[208:211], v[104:107]
	v_mfma_f32_16x16x32_bf16 v[100:103], v[182:185], v[208:211], v[100:103]
	v_mfma_f32_16x16x32_bf16 v[88:91], v[174:177], v[216:219], v[88:91]
	v_mfma_f32_16x16x32_bf16 v[84:87], v[182:185], v[216:219], v[84:87]
	v_mfma_f32_16x16x32_bf16 v[72:75], v[174:177], v[224:227], v[72:75]
	v_mfma_f32_16x16x32_bf16 v[68:71], v[182:185], v[224:227], v[68:71]
	s_barrier
	s_add_i32 s81, s83, s16
	v_lshl_add_u64 v[148:149], s[60:61], 0, v[136:137]
	s_mov_b32 m0, s81
	ds_read_b128 v[186:189], v153 offset:16384
	ds_read_b128 v[190:193], v153 offset:17408
	ds_read_b128 v[204:207], v153 offset:18432
	ds_read_b128 v[208:211], v153 offset:19456
	ds_read_b128 v[212:215], v153 offset:20480
	ds_read_b128 v[216:219], v153 offset:21504
	ds_read_b128 v[220:223], v153 offset:22528
	ds_read_b128 v[224:227], v153 offset:23552
	global_load_lds_dwordx4 v[148:149], off
	s_add_i32 m0, s81, 0x2000
	s_add_u32 s82, s60, 0x40000
	v_lshl_add_u64 v[194:195], s[60:61], 0, v[132:133]
	s_addc_u32 s83, s61, 0
	s_add_i32 s81, s84, s16
	global_load_lds_dwordx4 v[194:195], off
	v_lshl_add_u64 v[196:197], s[82:83], 0, v[136:137]
	s_mov_b32 m0, s81
	s_nop 0
	global_load_lds_dwordx4 v[196:197], off
	v_lshl_add_u64 v[196:197], s[82:83], 0, v[132:133]
	s_add_i32 m0, s81, 0x2000
	s_nop 0
	global_load_lds_dwordx4 v[196:197], off
	v_lshl_add_u64 v[196:197], s[4:5], 0, v[138:139]
	s_mov_b32 m0, s17
	s_nop 0
	global_load_lds_dwordx4 v[196:197], off
	v_lshl_add_u64 v[196:197], s[4:5], 0, v[134:135]
	s_mov_b32 m0, s46
	s_nop 0
	global_load_lds_dwordx4 v[196:197], off
	s_waitcnt vmcnt(8)
	s_waitcnt lgkmcnt(0)
	s_barrier
	v_mfma_f32_16x16x32_bf16 v[64:67], v[154:157], v[186:189], v[64:67]
	v_mfma_f32_16x16x32_bf16 v[60:63], v[162:165], v[186:189], v[60:63]
	v_mfma_f32_16x16x32_bf16 v[48:51], v[154:157], v[204:207], v[48:51]
	v_mfma_f32_16x16x32_bf16 v[44:47], v[162:165], v[204:207], v[44:47]
	v_mfma_f32_16x16x32_bf16 v[32:35], v[154:157], v[212:215], v[32:35]
	v_mfma_f32_16x16x32_bf16 v[28:31], v[162:165], v[212:215], v[28:31]
	v_mfma_f32_16x16x32_bf16 v[16:19], v[154:157], v[220:223], v[16:19]
	v_mfma_f32_16x16x32_bf16 v[12:15], v[162:165], v[220:223], v[12:15]
	v_mfma_f32_16x16x32_bf16 v[64:67], v[158:161], v[190:193], v[64:67]
	v_mfma_f32_16x16x32_bf16 v[60:63], v[166:169], v[190:193], v[60:63]
	v_mfma_f32_16x16x32_bf16 v[48:51], v[158:161], v[208:211], v[48:51]
	v_mfma_f32_16x16x32_bf16 v[44:47], v[166:169], v[208:211], v[44:47]
	v_mfma_f32_16x16x32_bf16 v[32:35], v[158:161], v[216:219], v[32:35]
	v_mfma_f32_16x16x32_bf16 v[28:31], v[166:169], v[216:219], v[28:31]
	v_mfma_f32_16x16x32_bf16 v[16:19], v[158:161], v[224:227], v[16:19]
	v_mfma_f32_16x16x32_bf16 v[12:15], v[166:169], v[224:227], v[12:15]
	v_mfma_f32_16x16x32_bf16 v[56:59], v[170:173], v[186:189], v[56:59]
	v_mfma_f32_16x16x32_bf16 v[52:55], v[178:181], v[186:189], v[52:55]
	v_mfma_f32_16x16x32_bf16 v[40:43], v[170:173], v[204:207], v[40:43]
	v_mfma_f32_16x16x32_bf16 v[36:39], v[178:181], v[204:207], v[36:39]
	v_mfma_f32_16x16x32_bf16 v[24:27], v[170:173], v[212:215], v[24:27]
	v_mfma_f32_16x16x32_bf16 v[20:23], v[178:181], v[212:215], v[20:23]
	v_mfma_f32_16x16x32_bf16 v[8:11], v[170:173], v[220:223], v[8:11]
	v_mfma_f32_16x16x32_bf16 v[4:7], v[178:181], v[220:223], v[4:7]
	v_mfma_f32_16x16x32_bf16 v[56:59], v[174:177], v[190:193], v[56:59]
	v_mfma_f32_16x16x32_bf16 v[52:55], v[182:185], v[190:193], v[52:55]
	v_mfma_f32_16x16x32_bf16 v[40:43], v[174:177], v[208:211], v[40:43]
	v_mfma_f32_16x16x32_bf16 v[36:39], v[182:185], v[208:211], v[36:39]
	v_mfma_f32_16x16x32_bf16 v[24:27], v[174:177], v[216:219], v[24:27]
	v_mfma_f32_16x16x32_bf16 v[20:23], v[182:185], v[216:219], v[20:23]
	v_mfma_f32_16x16x32_bf16 v[8:11], v[174:177], v[224:227], v[8:11]
	v_mfma_f32_16x16x32_bf16 v[4:7], v[182:185], v[224:227], v[4:7]
	s_barrier
	s_add_i32 s81, 0, 0x18000
	v_add_u32_e32 v2, s81, v151
	s_add_i32 s82, 0, 0x1c000
	ds_read_b128 v[154:157], v2
	ds_read_b128 v[158:161], v2 offset:1024
	ds_read_b128 v[162:165], v2 offset:2048
	ds_read_b128 v[166:169], v2 offset:3072
	v_add_u32_e32 v2, s82, v151
	ds_read_b128 v[170:173], v2
	ds_read_b128 v[174:177], v2 offset:1024
	ds_read_b128 v[178:181], v2 offset:2048
	ds_read_b128 v[182:185], v2 offset:3072
	s_add_u32 s4, s4, 0x40000
	s_addc_u32 s5, s5, 0
	s_mov_b32 m0, s47
	v_lshl_add_u64 v[196:197], s[4:5], 0, v[138:139]
	ds_read_b128 v[186:189], v153 offset:32768
	ds_read_b128 v[190:193], v153 offset:33792
	ds_read_b128 v[204:207], v153 offset:34816
	ds_read_b128 v[208:211], v153 offset:35840
	ds_read_b128 v[212:215], v153 offset:36864
	ds_read_b128 v[216:219], v153 offset:37888
	ds_read_b128 v[220:223], v153 offset:38912
	ds_read_b128 v[224:227], v153 offset:39936
	global_load_lds_dwordx4 v[196:197], off
	v_lshl_add_u64 v[196:197], s[4:5], 0, v[134:135]
	s_mov_b32 m0, s58
	s_nop 0
	global_load_lds_dwordx4 v[196:197], off
	s_waitcnt vmcnt(8)
	s_waitcnt lgkmcnt(0)
	s_barrier
	v_mfma_f32_16x16x32_bf16 v[128:131], v[154:157], v[186:189], v[128:131]
	v_mfma_f32_16x16x32_bf16 v[124:127], v[162:165], v[186:189], v[124:127]
	v_mfma_f32_16x16x32_bf16 v[112:115], v[154:157], v[204:207], v[112:115]
	v_mfma_f32_16x16x32_bf16 v[108:111], v[162:165], v[204:207], v[108:111]
	v_mfma_f32_16x16x32_bf16 v[96:99], v[154:157], v[212:215], v[96:99]
	v_mfma_f32_16x16x32_bf16 v[92:95], v[162:165], v[212:215], v[92:95]
	v_mfma_f32_16x16x32_bf16 v[80:83], v[154:157], v[220:223], v[80:83]
	v_mfma_f32_16x16x32_bf16 v[76:79], v[162:165], v[220:223], v[76:79]
	v_mfma_f32_16x16x32_bf16 v[128:131], v[158:161], v[190:193], v[128:131]
	v_mfma_f32_16x16x32_bf16 v[124:127], v[166:169], v[190:193], v[124:127]
	v_mfma_f32_16x16x32_bf16 v[112:115], v[158:161], v[208:211], v[112:115]
	v_mfma_f32_16x16x32_bf16 v[108:111], v[166:169], v[208:211], v[108:111]
	v_mfma_f32_16x16x32_bf16 v[96:99], v[158:161], v[216:219], v[96:99]
	v_mfma_f32_16x16x32_bf16 v[92:95], v[166:169], v[216:219], v[92:95]
	v_mfma_f32_16x16x32_bf16 v[80:83], v[158:161], v[224:227], v[80:83]
	v_mfma_f32_16x16x32_bf16 v[76:79], v[166:169], v[224:227], v[76:79]
	v_mfma_f32_16x16x32_bf16 v[120:123], v[170:173], v[186:189], v[120:123]
	v_mfma_f32_16x16x32_bf16 v[116:119], v[178:181], v[186:189], v[116:119]
	v_mfma_f32_16x16x32_bf16 v[104:107], v[170:173], v[204:207], v[104:107]
	v_mfma_f32_16x16x32_bf16 v[100:103], v[178:181], v[204:207], v[100:103]
	v_mfma_f32_16x16x32_bf16 v[88:91], v[170:173], v[212:215], v[88:91]
	v_mfma_f32_16x16x32_bf16 v[84:87], v[178:181], v[212:215], v[84:87]
	v_mfma_f32_16x16x32_bf16 v[72:75], v[170:173], v[220:223], v[72:75]
	v_mfma_f32_16x16x32_bf16 v[68:71], v[178:181], v[220:223], v[68:71]
	v_mfma_f32_16x16x32_bf16 v[120:123], v[174:177], v[190:193], v[120:123]
	v_mfma_f32_16x16x32_bf16 v[116:119], v[182:185], v[190:193], v[116:119]
	v_mfma_f32_16x16x32_bf16 v[104:107], v[174:177], v[208:211], v[104:107]
	v_mfma_f32_16x16x32_bf16 v[100:103], v[182:185], v[208:211], v[100:103]
	v_mfma_f32_16x16x32_bf16 v[88:91], v[174:177], v[216:219], v[88:91]
	v_mfma_f32_16x16x32_bf16 v[84:87], v[182:185], v[216:219], v[84:87]
	v_mfma_f32_16x16x32_bf16 v[72:75], v[174:177], v[224:227], v[72:75]
	v_mfma_f32_16x16x32_bf16 v[68:71], v[182:185], v[224:227], v[68:71]
	s_barrier
	s_add_i32 s4, s81, s16
	v_lshl_add_u64 v[148:149], v[148:149], 0, s[34:35]
	s_mov_b32 m0, s4
	ds_read_b128 v[186:189], v153 offset:49152
	ds_read_b128 v[190:193], v153 offset:50176
	ds_read_b128 v[204:207], v153 offset:51200
	ds_read_b128 v[208:211], v153 offset:52224
	ds_read_b128 v[212:215], v153 offset:53248
	ds_read_b128 v[216:219], v153 offset:54272
	ds_read_b128 v[220:223], v153 offset:55296
	ds_read_b128 v[224:227], v153 offset:56320
	global_load_lds_dwordx4 v[148:149], off
	s_add_i32 m0, s4, 0x2000
	s_add_u32 s4, s60, 0x40080
	v_lshl_add_u64 v[148:149], v[194:195], 0, s[34:35]
	s_addc_u32 s5, s61, 0
	s_add_i32 s60, s82, s16
	global_load_lds_dwordx4 v[148:149], off
	v_lshl_add_u64 v[148:149], s[4:5], 0, v[136:137]
	s_mov_b32 m0, s60
	s_nop 0
	global_load_lds_dwordx4 v[148:149], off
	v_lshl_add_u64 v[148:149], s[4:5], 0, v[132:133]
	s_add_i32 m0, s60, 0x2000
	s_nop 0
	global_load_lds_dwordx4 v[148:149], off
	v_lshl_add_u64 v[148:149], s[12:13], 0, v[138:139]
	s_mov_b32 m0, s74
	s_nop 0
	global_load_lds_dwordx4 v[148:149], off
	v_lshl_add_u64 v[148:149], s[12:13], 0, v[134:135]
	s_mov_b32 m0, s75
	s_nop 0
	global_load_lds_dwordx4 v[148:149], off
	s_waitcnt vmcnt(8)
	s_waitcnt lgkmcnt(0)
	s_barrier
	v_mfma_f32_16x16x32_bf16 v[64:67], v[154:157], v[186:189], v[64:67]
	v_mfma_f32_16x16x32_bf16 v[60:63], v[162:165], v[186:189], v[60:63]
	v_mfma_f32_16x16x32_bf16 v[48:51], v[154:157], v[204:207], v[48:51]
	v_mfma_f32_16x16x32_bf16 v[44:47], v[162:165], v[204:207], v[44:47]
	v_mfma_f32_16x16x32_bf16 v[32:35], v[154:157], v[212:215], v[32:35]
	v_mfma_f32_16x16x32_bf16 v[28:31], v[162:165], v[212:215], v[28:31]
	v_mfma_f32_16x16x32_bf16 v[16:19], v[154:157], v[220:223], v[16:19]
	v_mfma_f32_16x16x32_bf16 v[12:15], v[162:165], v[220:223], v[12:15]
	v_mfma_f32_16x16x32_bf16 v[64:67], v[158:161], v[190:193], v[64:67]
	v_mfma_f32_16x16x32_bf16 v[60:63], v[166:169], v[190:193], v[60:63]
	v_mfma_f32_16x16x32_bf16 v[48:51], v[158:161], v[208:211], v[48:51]
	v_mfma_f32_16x16x32_bf16 v[44:47], v[166:169], v[208:211], v[44:47]
	v_mfma_f32_16x16x32_bf16 v[32:35], v[158:161], v[216:219], v[32:35]
	v_mfma_f32_16x16x32_bf16 v[28:31], v[166:169], v[216:219], v[28:31]
	v_mfma_f32_16x16x32_bf16 v[16:19], v[158:161], v[224:227], v[16:19]
	v_mfma_f32_16x16x32_bf16 v[12:15], v[166:169], v[224:227], v[12:15]
	v_mfma_f32_16x16x32_bf16 v[56:59], v[170:173], v[186:189], v[56:59]
	v_mfma_f32_16x16x32_bf16 v[52:55], v[178:181], v[186:189], v[52:55]
	v_mfma_f32_16x16x32_bf16 v[40:43], v[170:173], v[204:207], v[40:43]
	v_mfma_f32_16x16x32_bf16 v[36:39], v[178:181], v[204:207], v[36:39]
	v_mfma_f32_16x16x32_bf16 v[24:27], v[170:173], v[212:215], v[24:27]
	v_mfma_f32_16x16x32_bf16 v[20:23], v[178:181], v[212:215], v[20:23]
	v_mfma_f32_16x16x32_bf16 v[8:11], v[170:173], v[220:223], v[8:11]
	v_mfma_f32_16x16x32_bf16 v[4:7], v[178:181], v[220:223], v[4:7]
	v_mfma_f32_16x16x32_bf16 v[56:59], v[174:177], v[190:193], v[56:59]
	v_mfma_f32_16x16x32_bf16 v[52:55], v[182:185], v[190:193], v[52:55]
	v_mfma_f32_16x16x32_bf16 v[40:43], v[174:177], v[208:211], v[40:43]
	v_mfma_f32_16x16x32_bf16 v[36:39], v[182:185], v[208:211], v[36:39]
	v_mfma_f32_16x16x32_bf16 v[24:27], v[174:177], v[216:219], v[24:27]
	v_mfma_f32_16x16x32_bf16 v[20:23], v[182:185], v[216:219], v[20:23]
	v_mfma_f32_16x16x32_bf16 v[8:11], v[174:177], v[224:227], v[8:11]
	v_mfma_f32_16x16x32_bf16 v[4:7], v[182:185], v[224:227], v[4:7]
	s_barrier
	s_add_i32 s80, s80, 2
	s_add_u32 s42, s42, 0x100
	s_addc_u32 s43, s43, 0
	s_cmp_gt_u32 s80, 13
	s_cbranch_scc0 .LBB0_211
	s_and_b64 vcc, exec, s[22:23]
	s_cbranch_vccz .LBB0_214
	s_barrier

.LBB0_288:
	s_ashr_i32 s41, s40, 31
	s_lshl_b64 s[4:5], s[40:41], 19
	s_add_u32 s42, s6, s4
	s_addc_u32 s43, s7, s5
	s_and_b64 s[4:5], s[22:23], exec
	s_cselect_b32 s41, s43, s37
	s_cselect_b32 s61, s42, s36
	s_ashr_i32 s39, s38, 31
	s_lshl_b64 s[4:5], s[38:39], 19
	s_add_u32 s44, s8, s4
	s_addc_u32 s45, s9, s5
	s_and_b64 s[4:5], s[22:23], exec
	s_cselect_b32 s39, s45, s49
	s_cselect_b32 s62, s44, s48
	s_add_u32 s63, s61, 0x80
	s_addc_u32 s64, s41, 0
	s_add_u32 s4, s36, 0x40080
	s_addc_u32 s5, s37, 0
	s_add_u32 s65, s48, 0x100
	v_lshl_add_u64 v[142:143], s[4:5], 0, v[138:139]
	v_lshl_add_u64 v[144:145], s[4:5], 0, v[140:141]
	s_addc_u32 s68, s49, 0
	s_mov_b32 s69, -2
	s_mov_b64 s[48:49], 0
	s_add_u32 s4, s36, s48
	s_addc_u32 s5, s37, s49
	s_add_u32 s70, s4, 0x100
	s_addc_u32 s71, s5, 0
	s_add_u32 s50, s65, s48
	s_addc_u32 s51, s68, s49
	s_add_u32 s4, s4, 0x180
	s_addc_u32 s5, s5, 0
	s_add_i32 s72, 0, 0x10000
	s_add_i32 s73, 0, 0x14000
	v_add_u32_e32 v160, s72, v146
	s_waitcnt vmcnt(0)
	v_add_u32_e32 v176, s73, v146
	ds_read_b128 v[148:151], v160
	ds_read_b128 v[152:155], v160 offset:1024
	ds_read_b128 v[156:159], v160 offset:2048
	ds_read_b128 v[160:163], v160 offset:3072
	ds_read_b128 v[164:167], v176
	ds_read_b128 v[168:171], v176 offset:1024
	ds_read_b128 v[172:175], v176 offset:2048
	ds_read_b128 v[176:179], v176 offset:3072
	s_cmpk_eq_i32 s48, 0x700
	s_cselect_b32 s13, s64, s5
	s_cselect_b32 s12, s63, s4
	s_cselect_b32 s51, s39, s51
	s_cselect_b32 s50, s62, s50
	s_cselect_b32 s5, s41, s71
	s_cselect_b32 s4, s61, s70
	v_lshl_add_u64 v[196:197], v[142:143], 0, s[48:49]
	s_add_i32 m0, s17, 0xc000
	ds_read_b128 v[180:183], v147
	ds_read_b128 v[184:187], v147 offset:1024
	ds_read_b128 v[188:191], v147 offset:2048
	ds_read_b128 v[192:195], v147 offset:3072
	ds_read_b128 v[204:207], v147 offset:4096
	ds_read_b128 v[208:211], v147 offset:5120
	ds_read_b128 v[212:215], v147 offset:6144
	ds_read_b128 v[216:219], v147 offset:7168
	global_load_lds_dwordx4 v[196:197], off
	v_lshl_add_u64 v[196:197], v[144:145], 0, s[48:49]
	s_add_i32 m0, s17, 0xe000
	s_nop 0
	global_load_lds_dwordx4 v[196:197], off
	s_waitcnt vmcnt(8)
	s_waitcnt lgkmcnt(0)
	s_barrier
	v_mfma_f32_16x16x32_bf16 v[128:131], v[148:151], v[180:183], 0
	v_mfma_f32_16x16x32_bf16 v[124:127], v[156:159], v[180:183], 0
	v_mfma_f32_16x16x32_bf16 v[120:123], v[148:151], v[188:191], 0
	v_mfma_f32_16x16x32_bf16 v[116:119], v[156:159], v[188:191], 0
	v_mfma_f32_16x16x32_bf16 v[104:107], v[148:151], v[204:207], 0
	v_mfma_f32_16x16x32_bf16 v[100:103], v[156:159], v[204:207], 0
	v_mfma_f32_16x16x32_bf16 v[88:91], v[148:151], v[212:215], 0
	v_mfma_f32_16x16x32_bf16 v[84:87], v[156:159], v[212:215], 0
	v_mfma_f32_16x16x32_bf16 v[128:131], v[152:155], v[184:187], v[128:131]
	v_mfma_f32_16x16x32_bf16 v[124:127], v[160:163], v[184:187], v[124:127]
	v_mfma_f32_16x16x32_bf16 v[120:123], v[152:155], v[192:195], v[120:123]
	v_mfma_f32_16x16x32_bf16 v[116:119], v[160:163], v[192:195], v[116:119]
	v_mfma_f32_16x16x32_bf16 v[104:107], v[152:155], v[208:211], v[104:107]
	v_mfma_f32_16x16x32_bf16 v[100:103], v[160:163], v[208:211], v[100:103]
	v_mfma_f32_16x16x32_bf16 v[88:91], v[152:155], v[216:219], v[88:91]
	v_mfma_f32_16x16x32_bf16 v[84:87], v[160:163], v[216:219], v[84:87]
	v_mfma_f32_16x16x32_bf16 v[112:115], v[164:167], v[180:183], 0
	v_mfma_f32_16x16x32_bf16 v[108:111], v[172:175], v[180:183], 0
	v_mfma_f32_16x16x32_bf16 v[96:99], v[164:167], v[188:191], 0
	v_mfma_f32_16x16x32_bf16 v[92:95], v[172:175], v[188:191], 0
	v_mfma_f32_16x16x32_bf16 v[80:83], v[164:167], v[204:207], 0
	v_mfma_f32_16x16x32_bf16 v[76:79], v[172:175], v[204:207], 0
	v_mfma_f32_16x16x32_bf16 v[72:75], v[164:167], v[212:215], 0
	v_mfma_f32_16x16x32_bf16 v[68:71], v[172:175], v[212:215], 0
	v_mfma_f32_16x16x32_bf16 v[112:115], v[168:171], v[184:187], v[112:115]
	v_mfma_f32_16x16x32_bf16 v[108:111], v[176:179], v[184:187], v[108:111]
	v_mfma_f32_16x16x32_bf16 v[96:99], v[168:171], v[192:195], v[96:99]
	v_mfma_f32_16x16x32_bf16 v[92:95], v[176:179], v[192:195], v[92:95]
	v_mfma_f32_16x16x32_bf16 v[80:83], v[168:171], v[208:211], v[80:83]
	v_mfma_f32_16x16x32_bf16 v[76:79], v[176:179], v[208:211], v[76:79]
	v_mfma_f32_16x16x32_bf16 v[72:75], v[168:171], v[216:219], v[72:75]
	v_mfma_f32_16x16x32_bf16 v[68:71], v[176:179], v[216:219], v[68:71]
	s_barrier
	s_add_i32 s70, s72, s16
	v_lshl_add_u64 v[196:197], s[50:51], 0, v[2:3]
	s_mov_b32 m0, s70
	ds_read_b128 v[180:183], v147 offset:16384
	ds_read_b128 v[184:187], v147 offset:17408
	ds_read_b128 v[188:191], v147 offset:18432
	ds_read_b128 v[192:195], v147 offset:19456
	ds_read_b128 v[204:207], v147 offset:20480
	ds_read_b128 v[208:211], v147 offset:21504
	ds_read_b128 v[212:215], v147 offset:22528
	ds_read_b128 v[216:219], v147 offset:23552
	global_load_lds_dwordx4 v[196:197], off
	s_add_i32 m0, s70, 0x2000
	s_add_u32 s70, s50, 0x40000
	v_lshl_add_u64 v[198:199], s[50:51], 0, v[136:137]
	s_addc_u32 s71, s51, 0
	s_add_i32 s72, s73, s16
	global_load_lds_dwordx4 v[198:199], off
	v_lshl_add_u64 v[220:221], s[70:71], 0, v[2:3]
	s_mov_b32 m0, s72
	s_nop 0
	global_load_lds_dwordx4 v[220:221], off
	v_lshl_add_u64 v[220:221], s[70:71], 0, v[136:137]
	s_add_i32 m0, s72, 0x2000
	s_nop 0
	global_load_lds_dwordx4 v[220:221], off
	v_lshl_add_u64 v[220:221], s[4:5], 0, v[132:133]
	s_mov_b32 m0, s17
	s_nop 0
	global_load_lds_dwordx4 v[220:221], off
	v_lshl_add_u64 v[220:221], s[4:5], 0, v[134:135]
	s_mov_b32 m0, s21
	s_nop 0
	global_load_lds_dwordx4 v[220:221], off
	s_waitcnt vmcnt(8)
	s_waitcnt lgkmcnt(0)
	s_barrier
	v_mfma_f32_16x16x32_bf16 v[64:67], v[148:151], v[180:183], 0
	v_mfma_f32_16x16x32_bf16 v[60:63], v[156:159], v[180:183], 0
	v_mfma_f32_16x16x32_bf16 v[56:59], v[148:151], v[188:191], 0
	v_mfma_f32_16x16x32_bf16 v[52:55], v[156:159], v[188:191], 0
	v_mfma_f32_16x16x32_bf16 v[40:43], v[148:151], v[204:207], 0
	v_mfma_f32_16x16x32_bf16 v[36:39], v[156:159], v[204:207], 0
	v_mfma_f32_16x16x32_bf16 v[24:27], v[148:151], v[212:215], 0
	v_mfma_f32_16x16x32_bf16 v[20:23], v[156:159], v[212:215], 0
	v_mfma_f32_16x16x32_bf16 v[64:67], v[152:155], v[184:187], v[64:67]
	v_mfma_f32_16x16x32_bf16 v[60:63], v[160:163], v[184:187], v[60:63]
	v_mfma_f32_16x16x32_bf16 v[56:59], v[152:155], v[192:195], v[56:59]
	v_mfma_f32_16x16x32_bf16 v[52:55], v[160:163], v[192:195], v[52:55]
	v_mfma_f32_16x16x32_bf16 v[40:43], v[152:155], v[208:211], v[40:43]
	v_mfma_f32_16x16x32_bf16 v[36:39], v[160:163], v[208:211], v[36:39]
	v_mfma_f32_16x16x32_bf16 v[24:27], v[152:155], v[216:219], v[24:27]
	v_mfma_f32_16x16x32_bf16 v[20:23], v[160:163], v[216:219], v[20:23]
	v_mfma_f32_16x16x32_bf16 v[48:51], v[164:167], v[180:183], 0
	v_mfma_f32_16x16x32_bf16 v[44:47], v[172:175], v[180:183], 0
	v_mfma_f32_16x16x32_bf16 v[32:35], v[164:167], v[188:191], 0
	v_mfma_f32_16x16x32_bf16 v[28:31], v[172:175], v[188:191], 0
	v_mfma_f32_16x16x32_bf16 v[16:19], v[164:167], v[204:207], 0
	v_mfma_f32_16x16x32_bf16 v[12:15], v[172:175], v[204:207], 0
	v_mfma_f32_16x16x32_bf16 v[8:11], v[164:167], v[212:215], 0
	v_mfma_f32_16x16x32_bf16 v[4:7], v[172:175], v[212:215], 0
	v_mfma_f32_16x16x32_bf16 v[48:51], v[168:171], v[184:187], v[48:51]
	v_mfma_f32_16x16x32_bf16 v[44:47], v[176:179], v[184:187], v[44:47]
	v_mfma_f32_16x16x32_bf16 v[32:35], v[168:171], v[192:195], v[32:35]
	v_mfma_f32_16x16x32_bf16 v[28:31], v[176:179], v[192:195], v[28:31]
	v_mfma_f32_16x16x32_bf16 v[16:19], v[168:171], v[208:211], v[16:19]
	v_mfma_f32_16x16x32_bf16 v[12:15], v[176:179], v[208:211], v[12:15]
	v_mfma_f32_16x16x32_bf16 v[8:11], v[168:171], v[216:219], v[8:11]
	v_mfma_f32_16x16x32_bf16 v[4:7], v[176:179], v[216:219], v[4:7]
	s_barrier
	s_add_i32 s70, 0, 0x18000
	s_add_i32 s71, 0, 0x1c000
	v_add_u32_e32 v160, s70, v146
	v_add_u32_e32 v176, s71, v146
	ds_read_b128 v[148:151], v160
	ds_read_b128 v[152:155], v160 offset:1024
	ds_read_b128 v[156:159], v160 offset:2048
	ds_read_b128 v[160:163], v160 offset:3072
	ds_read_b128 v[164:167], v176
	ds_read_b128 v[168:171], v176 offset:1024
	ds_read_b128 v[172:175], v176 offset:2048
	ds_read_b128 v[176:179], v176 offset:3072
	s_add_u32 s4, s4, 0x40000
	s_addc_u32 s5, s5, 0
	s_mov_b32 m0, s46
	v_lshl_add_u64 v[220:221], s[4:5], 0, v[132:133]
	ds_read_b128 v[180:183], v147 offset:32768
	ds_read_b128 v[184:187], v147 offset:33792
	ds_read_b128 v[188:191], v147 offset:34816
	ds_read_b128 v[192:195], v147 offset:35840
	ds_read_b128 v[204:207], v147 offset:36864
	ds_read_b128 v[208:211], v147 offset:37888
	ds_read_b128 v[212:215], v147 offset:38912
	ds_read_b128 v[216:219], v147 offset:39936
	global_load_lds_dwordx4 v[220:221], off
	v_lshl_add_u64 v[220:221], s[4:5], 0, v[134:135]
	s_mov_b32 m0, s47
	s_nop 0
	global_load_lds_dwordx4 v[220:221], off
	s_waitcnt vmcnt(8)
	s_waitcnt lgkmcnt(0)
	s_barrier
	v_mfma_f32_16x16x32_bf16 v[128:131], v[148:151], v[180:183], v[128:131]
	v_mfma_f32_16x16x32_bf16 v[124:127], v[156:159], v[180:183], v[124:127]
	v_mfma_f32_16x16x32_bf16 v[120:123], v[148:151], v[188:191], v[120:123]
	v_mfma_f32_16x16x32_bf16 v[116:119], v[156:159], v[188:191], v[116:119]
	v_mfma_f32_16x16x32_bf16 v[104:107], v[148:151], v[204:207], v[104:107]
	v_mfma_f32_16x16x32_bf16 v[100:103], v[156:159], v[204:207], v[100:103]
	v_mfma_f32_16x16x32_bf16 v[88:91], v[148:151], v[212:215], v[88:91]
	v_mfma_f32_16x16x32_bf16 v[84:87], v[156:159], v[212:215], v[84:87]
	v_mfma_f32_16x16x32_bf16 v[128:131], v[152:155], v[184:187], v[128:131]
	v_mfma_f32_16x16x32_bf16 v[124:127], v[160:163], v[184:187], v[124:127]
	v_mfma_f32_16x16x32_bf16 v[120:123], v[152:155], v[192:195], v[120:123]
	v_mfma_f32_16x16x32_bf16 v[116:119], v[160:163], v[192:195], v[116:119]
	v_mfma_f32_16x16x32_bf16 v[104:107], v[152:155], v[208:211], v[104:107]
	v_mfma_f32_16x16x32_bf16 v[100:103], v[160:163], v[208:211], v[100:103]
	v_mfma_f32_16x16x32_bf16 v[88:91], v[152:155], v[216:219], v[88:91]
	v_mfma_f32_16x16x32_bf16 v[84:87], v[160:163], v[216:219], v[84:87]
	v_mfma_f32_16x16x32_bf16 v[112:115], v[164:167], v[180:183], v[112:115]
	v_mfma_f32_16x16x32_bf16 v[108:111], v[172:175], v[180:183], v[108:111]
	v_mfma_f32_16x16x32_bf16 v[96:99], v[164:167], v[188:191], v[96:99]
	v_mfma_f32_16x16x32_bf16 v[92:95], v[172:175], v[188:191], v[92:95]
	v_mfma_f32_16x16x32_bf16 v[80:83], v[164:167], v[204:207], v[80:83]
	v_mfma_f32_16x16x32_bf16 v[76:79], v[172:175], v[204:207], v[76:79]
	v_mfma_f32_16x16x32_bf16 v[72:75], v[164:167], v[212:215], v[72:75]
	v_mfma_f32_16x16x32_bf16 v[68:71], v[172:175], v[212:215], v[68:71]
	v_mfma_f32_16x16x32_bf16 v[112:115], v[168:171], v[184:187], v[112:115]
	v_mfma_f32_16x16x32_bf16 v[108:111], v[176:179], v[184:187], v[108:111]
	v_mfma_f32_16x16x32_bf16 v[96:99], v[168:171], v[192:195], v[96:99]
	v_mfma_f32_16x16x32_bf16 v[92:95], v[176:179], v[192:195], v[92:95]
	v_mfma_f32_16x16x32_bf16 v[80:83], v[168:171], v[208:211], v[80:83]
	v_mfma_f32_16x16x32_bf16 v[76:79], v[176:179], v[208:211], v[76:79]
	v_mfma_f32_16x16x32_bf16 v[72:75], v[168:171], v[216:219], v[72:75]
	v_mfma_f32_16x16x32_bf16 v[68:71], v[176:179], v[216:219], v[68:71]
	s_barrier
	s_add_i32 s4, s70, s16
	v_lshl_add_u64 v[196:197], v[196:197], 0, s[34:35]
	s_mov_b32 m0, s4
	ds_read_b128 v[180:183], v147 offset:49152
	ds_read_b128 v[184:187], v147 offset:50176
	ds_read_b128 v[188:191], v147 offset:51200
	ds_read_b128 v[192:195], v147 offset:52224
	ds_read_b128 v[204:207], v147 offset:53248
	ds_read_b128 v[208:211], v147 offset:54272
	ds_read_b128 v[212:215], v147 offset:55296
	ds_read_b128 v[216:219], v147 offset:56320
	global_load_lds_dwordx4 v[196:197], off
	s_add_i32 m0, s4, 0x2000
	s_add_u32 s4, s50, 0x40080
	v_lshl_add_u64 v[196:197], v[198:199], 0, s[34:35]
	s_addc_u32 s5, s51, 0
	s_add_i32 s50, s71, s16
	global_load_lds_dwordx4 v[196:197], off
	v_lshl_add_u64 v[196:197], s[4:5], 0, v[2:3]
	s_mov_b32 m0, s50
	s_nop 0
	global_load_lds_dwordx4 v[196:197], off
	v_lshl_add_u64 v[196:197], s[4:5], 0, v[136:137]
	s_add_i32 m0, s50, 0x2000
	s_nop 0
	global_load_lds_dwordx4 v[196:197], off
	v_lshl_add_u64 v[196:197], s[12:13], 0, v[132:133]
	s_mov_b32 m0, s56
	s_nop 0
	global_load_lds_dwordx4 v[196:197], off
	v_lshl_add_u64 v[196:197], s[12:13], 0, v[134:135]
	s_mov_b32 m0, s58
	s_nop 0
	global_load_lds_dwordx4 v[196:197], off
	s_waitcnt vmcnt(8)
	s_waitcnt lgkmcnt(0)
	s_barrier
	v_mfma_f32_16x16x32_bf16 v[64:67], v[148:151], v[180:183], v[64:67]
	v_mfma_f32_16x16x32_bf16 v[60:63], v[156:159], v[180:183], v[60:63]
	v_mfma_f32_16x16x32_bf16 v[56:59], v[148:151], v[188:191], v[56:59]
	v_mfma_f32_16x16x32_bf16 v[52:55], v[156:159], v[188:191], v[52:55]
	v_mfma_f32_16x16x32_bf16 v[40:43], v[148:151], v[204:207], v[40:43]
	v_mfma_f32_16x16x32_bf16 v[36:39], v[156:159], v[204:207], v[36:39]
	v_mfma_f32_16x16x32_bf16 v[24:27], v[148:151], v[212:215], v[24:27]
	v_mfma_f32_16x16x32_bf16 v[20:23], v[156:159], v[212:215], v[20:23]
	v_mfma_f32_16x16x32_bf16 v[64:67], v[152:155], v[184:187], v[64:67]
	v_mfma_f32_16x16x32_bf16 v[60:63], v[160:163], v[184:187], v[60:63]
	v_mfma_f32_16x16x32_bf16 v[56:59], v[152:155], v[192:195], v[56:59]
	v_mfma_f32_16x16x32_bf16 v[52:55], v[160:163], v[192:195], v[52:55]
	v_mfma_f32_16x16x32_bf16 v[40:43], v[152:155], v[208:211], v[40:43]
	v_mfma_f32_16x16x32_bf16 v[36:39], v[160:163], v[208:211], v[36:39]
	v_mfma_f32_16x16x32_bf16 v[24:27], v[152:155], v[216:219], v[24:27]
	v_mfma_f32_16x16x32_bf16 v[20:23], v[160:163], v[216:219], v[20:23]
	v_mfma_f32_16x16x32_bf16 v[48:51], v[164:167], v[180:183], v[48:51]
	v_mfma_f32_16x16x32_bf16 v[44:47], v[172:175], v[180:183], v[44:47]
	v_mfma_f32_16x16x32_bf16 v[32:35], v[164:167], v[188:191], v[32:35]
	v_mfma_f32_16x16x32_bf16 v[28:31], v[172:175], v[188:191], v[28:31]
	v_mfma_f32_16x16x32_bf16 v[16:19], v[164:167], v[204:207], v[16:19]
	v_mfma_f32_16x16x32_bf16 v[12:15], v[172:175], v[204:207], v[12:15]
	v_mfma_f32_16x16x32_bf16 v[8:11], v[164:167], v[212:215], v[8:11]
	v_mfma_f32_16x16x32_bf16 v[4:7], v[172:175], v[212:215], v[4:7]
	v_mfma_f32_16x16x32_bf16 v[48:51], v[168:171], v[184:187], v[48:51]
	v_mfma_f32_16x16x32_bf16 v[44:47], v[176:179], v[184:187], v[44:47]
	v_mfma_f32_16x16x32_bf16 v[32:35], v[168:171], v[192:195], v[32:35]
	v_mfma_f32_16x16x32_bf16 v[28:31], v[176:179], v[192:195], v[28:31]
	v_mfma_f32_16x16x32_bf16 v[16:19], v[168:171], v[208:211], v[16:19]
	v_mfma_f32_16x16x32_bf16 v[12:15], v[176:179], v[208:211], v[12:15]
	v_mfma_f32_16x16x32_bf16 v[8:11], v[168:171], v[216:219], v[8:11]
	v_mfma_f32_16x16x32_bf16 v[4:7], v[176:179], v[216:219], v[4:7]
	s_barrier
	s_add_i32 s69, s69, 2
	s_add_u32 s48, s48, 0x100
	s_addc_u32 s49, s49, 0
	s_cmp_gt_u32 s69, 13
.LBB0_289:
	s_add_u32 s4, s36, s48
	s_addc_u32 s5, s37, s49
	s_add_u32 s70, s4, 0x100
	s_addc_u32 s71, s5, 0
	s_add_u32 s50, s65, s48
	s_addc_u32 s51, s68, s49
	s_add_u32 s4, s4, 0x180
	s_addc_u32 s5, s5, 0
	s_add_i32 s72, 0, 0x10000
	s_add_i32 s73, 0, 0x14000
	v_add_u32_e32 v160, s72, v146
	s_waitcnt vmcnt(0)
	v_add_u32_e32 v176, s73, v146
	ds_read_b128 v[148:151], v160
	ds_read_b128 v[152:155], v160 offset:1024
	ds_read_b128 v[156:159], v160 offset:2048
	ds_read_b128 v[160:163], v160 offset:3072
	ds_read_b128 v[164:167], v176
	ds_read_b128 v[168:171], v176 offset:1024
	ds_read_b128 v[172:175], v176 offset:2048
	ds_read_b128 v[176:179], v176 offset:3072
	s_cmpk_eq_i32 s48, 0x700
	s_cselect_b32 s13, s64, s5
	s_cselect_b32 s12, s63, s4
	s_cselect_b32 s51, s39, s51
	s_cselect_b32 s50, s62, s50
	s_cselect_b32 s5, s41, s71
	s_cselect_b32 s4, s61, s70
	v_lshl_add_u64 v[196:197], v[142:143], 0, s[48:49]
	s_add_i32 m0, s17, 0xc000
	ds_read_b128 v[180:183], v147
	ds_read_b128 v[184:187], v147 offset:1024
	ds_read_b128 v[188:191], v147 offset:2048
	ds_read_b128 v[192:195], v147 offset:3072
	ds_read_b128 v[204:207], v147 offset:4096
	ds_read_b128 v[208:211], v147 offset:5120
	ds_read_b128 v[212:215], v147 offset:6144
	ds_read_b128 v[216:219], v147 offset:7168
	global_load_lds_dwordx4 v[196:197], off
	v_lshl_add_u64 v[196:197], v[144:145], 0, s[48:49]
	s_add_i32 m0, s17, 0xe000
	s_nop 0
	global_load_lds_dwordx4 v[196:197], off
	s_waitcnt vmcnt(8)
	s_waitcnt lgkmcnt(0)
	s_barrier
	v_mfma_f32_16x16x32_bf16 v[128:131], v[148:151], v[180:183], v[128:131]
	v_mfma_f32_16x16x32_bf16 v[124:127], v[156:159], v[180:183], v[124:127]
	v_mfma_f32_16x16x32_bf16 v[120:123], v[148:151], v[188:191], v[120:123]
	v_mfma_f32_16x16x32_bf16 v[116:119], v[156:159], v[188:191], v[116:119]
	v_mfma_f32_16x16x32_bf16 v[104:107], v[148:151], v[204:207], v[104:107]
	v_mfma_f32_16x16x32_bf16 v[100:103], v[156:159], v[204:207], v[100:103]
	v_mfma_f32_16x16x32_bf16 v[88:91], v[148:151], v[212:215], v[88:91]
	v_mfma_f32_16x16x32_bf16 v[84:87], v[156:159], v[212:215], v[84:87]
	v_mfma_f32_16x16x32_bf16 v[128:131], v[152:155], v[184:187], v[128:131]
	v_mfma_f32_16x16x32_bf16 v[124:127], v[160:163], v[184:187], v[124:127]
	v_mfma_f32_16x16x32_bf16 v[120:123], v[152:155], v[192:195], v[120:123]
	v_mfma_f32_16x16x32_bf16 v[116:119], v[160:163], v[192:195], v[116:119]
	v_mfma_f32_16x16x32_bf16 v[104:107], v[152:155], v[208:211], v[104:107]
	v_mfma_f32_16x16x32_bf16 v[100:103], v[160:163], v[208:211], v[100:103]
	v_mfma_f32_16x16x32_bf16 v[88:91], v[152:155], v[216:219], v[88:91]
	v_mfma_f32_16x16x32_bf16 v[84:87], v[160:163], v[216:219], v[84:87]
	v_mfma_f32_16x16x32_bf16 v[112:115], v[164:167], v[180:183], v[112:115]
	v_mfma_f32_16x16x32_bf16 v[108:111], v[172:175], v[180:183], v[108:111]
	v_mfma_f32_16x16x32_bf16 v[96:99], v[164:167], v[188:191], v[96:99]
	v_mfma_f32_16x16x32_bf16 v[92:95], v[172:175], v[188:191], v[92:95]
	v_mfma_f32_16x16x32_bf16 v[80:83], v[164:167], v[204:207], v[80:83]
	v_mfma_f32_16x16x32_bf16 v[76:79], v[172:175], v[204:207], v[76:79]
	v_mfma_f32_16x16x32_bf16 v[72:75], v[164:167], v[212:215], v[72:75]
	v_mfma_f32_16x16x32_bf16 v[68:71], v[172:175], v[212:215], v[68:71]
	v_mfma_f32_16x16x32_bf16 v[112:115], v[168:171], v[184:187], v[112:115]
	v_mfma_f32_16x16x32_bf16 v[108:111], v[176:179], v[184:187], v[108:111]
	v_mfma_f32_16x16x32_bf16 v[96:99], v[168:171], v[192:195], v[96:99]
	v_mfma_f32_16x16x32_bf16 v[92:95], v[176:179], v[192:195], v[92:95]
	v_mfma_f32_16x16x32_bf16 v[80:83], v[168:171], v[208:211], v[80:83]
	v_mfma_f32_16x16x32_bf16 v[76:79], v[176:179], v[208:211], v[76:79]
	v_mfma_f32_16x16x32_bf16 v[72:75], v[168:171], v[216:219], v[72:75]
	v_mfma_f32_16x16x32_bf16 v[68:71], v[176:179], v[216:219], v[68:71]
	s_barrier
	s_add_i32 s70, s72, s16
	v_lshl_add_u64 v[196:197], s[50:51], 0, v[2:3]
	s_mov_b32 m0, s70
	ds_read_b128 v[180:183], v147 offset:16384
	ds_read_b128 v[184:187], v147 offset:17408
	ds_read_b128 v[188:191], v147 offset:18432
	ds_read_b128 v[192:195], v147 offset:19456
	ds_read_b128 v[204:207], v147 offset:20480
	ds_read_b128 v[208:211], v147 offset:21504
	ds_read_b128 v[212:215], v147 offset:22528
	ds_read_b128 v[216:219], v147 offset:23552
	global_load_lds_dwordx4 v[196:197], off
	s_add_i32 m0, s70, 0x2000
	s_add_u32 s70, s50, 0x40000
	v_lshl_add_u64 v[198:199], s[50:51], 0, v[136:137]
	s_addc_u32 s71, s51, 0
	s_add_i32 s72, s73, s16
	global_load_lds_dwordx4 v[198:199], off
	v_lshl_add_u64 v[220:221], s[70:71], 0, v[2:3]
	s_mov_b32 m0, s72
	s_nop 0
	global_load_lds_dwordx4 v[220:221], off
	v_lshl_add_u64 v[220:221], s[70:71], 0, v[136:137]
	s_add_i32 m0, s72, 0x2000
	s_nop 0
	global_load_lds_dwordx4 v[220:221], off
	v_lshl_add_u64 v[220:221], s[4:5], 0, v[132:133]
	s_mov_b32 m0, s17
	s_nop 0
	global_load_lds_dwordx4 v[220:221], off
	v_lshl_add_u64 v[220:221], s[4:5], 0, v[134:135]
	s_mov_b32 m0, s21
	s_nop 0
	global_load_lds_dwordx4 v[220:221], off
	s_waitcnt vmcnt(8)
	s_waitcnt lgkmcnt(0)
	s_barrier
	v_mfma_f32_16x16x32_bf16 v[64:67], v[148:151], v[180:183], v[64:67]
	v_mfma_f32_16x16x32_bf16 v[60:63], v[156:159], v[180:183], v[60:63]
	v_mfma_f32_16x16x32_bf16 v[56:59], v[148:151], v[188:191], v[56:59]
	v_mfma_f32_16x16x32_bf16 v[52:55], v[156:159], v[188:191], v[52:55]
	v_mfma_f32_16x16x32_bf16 v[40:43], v[148:151], v[204:207], v[40:43]
	v_mfma_f32_16x16x32_bf16 v[36:39], v[156:159], v[204:207], v[36:39]
	v_mfma_f32_16x16x32_bf16 v[24:27], v[148:151], v[212:215], v[24:27]
	v_mfma_f32_16x16x32_bf16 v[20:23], v[156:159], v[212:215], v[20:23]
	v_mfma_f32_16x16x32_bf16 v[64:67], v[152:155], v[184:187], v[64:67]
	v_mfma_f32_16x16x32_bf16 v[60:63], v[160:163], v[184:187], v[60:63]
	v_mfma_f32_16x16x32_bf16 v[56:59], v[152:155], v[192:195], v[56:59]
	v_mfma_f32_16x16x32_bf16 v[52:55], v[160:163], v[192:195], v[52:55]
	v_mfma_f32_16x16x32_bf16 v[40:43], v[152:155], v[208:211], v[40:43]
	v_mfma_f32_16x16x32_bf16 v[36:39], v[160:163], v[208:211], v[36:39]
	v_mfma_f32_16x16x32_bf16 v[24:27], v[152:155], v[216:219], v[24:27]
	v_mfma_f32_16x16x32_bf16 v[20:23], v[160:163], v[216:219], v[20:23]
	v_mfma_f32_16x16x32_bf16 v[48:51], v[164:167], v[180:183], v[48:51]
	v_mfma_f32_16x16x32_bf16 v[44:47], v[172:175], v[180:183], v[44:47]
	v_mfma_f32_16x16x32_bf16 v[32:35], v[164:167], v[188:191], v[32:35]
	v_mfma_f32_16x16x32_bf16 v[28:31], v[172:175], v[188:191], v[28:31]
	v_mfma_f32_16x16x32_bf16 v[16:19], v[164:167], v[204:207], v[16:19]
	v_mfma_f32_16x16x32_bf16 v[12:15], v[172:175], v[204:207], v[12:15]
	v_mfma_f32_16x16x32_bf16 v[8:11], v[164:167], v[212:215], v[8:11]
	v_mfma_f32_16x16x32_bf16 v[4:7], v[172:175], v[212:215], v[4:7]
	v_mfma_f32_16x16x32_bf16 v[48:51], v[168:171], v[184:187], v[48:51]
	v_mfma_f32_16x16x32_bf16 v[44:47], v[176:179], v[184:187], v[44:47]
	v_mfma_f32_16x16x32_bf16 v[32:35], v[168:171], v[192:195], v[32:35]
	v_mfma_f32_16x16x32_bf16 v[28:31], v[176:179], v[192:195], v[28:31]
	v_mfma_f32_16x16x32_bf16 v[16:19], v[168:171], v[208:211], v[16:19]
	v_mfma_f32_16x16x32_bf16 v[12:15], v[176:179], v[208:211], v[12:15]
	v_mfma_f32_16x16x32_bf16 v[8:11], v[168:171], v[216:219], v[8:11]
	v_mfma_f32_16x16x32_bf16 v[4:7], v[176:179], v[216:219], v[4:7]
	s_barrier
	s_add_i32 s70, 0, 0x18000
	s_add_i32 s71, 0, 0x1c000
	v_add_u32_e32 v160, s70, v146
	v_add_u32_e32 v176, s71, v146
	ds_read_b128 v[148:151], v160
	ds_read_b128 v[152:155], v160 offset:1024
	ds_read_b128 v[156:159], v160 offset:2048
	ds_read_b128 v[160:163], v160 offset:3072
	ds_read_b128 v[164:167], v176
	ds_read_b128 v[168:171], v176 offset:1024
	ds_read_b128 v[172:175], v176 offset:2048
	ds_read_b128 v[176:179], v176 offset:3072
	s_add_u32 s4, s4, 0x40000
	s_addc_u32 s5, s5, 0
	s_mov_b32 m0, s46
	v_lshl_add_u64 v[220:221], s[4:5], 0, v[132:133]
	ds_read_b128 v[180:183], v147 offset:32768
	ds_read_b128 v[184:187], v147 offset:33792
	ds_read_b128 v[188:191], v147 offset:34816
	ds_read_b128 v[192:195], v147 offset:35840
	ds_read_b128 v[204:207], v147 offset:36864
	ds_read_b128 v[208:211], v147 offset:37888
	ds_read_b128 v[212:215], v147 offset:38912
	ds_read_b128 v[216:219], v147 offset:39936
	global_load_lds_dwordx4 v[220:221], off
	v_lshl_add_u64 v[220:221], s[4:5], 0, v[134:135]
	s_mov_b32 m0, s47
	s_nop 0
	global_load_lds_dwordx4 v[220:221], off
	s_waitcnt vmcnt(8)
	s_waitcnt lgkmcnt(0)
	s_barrier
	v_mfma_f32_16x16x32_bf16 v[128:131], v[148:151], v[180:183], v[128:131]
	v_mfma_f32_16x16x32_bf16 v[124:127], v[156:159], v[180:183], v[124:127]
	v_mfma_f32_16x16x32_bf16 v[120:123], v[148:151], v[188:191], v[120:123]
	v_mfma_f32_16x16x32_bf16 v[116:119], v[156:159], v[188:191], v[116:119]
	v_mfma_f32_16x16x32_bf16 v[104:107], v[148:151], v[204:207], v[104:107]
	v_mfma_f32_16x16x32_bf16 v[100:103], v[156:159], v[204:207], v[100:103]
	v_mfma_f32_16x16x32_bf16 v[88:91], v[148:151], v[212:215], v[88:91]
	v_mfma_f32_16x16x32_bf16 v[84:87], v[156:159], v[212:215], v[84:87]
	v_mfma_f32_16x16x32_bf16 v[128:131], v[152:155], v[184:187], v[128:131]
	v_mfma_f32_16x16x32_bf16 v[124:127], v[160:163], v[184:187], v[124:127]
	v_mfma_f32_16x16x32_bf16 v[120:123], v[152:155], v[192:195], v[120:123]
	v_mfma_f32_16x16x32_bf16 v[116:119], v[160:163], v[192:195], v[116:119]
	v_mfma_f32_16x16x32_bf16 v[104:107], v[152:155], v[208:211], v[104:107]
	v_mfma_f32_16x16x32_bf16 v[100:103], v[160:163], v[208:211], v[100:103]
	v_mfma_f32_16x16x32_bf16 v[88:91], v[152:155], v[216:219], v[88:91]
	v_mfma_f32_16x16x32_bf16 v[84:87], v[160:163], v[216:219], v[84:87]
	v_mfma_f32_16x16x32_bf16 v[112:115], v[164:167], v[180:183], v[112:115]
	v_mfma_f32_16x16x32_bf16 v[108:111], v[172:175], v[180:183], v[108:111]
	v_mfma_f32_16x16x32_bf16 v[96:99], v[164:167], v[188:191], v[96:99]
	v_mfma_f32_16x16x32_bf16 v[92:95], v[172:175], v[188:191], v[92:95]
	v_mfma_f32_16x16x32_bf16 v[80:83], v[164:167], v[204:207], v[80:83]
	v_mfma_f32_16x16x32_bf16 v[76:79], v[172:175], v[204:207], v[76:79]
	v_mfma_f32_16x16x32_bf16 v[72:75], v[164:167], v[212:215], v[72:75]
	v_mfma_f32_16x16x32_bf16 v[68:71], v[172:175], v[212:215], v[68:71]
	v_mfma_f32_16x16x32_bf16 v[112:115], v[168:171], v[184:187], v[112:115]
	v_mfma_f32_16x16x32_bf16 v[108:111], v[176:179], v[184:187], v[108:111]
	v_mfma_f32_16x16x32_bf16 v[96:99], v[168:171], v[192:195], v[96:99]
	v_mfma_f32_16x16x32_bf16 v[92:95], v[176:179], v[192:195], v[92:95]
	v_mfma_f32_16x16x32_bf16 v[80:83], v[168:171], v[208:211], v[80:83]
	v_mfma_f32_16x16x32_bf16 v[76:79], v[176:179], v[208:211], v[76:79]
	v_mfma_f32_16x16x32_bf16 v[72:75], v[168:171], v[216:219], v[72:75]
	v_mfma_f32_16x16x32_bf16 v[68:71], v[176:179], v[216:219], v[68:71]
	s_barrier
	s_add_i32 s4, s70, s16
	v_lshl_add_u64 v[196:197], v[196:197], 0, s[34:35]
	s_mov_b32 m0, s4
	ds_read_b128 v[180:183], v147 offset:49152
	ds_read_b128 v[184:187], v147 offset:50176
	ds_read_b128 v[188:191], v147 offset:51200
	ds_read_b128 v[192:195], v147 offset:52224
	ds_read_b128 v[204:207], v147 offset:53248
	ds_read_b128 v[208:211], v147 offset:54272
	ds_read_b128 v[212:215], v147 offset:55296
	ds_read_b128 v[216:219], v147 offset:56320
	global_load_lds_dwordx4 v[196:197], off
	s_add_i32 m0, s4, 0x2000
	s_add_u32 s4, s50, 0x40080
	v_lshl_add_u64 v[196:197], v[198:199], 0, s[34:35]
	s_addc_u32 s5, s51, 0
	s_add_i32 s50, s71, s16
	global_load_lds_dwordx4 v[196:197], off
	v_lshl_add_u64 v[196:197], s[4:5], 0, v[2:3]
	s_mov_b32 m0, s50
	s_nop 0
	global_load_lds_dwordx4 v[196:197], off
	v_lshl_add_u64 v[196:197], s[4:5], 0, v[136:137]
	s_add_i32 m0, s50, 0x2000
	s_nop 0
	global_load_lds_dwordx4 v[196:197], off
	v_lshl_add_u64 v[196:197], s[12:13], 0, v[132:133]
	s_mov_b32 m0, s56
	s_nop 0
	global_load_lds_dwordx4 v[196:197], off
	v_lshl_add_u64 v[196:197], s[12:13], 0, v[134:135]
	s_mov_b32 m0, s58
	s_nop 0
	global_load_lds_dwordx4 v[196:197], off
	s_waitcnt vmcnt(8)
	s_waitcnt lgkmcnt(0)
	s_barrier
	v_mfma_f32_16x16x32_bf16 v[64:67], v[148:151], v[180:183], v[64:67]
	v_mfma_f32_16x16x32_bf16 v[60:63], v[156:159], v[180:183], v[60:63]
	v_mfma_f32_16x16x32_bf16 v[56:59], v[148:151], v[188:191], v[56:59]
	v_mfma_f32_16x16x32_bf16 v[52:55], v[156:159], v[188:191], v[52:55]
	v_mfma_f32_16x16x32_bf16 v[40:43], v[148:151], v[204:207], v[40:43]
	v_mfma_f32_16x16x32_bf16 v[36:39], v[156:159], v[204:207], v[36:39]
	v_mfma_f32_16x16x32_bf16 v[24:27], v[148:151], v[212:215], v[24:27]
	v_mfma_f32_16x16x32_bf16 v[20:23], v[156:159], v[212:215], v[20:23]
	v_mfma_f32_16x16x32_bf16 v[64:67], v[152:155], v[184:187], v[64:67]
	v_mfma_f32_16x16x32_bf16 v[60:63], v[160:163], v[184:187], v[60:63]
	v_mfma_f32_16x16x32_bf16 v[56:59], v[152:155], v[192:195], v[56:59]
	v_mfma_f32_16x16x32_bf16 v[52:55], v[160:163], v[192:195], v[52:55]
	v_mfma_f32_16x16x32_bf16 v[40:43], v[152:155], v[208:211], v[40:43]
	v_mfma_f32_16x16x32_bf16 v[36:39], v[160:163], v[208:211], v[36:39]
	v_mfma_f32_16x16x32_bf16 v[24:27], v[152:155], v[216:219], v[24:27]
	v_mfma_f32_16x16x32_bf16 v[20:23], v[160:163], v[216:219], v[20:23]
	v_mfma_f32_16x16x32_bf16 v[48:51], v[164:167], v[180:183], v[48:51]
	v_mfma_f32_16x16x32_bf16 v[44:47], v[172:175], v[180:183], v[44:47]
	v_mfma_f32_16x16x32_bf16 v[32:35], v[164:167], v[188:191], v[32:35]
	v_mfma_f32_16x16x32_bf16 v[28:31], v[172:175], v[188:191], v[28:31]
	v_mfma_f32_16x16x32_bf16 v[16:19], v[164:167], v[204:207], v[16:19]
	v_mfma_f32_16x16x32_bf16 v[12:15], v[172:175], v[204:207], v[12:15]
	v_mfma_f32_16x16x32_bf16 v[8:11], v[164:167], v[212:215], v[8:11]
	v_mfma_f32_16x16x32_bf16 v[4:7], v[172:175], v[212:215], v[4:7]
	v_mfma_f32_16x16x32_bf16 v[48:51], v[168:171], v[184:187], v[48:51]
	v_mfma_f32_16x16x32_bf16 v[44:47], v[176:179], v[184:187], v[44:47]
	v_mfma_f32_16x16x32_bf16 v[32:35], v[168:171], v[192:195], v[32:35]
	v_mfma_f32_16x16x32_bf16 v[28:31], v[176:179], v[192:195], v[28:31]
	v_mfma_f32_16x16x32_bf16 v[16:19], v[168:171], v[208:211], v[16:19]
	v_mfma_f32_16x16x32_bf16 v[12:15], v[176:179], v[208:211], v[12:15]
	v_mfma_f32_16x16x32_bf16 v[8:11], v[168:171], v[216:219], v[8:11]
	v_mfma_f32_16x16x32_bf16 v[4:7], v[176:179], v[216:219], v[4:7]
	s_barrier
	s_add_i32 s69, s69, 2
	s_add_u32 s48, s48, 0x100
	s_addc_u32 s49, s49, 0
	s_cmp_gt_u32 s69, 13
	s_cbranch_scc0 .LBB0_289
	s_and_b64 vcc, exec, s[18:19]
	s_mov_b32 s62, 0x18000
	s_mov_b32 s63, 0x1a000
	s_cbranch_vccz .LBB0_292
	s_barrier

.LBB0_310:
	s_ashr_i32 s41, s40, 31
	s_lshl_b64 s[4:5], s[40:41], 19
	s_add_u32 s42, s6, s4
	s_addc_u32 s43, s7, s5
	s_and_b64 s[4:5], s[22:23], exec
	s_cselect_b32 s41, s43, s39
	s_cselect_b32 s60, s42, s38
	s_ashr_i32 s37, s36, 31
	s_lshl_b64 s[4:5], s[36:37], 19
	s_add_u32 s44, s8, s4
	s_addc_u32 s45, s9, s5
	s_and_b64 s[4:5], s[22:23], exec
	s_cselect_b32 s37, s45, s49
	s_cselect_b32 s61, s44, s48
	s_add_u32 s62, s60, 0x80
	s_addc_u32 s63, s41, 0
	s_add_u32 s4, s38, 0x40080
	s_addc_u32 s5, s39, 0
	s_add_u32 s64, s48, 0x100
	v_lshl_add_u64 v[144:145], s[4:5], 0, v[140:141]
	v_lshl_add_u64 v[146:147], s[4:5], 0, v[142:143]
	s_addc_u32 s65, s49, 0
	s_mov_b32 s68, -2
	s_mov_b64 s[48:49], 0
	s_add_u32 s4, s38, s48
	s_addc_u32 s5, s39, s49
	s_add_u32 s69, s4, 0x100
	s_addc_u32 s70, s5, 0
	s_add_u32 s50, s64, s48
	s_addc_u32 s51, s65, s49
	s_add_u32 s4, s4, 0x180
	s_addc_u32 s5, s5, 0
	s_add_i32 s71, 0, 0x10000
	s_add_i32 s72, 0, 0x14000
	v_add_u32_e32 v2, s71, v149
	ds_read_b128 v[152:155], v2
	s_waitcnt vmcnt(0)
	ds_read_b128 v[156:159], v2 offset:1024
	ds_read_b128 v[160:163], v2 offset:2048
	ds_read_b128 v[164:167], v2 offset:3072
	v_add_u32_e32 v2, s72, v149
	ds_read_b128 v[168:171], v2
	ds_read_b128 v[172:175], v2 offset:1024
	ds_read_b128 v[176:179], v2 offset:2048
	ds_read_b128 v[180:183], v2 offset:3072
	s_cmpk_eq_i32 s48, 0x700
	s_cselect_b32 s13, s63, s5
	s_cselect_b32 s12, s62, s4
	s_cselect_b32 s51, s37, s51
	s_cselect_b32 s50, s61, s50
	s_cselect_b32 s5, s41, s70
	s_cselect_b32 s4, s60, s69
	v_lshl_add_u64 v[196:197], v[144:145], 0, s[48:49]
	s_add_i32 m0, s17, 0xc000
	ds_read_b128 v[184:187], v151
	ds_read_b128 v[188:191], v151 offset:1024
	ds_read_b128 v[192:195], v151 offset:2048
	ds_read_b128 v[204:207], v151 offset:3072
	ds_read_b128 v[208:211], v151 offset:4096
	ds_read_b128 v[212:215], v151 offset:5120
	ds_read_b128 v[216:219], v151 offset:6144
	ds_read_b128 v[220:223], v151 offset:7168
	global_load_lds_dwordx4 v[196:197], off
	v_lshl_add_u64 v[196:197], v[146:147], 0, s[48:49]
	s_add_i32 m0, s17, 0xe000
	s_nop 0
	global_load_lds_dwordx4 v[196:197], off
	s_waitcnt vmcnt(8)
	s_waitcnt lgkmcnt(0)
	s_barrier
	v_mfma_f32_16x16x32_bf16 v[128:131], v[152:155], v[184:187], 0
	v_mfma_f32_16x16x32_bf16 v[124:127], v[160:163], v[184:187], 0
	v_mfma_f32_16x16x32_bf16 v[120:123], v[152:155], v[192:195], 0
	v_mfma_f32_16x16x32_bf16 v[116:119], v[160:163], v[192:195], 0
	v_mfma_f32_16x16x32_bf16 v[104:107], v[152:155], v[208:211], 0
	v_mfma_f32_16x16x32_bf16 v[100:103], v[160:163], v[208:211], 0
	v_mfma_f32_16x16x32_bf16 v[88:91], v[152:155], v[216:219], 0
	v_mfma_f32_16x16x32_bf16 v[84:87], v[160:163], v[216:219], 0
	v_mfma_f32_16x16x32_bf16 v[128:131], v[156:159], v[188:191], v[128:131]
	v_mfma_f32_16x16x32_bf16 v[124:127], v[164:167], v[188:191], v[124:127]
	v_mfma_f32_16x16x32_bf16 v[120:123], v[156:159], v[204:207], v[120:123]
	v_mfma_f32_16x16x32_bf16 v[116:119], v[164:167], v[204:207], v[116:119]
	v_mfma_f32_16x16x32_bf16 v[104:107], v[156:159], v[212:215], v[104:107]
	v_mfma_f32_16x16x32_bf16 v[100:103], v[164:167], v[212:215], v[100:103]
	v_mfma_f32_16x16x32_bf16 v[88:91], v[156:159], v[220:223], v[88:91]
	v_mfma_f32_16x16x32_bf16 v[84:87], v[164:167], v[220:223], v[84:87]
	v_mfma_f32_16x16x32_bf16 v[112:115], v[168:171], v[184:187], 0
	v_mfma_f32_16x16x32_bf16 v[108:111], v[176:179], v[184:187], 0
	v_mfma_f32_16x16x32_bf16 v[96:99], v[168:171], v[192:195], 0
	v_mfma_f32_16x16x32_bf16 v[92:95], v[176:179], v[192:195], 0
	v_mfma_f32_16x16x32_bf16 v[80:83], v[168:171], v[208:211], 0
	v_mfma_f32_16x16x32_bf16 v[76:79], v[176:179], v[208:211], 0
	v_mfma_f32_16x16x32_bf16 v[72:75], v[168:171], v[216:219], 0
	v_mfma_f32_16x16x32_bf16 v[68:71], v[176:179], v[216:219], 0
	v_mfma_f32_16x16x32_bf16 v[112:115], v[172:175], v[188:191], v[112:115]
	v_mfma_f32_16x16x32_bf16 v[108:111], v[180:183], v[188:191], v[108:111]
	v_mfma_f32_16x16x32_bf16 v[96:99], v[172:175], v[204:207], v[96:99]
	v_mfma_f32_16x16x32_bf16 v[92:95], v[180:183], v[204:207], v[92:95]
	v_mfma_f32_16x16x32_bf16 v[80:83], v[172:175], v[212:215], v[80:83]
	v_mfma_f32_16x16x32_bf16 v[76:79], v[180:183], v[212:215], v[76:79]
	v_mfma_f32_16x16x32_bf16 v[72:75], v[172:175], v[220:223], v[72:75]
	v_mfma_f32_16x16x32_bf16 v[68:71], v[180:183], v[220:223], v[68:71]
	s_barrier
	s_add_i32 s69, s71, s16
	v_lshl_add_u64 v[196:197], s[50:51], 0, v[134:135]
	s_mov_b32 m0, s69
	ds_read_b128 v[184:187], v151 offset:16384
	ds_read_b128 v[188:191], v151 offset:17408
	ds_read_b128 v[192:195], v151 offset:18432
	ds_read_b128 v[204:207], v151 offset:19456
	ds_read_b128 v[208:211], v151 offset:20480
	ds_read_b128 v[212:215], v151 offset:21504
	ds_read_b128 v[216:219], v151 offset:22528
	ds_read_b128 v[220:223], v151 offset:23552
	global_load_lds_dwordx4 v[196:197], off
	s_add_i32 m0, s69, 0x2000
	s_add_u32 s70, s50, 0x40000
	v_lshl_add_u64 v[198:199], s[50:51], 0, v[138:139]
	s_addc_u32 s71, s51, 0
	s_add_i32 s69, s72, s16
	global_load_lds_dwordx4 v[198:199], off
	v_lshl_add_u64 v[224:225], s[70:71], 0, v[134:135]
	s_mov_b32 m0, s69
	s_nop 0
	global_load_lds_dwordx4 v[224:225], off
	v_lshl_add_u64 v[224:225], s[70:71], 0, v[138:139]
	s_add_i32 m0, s69, 0x2000
	s_nop 0
	global_load_lds_dwordx4 v[224:225], off
	v_lshl_add_u64 v[224:225], s[4:5], 0, v[132:133]
	s_mov_b32 m0, s17
	s_nop 0
	global_load_lds_dwordx4 v[224:225], off
	v_lshl_add_u64 v[224:225], s[4:5], 0, v[136:137]
	s_mov_b32 m0, s21
	s_nop 0
	global_load_lds_dwordx4 v[224:225], off
	s_waitcnt vmcnt(8)
	s_waitcnt lgkmcnt(0)
	s_barrier
	v_mfma_f32_16x16x32_bf16 v[64:67], v[152:155], v[184:187], 0
	v_mfma_f32_16x16x32_bf16 v[60:63], v[160:163], v[184:187], 0
	v_mfma_f32_16x16x32_bf16 v[56:59], v[152:155], v[192:195], 0
	v_mfma_f32_16x16x32_bf16 v[52:55], v[160:163], v[192:195], 0
	v_mfma_f32_16x16x32_bf16 v[40:43], v[152:155], v[208:211], 0
	v_mfma_f32_16x16x32_bf16 v[36:39], v[160:163], v[208:211], 0
	v_mfma_f32_16x16x32_bf16 v[24:27], v[152:155], v[216:219], 0
	v_mfma_f32_16x16x32_bf16 v[20:23], v[160:163], v[216:219], 0
	v_mfma_f32_16x16x32_bf16 v[64:67], v[156:159], v[188:191], v[64:67]
	v_mfma_f32_16x16x32_bf16 v[60:63], v[164:167], v[188:191], v[60:63]
	v_mfma_f32_16x16x32_bf16 v[56:59], v[156:159], v[204:207], v[56:59]
	v_mfma_f32_16x16x32_bf16 v[52:55], v[164:167], v[204:207], v[52:55]
	v_mfma_f32_16x16x32_bf16 v[40:43], v[156:159], v[212:215], v[40:43]
	v_mfma_f32_16x16x32_bf16 v[36:39], v[164:167], v[212:215], v[36:39]
	v_mfma_f32_16x16x32_bf16 v[24:27], v[156:159], v[220:223], v[24:27]
	v_mfma_f32_16x16x32_bf16 v[20:23], v[164:167], v[220:223], v[20:23]
	v_mfma_f32_16x16x32_bf16 v[48:51], v[168:171], v[184:187], 0
	v_mfma_f32_16x16x32_bf16 v[44:47], v[176:179], v[184:187], 0
	v_mfma_f32_16x16x32_bf16 v[32:35], v[168:171], v[192:195], 0
	v_mfma_f32_16x16x32_bf16 v[28:31], v[176:179], v[192:195], 0
	v_mfma_f32_16x16x32_bf16 v[16:19], v[168:171], v[208:211], 0
	v_mfma_f32_16x16x32_bf16 v[12:15], v[176:179], v[208:211], 0
	v_mfma_f32_16x16x32_bf16 v[8:11], v[168:171], v[216:219], 0
	v_mfma_f32_16x16x32_bf16 v[4:7], v[176:179], v[216:219], 0
	v_mfma_f32_16x16x32_bf16 v[48:51], v[172:175], v[188:191], v[48:51]
	v_mfma_f32_16x16x32_bf16 v[44:47], v[180:183], v[188:191], v[44:47]
	v_mfma_f32_16x16x32_bf16 v[32:35], v[172:175], v[204:207], v[32:35]
	v_mfma_f32_16x16x32_bf16 v[28:31], v[180:183], v[204:207], v[28:31]
	v_mfma_f32_16x16x32_bf16 v[16:19], v[172:175], v[212:215], v[16:19]
	v_mfma_f32_16x16x32_bf16 v[12:15], v[180:183], v[212:215], v[12:15]
	v_mfma_f32_16x16x32_bf16 v[8:11], v[172:175], v[220:223], v[8:11]
	v_mfma_f32_16x16x32_bf16 v[4:7], v[180:183], v[220:223], v[4:7]
	s_barrier
	s_add_i32 s69, 0, 0x18000
	v_add_u32_e32 v2, s69, v149
	s_add_i32 s70, 0, 0x1c000
	ds_read_b128 v[152:155], v2
	ds_read_b128 v[156:159], v2 offset:1024
	ds_read_b128 v[160:163], v2 offset:2048
	ds_read_b128 v[164:167], v2 offset:3072
	v_add_u32_e32 v2, s70, v149
	ds_read_b128 v[168:171], v2
	ds_read_b128 v[172:175], v2 offset:1024
	ds_read_b128 v[176:179], v2 offset:2048
	ds_read_b128 v[180:183], v2 offset:3072
	s_add_u32 s4, s4, 0x40000
	s_addc_u32 s5, s5, 0
	s_mov_b32 m0, s46
	v_lshl_add_u64 v[224:225], s[4:5], 0, v[132:133]
	ds_read_b128 v[184:187], v151 offset:32768
	ds_read_b128 v[188:191], v151 offset:33792
	ds_read_b128 v[192:195], v151 offset:34816
	ds_read_b128 v[204:207], v151 offset:35840
	ds_read_b128 v[208:211], v151 offset:36864
	ds_read_b128 v[212:215], v151 offset:37888
	ds_read_b128 v[216:219], v151 offset:38912
	ds_read_b128 v[220:223], v151 offset:39936
	global_load_lds_dwordx4 v[224:225], off
	v_lshl_add_u64 v[224:225], s[4:5], 0, v[136:137]
	s_mov_b32 m0, s47
	s_nop 0
	global_load_lds_dwordx4 v[224:225], off
	s_waitcnt vmcnt(8)
	s_waitcnt lgkmcnt(0)
	s_barrier
	v_mfma_f32_16x16x32_bf16 v[128:131], v[152:155], v[184:187], v[128:131]
	v_mfma_f32_16x16x32_bf16 v[124:127], v[160:163], v[184:187], v[124:127]
	v_mfma_f32_16x16x32_bf16 v[120:123], v[152:155], v[192:195], v[120:123]
	v_mfma_f32_16x16x32_bf16 v[116:119], v[160:163], v[192:195], v[116:119]
	v_mfma_f32_16x16x32_bf16 v[104:107], v[152:155], v[208:211], v[104:107]
	v_mfma_f32_16x16x32_bf16 v[100:103], v[160:163], v[208:211], v[100:103]
	v_mfma_f32_16x16x32_bf16 v[88:91], v[152:155], v[216:219], v[88:91]
	v_mfma_f32_16x16x32_bf16 v[84:87], v[160:163], v[216:219], v[84:87]
	v_mfma_f32_16x16x32_bf16 v[128:131], v[156:159], v[188:191], v[128:131]
	v_mfma_f32_16x16x32_bf16 v[124:127], v[164:167], v[188:191], v[124:127]
	v_mfma_f32_16x16x32_bf16 v[120:123], v[156:159], v[204:207], v[120:123]
	v_mfma_f32_16x16x32_bf16 v[116:119], v[164:167], v[204:207], v[116:119]
	v_mfma_f32_16x16x32_bf16 v[104:107], v[156:159], v[212:215], v[104:107]
	v_mfma_f32_16x16x32_bf16 v[100:103], v[164:167], v[212:215], v[100:103]
	v_mfma_f32_16x16x32_bf16 v[88:91], v[156:159], v[220:223], v[88:91]
	v_mfma_f32_16x16x32_bf16 v[84:87], v[164:167], v[220:223], v[84:87]
	v_mfma_f32_16x16x32_bf16 v[112:115], v[168:171], v[184:187], v[112:115]
	v_mfma_f32_16x16x32_bf16 v[108:111], v[176:179], v[184:187], v[108:111]
	v_mfma_f32_16x16x32_bf16 v[96:99], v[168:171], v[192:195], v[96:99]
	v_mfma_f32_16x16x32_bf16 v[92:95], v[176:179], v[192:195], v[92:95]
	v_mfma_f32_16x16x32_bf16 v[80:83], v[168:171], v[208:211], v[80:83]
	v_mfma_f32_16x16x32_bf16 v[76:79], v[176:179], v[208:211], v[76:79]
	v_mfma_f32_16x16x32_bf16 v[72:75], v[168:171], v[216:219], v[72:75]
	v_mfma_f32_16x16x32_bf16 v[68:71], v[176:179], v[216:219], v[68:71]
	v_mfma_f32_16x16x32_bf16 v[112:115], v[172:175], v[188:191], v[112:115]
	v_mfma_f32_16x16x32_bf16 v[108:111], v[180:183], v[188:191], v[108:111]
	v_mfma_f32_16x16x32_bf16 v[96:99], v[172:175], v[204:207], v[96:99]
	v_mfma_f32_16x16x32_bf16 v[92:95], v[180:183], v[204:207], v[92:95]
	v_mfma_f32_16x16x32_bf16 v[80:83], v[172:175], v[212:215], v[80:83]
	v_mfma_f32_16x16x32_bf16 v[76:79], v[180:183], v[212:215], v[76:79]
	v_mfma_f32_16x16x32_bf16 v[72:75], v[172:175], v[220:223], v[72:75]
	v_mfma_f32_16x16x32_bf16 v[68:71], v[180:183], v[220:223], v[68:71]
	s_barrier
	s_add_i32 s4, s69, s16
	v_lshl_add_u64 v[196:197], v[196:197], 0, s[34:35]
	s_mov_b32 m0, s4
	ds_read_b128 v[184:187], v151 offset:49152
	ds_read_b128 v[188:191], v151 offset:50176
	ds_read_b128 v[192:195], v151 offset:51200
	ds_read_b128 v[204:207], v151 offset:52224
	ds_read_b128 v[208:211], v151 offset:53248
	ds_read_b128 v[212:215], v151 offset:54272
	ds_read_b128 v[216:219], v151 offset:55296
	ds_read_b128 v[220:223], v151 offset:56320
	global_load_lds_dwordx4 v[196:197], off
	s_add_i32 m0, s4, 0x2000
	s_add_u32 s4, s50, 0x40080
	v_lshl_add_u64 v[196:197], v[198:199], 0, s[34:35]
	s_addc_u32 s5, s51, 0
	s_add_i32 s50, s70, s16
	global_load_lds_dwordx4 v[196:197], off
	v_lshl_add_u64 v[196:197], s[4:5], 0, v[134:135]
	s_mov_b32 m0, s50
	s_nop 0
	global_load_lds_dwordx4 v[196:197], off
	v_lshl_add_u64 v[196:197], s[4:5], 0, v[138:139]
	s_add_i32 m0, s50, 0x2000
	s_nop 0
	global_load_lds_dwordx4 v[196:197], off
	v_lshl_add_u64 v[196:197], s[12:13], 0, v[132:133]
	s_mov_b32 m0, s53
	s_nop 0
	global_load_lds_dwordx4 v[196:197], off
	v_lshl_add_u64 v[196:197], s[12:13], 0, v[136:137]
	s_mov_b32 m0, s56
	s_nop 0
	global_load_lds_dwordx4 v[196:197], off
	s_waitcnt vmcnt(8)
	s_waitcnt lgkmcnt(0)
	s_barrier
	v_mfma_f32_16x16x32_bf16 v[64:67], v[152:155], v[184:187], v[64:67]
	v_mfma_f32_16x16x32_bf16 v[60:63], v[160:163], v[184:187], v[60:63]
	v_mfma_f32_16x16x32_bf16 v[56:59], v[152:155], v[192:195], v[56:59]
	v_mfma_f32_16x16x32_bf16 v[52:55], v[160:163], v[192:195], v[52:55]
	v_mfma_f32_16x16x32_bf16 v[40:43], v[152:155], v[208:211], v[40:43]
	v_mfma_f32_16x16x32_bf16 v[36:39], v[160:163], v[208:211], v[36:39]
	v_mfma_f32_16x16x32_bf16 v[24:27], v[152:155], v[216:219], v[24:27]
	v_mfma_f32_16x16x32_bf16 v[20:23], v[160:163], v[216:219], v[20:23]
	v_mfma_f32_16x16x32_bf16 v[64:67], v[156:159], v[188:191], v[64:67]
	v_mfma_f32_16x16x32_bf16 v[60:63], v[164:167], v[188:191], v[60:63]
	v_mfma_f32_16x16x32_bf16 v[56:59], v[156:159], v[204:207], v[56:59]
	v_mfma_f32_16x16x32_bf16 v[52:55], v[164:167], v[204:207], v[52:55]
	v_mfma_f32_16x16x32_bf16 v[40:43], v[156:159], v[212:215], v[40:43]
	v_mfma_f32_16x16x32_bf16 v[36:39], v[164:167], v[212:215], v[36:39]
	v_mfma_f32_16x16x32_bf16 v[24:27], v[156:159], v[220:223], v[24:27]
	v_mfma_f32_16x16x32_bf16 v[20:23], v[164:167], v[220:223], v[20:23]
	v_mfma_f32_16x16x32_bf16 v[48:51], v[168:171], v[184:187], v[48:51]
	v_mfma_f32_16x16x32_bf16 v[44:47], v[176:179], v[184:187], v[44:47]
	v_mfma_f32_16x16x32_bf16 v[32:35], v[168:171], v[192:195], v[32:35]
	v_mfma_f32_16x16x32_bf16 v[28:31], v[176:179], v[192:195], v[28:31]
	v_mfma_f32_16x16x32_bf16 v[16:19], v[168:171], v[208:211], v[16:19]
	v_mfma_f32_16x16x32_bf16 v[12:15], v[176:179], v[208:211], v[12:15]
	v_mfma_f32_16x16x32_bf16 v[8:11], v[168:171], v[216:219], v[8:11]
	v_mfma_f32_16x16x32_bf16 v[4:7], v[176:179], v[216:219], v[4:7]
	v_mfma_f32_16x16x32_bf16 v[48:51], v[172:175], v[188:191], v[48:51]
	v_mfma_f32_16x16x32_bf16 v[44:47], v[180:183], v[188:191], v[44:47]
	v_mfma_f32_16x16x32_bf16 v[32:35], v[172:175], v[204:207], v[32:35]
	v_mfma_f32_16x16x32_bf16 v[28:31], v[180:183], v[204:207], v[28:31]
	v_mfma_f32_16x16x32_bf16 v[16:19], v[172:175], v[212:215], v[16:19]
	v_mfma_f32_16x16x32_bf16 v[12:15], v[180:183], v[212:215], v[12:15]
	v_mfma_f32_16x16x32_bf16 v[8:11], v[172:175], v[220:223], v[8:11]
	v_mfma_f32_16x16x32_bf16 v[4:7], v[180:183], v[220:223], v[4:7]
	s_barrier
	s_add_i32 s68, s68, 2
	s_add_u32 s48, s48, 0x100
	s_addc_u32 s49, s49, 0
	s_cmp_gt_u32 s68, 13
.LBB0_311:
	s_add_u32 s4, s38, s48
	s_addc_u32 s5, s39, s49
	s_add_u32 s69, s4, 0x100
	s_addc_u32 s70, s5, 0
	s_add_u32 s50, s64, s48
	s_addc_u32 s51, s65, s49
	s_add_u32 s4, s4, 0x180
	s_addc_u32 s5, s5, 0
	s_add_i32 s71, 0, 0x10000
	s_add_i32 s72, 0, 0x14000
	v_add_u32_e32 v2, s71, v149
	ds_read_b128 v[152:155], v2
	s_waitcnt vmcnt(0)
	ds_read_b128 v[156:159], v2 offset:1024
	ds_read_b128 v[160:163], v2 offset:2048
	ds_read_b128 v[164:167], v2 offset:3072
	v_add_u32_e32 v2, s72, v149
	ds_read_b128 v[168:171], v2
	ds_read_b128 v[172:175], v2 offset:1024
	ds_read_b128 v[176:179], v2 offset:2048
	ds_read_b128 v[180:183], v2 offset:3072
	s_cmpk_eq_i32 s48, 0x700
	s_cselect_b32 s13, s63, s5
	s_cselect_b32 s12, s62, s4
	s_cselect_b32 s51, s37, s51
	s_cselect_b32 s50, s61, s50
	s_cselect_b32 s5, s41, s70
	s_cselect_b32 s4, s60, s69
	v_lshl_add_u64 v[196:197], v[144:145], 0, s[48:49]
	s_add_i32 m0, s17, 0xc000
	ds_read_b128 v[184:187], v151
	ds_read_b128 v[188:191], v151 offset:1024
	ds_read_b128 v[192:195], v151 offset:2048
	ds_read_b128 v[204:207], v151 offset:3072
	ds_read_b128 v[208:211], v151 offset:4096
	ds_read_b128 v[212:215], v151 offset:5120
	ds_read_b128 v[216:219], v151 offset:6144
	ds_read_b128 v[220:223], v151 offset:7168
	global_load_lds_dwordx4 v[196:197], off
	v_lshl_add_u64 v[196:197], v[146:147], 0, s[48:49]
	s_add_i32 m0, s17, 0xe000
	s_nop 0
	global_load_lds_dwordx4 v[196:197], off
	s_waitcnt vmcnt(8)
	s_waitcnt lgkmcnt(0)
	s_barrier
	v_mfma_f32_16x16x32_bf16 v[128:131], v[152:155], v[184:187], v[128:131]
	v_mfma_f32_16x16x32_bf16 v[124:127], v[160:163], v[184:187], v[124:127]
	v_mfma_f32_16x16x32_bf16 v[120:123], v[152:155], v[192:195], v[120:123]
	v_mfma_f32_16x16x32_bf16 v[116:119], v[160:163], v[192:195], v[116:119]
	v_mfma_f32_16x16x32_bf16 v[104:107], v[152:155], v[208:211], v[104:107]
	v_mfma_f32_16x16x32_bf16 v[100:103], v[160:163], v[208:211], v[100:103]
	v_mfma_f32_16x16x32_bf16 v[88:91], v[152:155], v[216:219], v[88:91]
	v_mfma_f32_16x16x32_bf16 v[84:87], v[160:163], v[216:219], v[84:87]
	v_mfma_f32_16x16x32_bf16 v[128:131], v[156:159], v[188:191], v[128:131]
	v_mfma_f32_16x16x32_bf16 v[124:127], v[164:167], v[188:191], v[124:127]
	v_mfma_f32_16x16x32_bf16 v[120:123], v[156:159], v[204:207], v[120:123]
	v_mfma_f32_16x16x32_bf16 v[116:119], v[164:167], v[204:207], v[116:119]
	v_mfma_f32_16x16x32_bf16 v[104:107], v[156:159], v[212:215], v[104:107]
	v_mfma_f32_16x16x32_bf16 v[100:103], v[164:167], v[212:215], v[100:103]
	v_mfma_f32_16x16x32_bf16 v[88:91], v[156:159], v[220:223], v[88:91]
	v_mfma_f32_16x16x32_bf16 v[84:87], v[164:167], v[220:223], v[84:87]
	v_mfma_f32_16x16x32_bf16 v[112:115], v[168:171], v[184:187], v[112:115]
	v_mfma_f32_16x16x32_bf16 v[108:111], v[176:179], v[184:187], v[108:111]
	v_mfma_f32_16x16x32_bf16 v[96:99], v[168:171], v[192:195], v[96:99]
	v_mfma_f32_16x16x32_bf16 v[92:95], v[176:179], v[192:195], v[92:95]
	v_mfma_f32_16x16x32_bf16 v[80:83], v[168:171], v[208:211], v[80:83]
	v_mfma_f32_16x16x32_bf16 v[76:79], v[176:179], v[208:211], v[76:79]
	v_mfma_f32_16x16x32_bf16 v[72:75], v[168:171], v[216:219], v[72:75]
	v_mfma_f32_16x16x32_bf16 v[68:71], v[176:179], v[216:219], v[68:71]
	v_mfma_f32_16x16x32_bf16 v[112:115], v[172:175], v[188:191], v[112:115]
	v_mfma_f32_16x16x32_bf16 v[108:111], v[180:183], v[188:191], v[108:111]
	v_mfma_f32_16x16x32_bf16 v[96:99], v[172:175], v[204:207], v[96:99]
	v_mfma_f32_16x16x32_bf16 v[92:95], v[180:183], v[204:207], v[92:95]
	v_mfma_f32_16x16x32_bf16 v[80:83], v[172:175], v[212:215], v[80:83]
	v_mfma_f32_16x16x32_bf16 v[76:79], v[180:183], v[212:215], v[76:79]
	v_mfma_f32_16x16x32_bf16 v[72:75], v[172:175], v[220:223], v[72:75]
	v_mfma_f32_16x16x32_bf16 v[68:71], v[180:183], v[220:223], v[68:71]
	s_barrier
	s_add_i32 s69, s71, s16
	v_lshl_add_u64 v[196:197], s[50:51], 0, v[134:135]
	s_mov_b32 m0, s69
	ds_read_b128 v[184:187], v151 offset:16384
	ds_read_b128 v[188:191], v151 offset:17408
	ds_read_b128 v[192:195], v151 offset:18432
	ds_read_b128 v[204:207], v151 offset:19456
	ds_read_b128 v[208:211], v151 offset:20480
	ds_read_b128 v[212:215], v151 offset:21504
	ds_read_b128 v[216:219], v151 offset:22528
	ds_read_b128 v[220:223], v151 offset:23552
	global_load_lds_dwordx4 v[196:197], off
	s_add_i32 m0, s69, 0x2000
	s_add_u32 s70, s50, 0x40000
	v_lshl_add_u64 v[198:199], s[50:51], 0, v[138:139]
	s_addc_u32 s71, s51, 0
	s_add_i32 s69, s72, s16
	global_load_lds_dwordx4 v[198:199], off
	v_lshl_add_u64 v[224:225], s[70:71], 0, v[134:135]
	s_mov_b32 m0, s69
	s_nop 0
	global_load_lds_dwordx4 v[224:225], off
	v_lshl_add_u64 v[224:225], s[70:71], 0, v[138:139]
	s_add_i32 m0, s69, 0x2000
	s_nop 0
	global_load_lds_dwordx4 v[224:225], off
	v_lshl_add_u64 v[224:225], s[4:5], 0, v[132:133]
	s_mov_b32 m0, s17
	s_nop 0
	global_load_lds_dwordx4 v[224:225], off
	v_lshl_add_u64 v[224:225], s[4:5], 0, v[136:137]
	s_mov_b32 m0, s21
	s_nop 0
	global_load_lds_dwordx4 v[224:225], off
	s_waitcnt vmcnt(8)
	s_waitcnt lgkmcnt(0)
	s_barrier
	v_mfma_f32_16x16x32_bf16 v[64:67], v[152:155], v[184:187], v[64:67]
	v_mfma_f32_16x16x32_bf16 v[60:63], v[160:163], v[184:187], v[60:63]
	v_mfma_f32_16x16x32_bf16 v[56:59], v[152:155], v[192:195], v[56:59]
	v_mfma_f32_16x16x32_bf16 v[52:55], v[160:163], v[192:195], v[52:55]
	v_mfma_f32_16x16x32_bf16 v[40:43], v[152:155], v[208:211], v[40:43]
	v_mfma_f32_16x16x32_bf16 v[36:39], v[160:163], v[208:211], v[36:39]
	v_mfma_f32_16x16x32_bf16 v[24:27], v[152:155], v[216:219], v[24:27]
	v_mfma_f32_16x16x32_bf16 v[20:23], v[160:163], v[216:219], v[20:23]
	v_mfma_f32_16x16x32_bf16 v[64:67], v[156:159], v[188:191], v[64:67]
	v_mfma_f32_16x16x32_bf16 v[60:63], v[164:167], v[188:191], v[60:63]
	v_mfma_f32_16x16x32_bf16 v[56:59], v[156:159], v[204:207], v[56:59]
	v_mfma_f32_16x16x32_bf16 v[52:55], v[164:167], v[204:207], v[52:55]
	v_mfma_f32_16x16x32_bf16 v[40:43], v[156:159], v[212:215], v[40:43]
	v_mfma_f32_16x16x32_bf16 v[36:39], v[164:167], v[212:215], v[36:39]
	v_mfma_f32_16x16x32_bf16 v[24:27], v[156:159], v[220:223], v[24:27]
	v_mfma_f32_16x16x32_bf16 v[20:23], v[164:167], v[220:223], v[20:23]
	v_mfma_f32_16x16x32_bf16 v[48:51], v[168:171], v[184:187], v[48:51]
	v_mfma_f32_16x16x32_bf16 v[44:47], v[176:179], v[184:187], v[44:47]
	v_mfma_f32_16x16x32_bf16 v[32:35], v[168:171], v[192:195], v[32:35]
	v_mfma_f32_16x16x32_bf16 v[28:31], v[176:179], v[192:195], v[28:31]
	v_mfma_f32_16x16x32_bf16 v[16:19], v[168:171], v[208:211], v[16:19]
	v_mfma_f32_16x16x32_bf16 v[12:15], v[176:179], v[208:211], v[12:15]
	v_mfma_f32_16x16x32_bf16 v[8:11], v[168:171], v[216:219], v[8:11]
	v_mfma_f32_16x16x32_bf16 v[4:7], v[176:179], v[216:219], v[4:7]
	v_mfma_f32_16x16x32_bf16 v[48:51], v[172:175], v[188:191], v[48:51]
	v_mfma_f32_16x16x32_bf16 v[44:47], v[180:183], v[188:191], v[44:47]
	v_mfma_f32_16x16x32_bf16 v[32:35], v[172:175], v[204:207], v[32:35]
	v_mfma_f32_16x16x32_bf16 v[28:31], v[180:183], v[204:207], v[28:31]
	v_mfma_f32_16x16x32_bf16 v[16:19], v[172:175], v[212:215], v[16:19]
	v_mfma_f32_16x16x32_bf16 v[12:15], v[180:183], v[212:215], v[12:15]
	v_mfma_f32_16x16x32_bf16 v[8:11], v[172:175], v[220:223], v[8:11]
	v_mfma_f32_16x16x32_bf16 v[4:7], v[180:183], v[220:223], v[4:7]
	s_barrier
	s_add_i32 s69, 0, 0x18000
	v_add_u32_e32 v2, s69, v149
	s_add_i32 s70, 0, 0x1c000
	ds_read_b128 v[152:155], v2
	ds_read_b128 v[156:159], v2 offset:1024
	ds_read_b128 v[160:163], v2 offset:2048
	ds_read_b128 v[164:167], v2 offset:3072
	v_add_u32_e32 v2, s70, v149
	ds_read_b128 v[168:171], v2
	ds_read_b128 v[172:175], v2 offset:1024
	ds_read_b128 v[176:179], v2 offset:2048
	ds_read_b128 v[180:183], v2 offset:3072
	s_add_u32 s4, s4, 0x40000
	s_addc_u32 s5, s5, 0
	s_mov_b32 m0, s46
	v_lshl_add_u64 v[224:225], s[4:5], 0, v[132:133]
	ds_read_b128 v[184:187], v151 offset:32768
	ds_read_b128 v[188:191], v151 offset:33792
	ds_read_b128 v[192:195], v151 offset:34816
	ds_read_b128 v[204:207], v151 offset:35840
	ds_read_b128 v[208:211], v151 offset:36864
	ds_read_b128 v[212:215], v151 offset:37888
	ds_read_b128 v[216:219], v151 offset:38912
	ds_read_b128 v[220:223], v151 offset:39936
	global_load_lds_dwordx4 v[224:225], off
	v_lshl_add_u64 v[224:225], s[4:5], 0, v[136:137]
	s_mov_b32 m0, s47
	s_nop 0
	global_load_lds_dwordx4 v[224:225], off
	s_waitcnt vmcnt(8)
	s_waitcnt lgkmcnt(0)
	s_barrier
	v_mfma_f32_16x16x32_bf16 v[128:131], v[152:155], v[184:187], v[128:131]
	v_mfma_f32_16x16x32_bf16 v[124:127], v[160:163], v[184:187], v[124:127]
	v_mfma_f32_16x16x32_bf16 v[120:123], v[152:155], v[192:195], v[120:123]
	v_mfma_f32_16x16x32_bf16 v[116:119], v[160:163], v[192:195], v[116:119]
	v_mfma_f32_16x16x32_bf16 v[104:107], v[152:155], v[208:211], v[104:107]
	v_mfma_f32_16x16x32_bf16 v[100:103], v[160:163], v[208:211], v[100:103]
	v_mfma_f32_16x16x32_bf16 v[88:91], v[152:155], v[216:219], v[88:91]
	v_mfma_f32_16x16x32_bf16 v[84:87], v[160:163], v[216:219], v[84:87]
	v_mfma_f32_16x16x32_bf16 v[128:131], v[156:159], v[188:191], v[128:131]
	v_mfma_f32_16x16x32_bf16 v[124:127], v[164:167], v[188:191], v[124:127]
	v_mfma_f32_16x16x32_bf16 v[120:123], v[156:159], v[204:207], v[120:123]
	v_mfma_f32_16x16x32_bf16 v[116:119], v[164:167], v[204:207], v[116:119]
	v_mfma_f32_16x16x32_bf16 v[104:107], v[156:159], v[212:215], v[104:107]
	v_mfma_f32_16x16x32_bf16 v[100:103], v[164:167], v[212:215], v[100:103]
	v_mfma_f32_16x16x32_bf16 v[88:91], v[156:159], v[220:223], v[88:91]
	v_mfma_f32_16x16x32_bf16 v[84:87], v[164:167], v[220:223], v[84:87]
	v_mfma_f32_16x16x32_bf16 v[112:115], v[168:171], v[184:187], v[112:115]
	v_mfma_f32_16x16x32_bf16 v[108:111], v[176:179], v[184:187], v[108:111]
	v_mfma_f32_16x16x32_bf16 v[96:99], v[168:171], v[192:195], v[96:99]
	v_mfma_f32_16x16x32_bf16 v[92:95], v[176:179], v[192:195], v[92:95]
	v_mfma_f32_16x16x32_bf16 v[80:83], v[168:171], v[208:211], v[80:83]
	v_mfma_f32_16x16x32_bf16 v[76:79], v[176:179], v[208:211], v[76:79]
	v_mfma_f32_16x16x32_bf16 v[72:75], v[168:171], v[216:219], v[72:75]
	v_mfma_f32_16x16x32_bf16 v[68:71], v[176:179], v[216:219], v[68:71]
	v_mfma_f32_16x16x32_bf16 v[112:115], v[172:175], v[188:191], v[112:115]
	v_mfma_f32_16x16x32_bf16 v[108:111], v[180:183], v[188:191], v[108:111]
	v_mfma_f32_16x16x32_bf16 v[96:99], v[172:175], v[204:207], v[96:99]
	v_mfma_f32_16x16x32_bf16 v[92:95], v[180:183], v[204:207], v[92:95]
	v_mfma_f32_16x16x32_bf16 v[80:83], v[172:175], v[212:215], v[80:83]
	v_mfma_f32_16x16x32_bf16 v[76:79], v[180:183], v[212:215], v[76:79]
	v_mfma_f32_16x16x32_bf16 v[72:75], v[172:175], v[220:223], v[72:75]
	v_mfma_f32_16x16x32_bf16 v[68:71], v[180:183], v[220:223], v[68:71]
	s_barrier
	s_add_i32 s4, s69, s16
	v_lshl_add_u64 v[196:197], v[196:197], 0, s[34:35]
	s_mov_b32 m0, s4
	ds_read_b128 v[184:187], v151 offset:49152
	ds_read_b128 v[188:191], v151 offset:50176
	ds_read_b128 v[192:195], v151 offset:51200
	ds_read_b128 v[204:207], v151 offset:52224
	ds_read_b128 v[208:211], v151 offset:53248
	ds_read_b128 v[212:215], v151 offset:54272
	ds_read_b128 v[216:219], v151 offset:55296
	ds_read_b128 v[220:223], v151 offset:56320
	global_load_lds_dwordx4 v[196:197], off
	s_add_i32 m0, s4, 0x2000
	s_add_u32 s4, s50, 0x40080
	v_lshl_add_u64 v[196:197], v[198:199], 0, s[34:35]
	s_addc_u32 s5, s51, 0
	s_add_i32 s50, s70, s16
	global_load_lds_dwordx4 v[196:197], off
	v_lshl_add_u64 v[196:197], s[4:5], 0, v[134:135]
	s_mov_b32 m0, s50
	s_nop 0
	global_load_lds_dwordx4 v[196:197], off
	v_lshl_add_u64 v[196:197], s[4:5], 0, v[138:139]
	s_add_i32 m0, s50, 0x2000
	s_nop 0
	global_load_lds_dwordx4 v[196:197], off
	v_lshl_add_u64 v[196:197], s[12:13], 0, v[132:133]
	s_mov_b32 m0, s53
	s_nop 0
	global_load_lds_dwordx4 v[196:197], off
	v_lshl_add_u64 v[196:197], s[12:13], 0, v[136:137]
	s_mov_b32 m0, s56
	s_nop 0
	global_load_lds_dwordx4 v[196:197], off
	s_waitcnt vmcnt(8)
	s_waitcnt lgkmcnt(0)
	s_barrier
	v_mfma_f32_16x16x32_bf16 v[64:67], v[152:155], v[184:187], v[64:67]
	v_mfma_f32_16x16x32_bf16 v[60:63], v[160:163], v[184:187], v[60:63]
	v_mfma_f32_16x16x32_bf16 v[56:59], v[152:155], v[192:195], v[56:59]
	v_mfma_f32_16x16x32_bf16 v[52:55], v[160:163], v[192:195], v[52:55]
	v_mfma_f32_16x16x32_bf16 v[40:43], v[152:155], v[208:211], v[40:43]
	v_mfma_f32_16x16x32_bf16 v[36:39], v[160:163], v[208:211], v[36:39]
	v_mfma_f32_16x16x32_bf16 v[24:27], v[152:155], v[216:219], v[24:27]
	v_mfma_f32_16x16x32_bf16 v[20:23], v[160:163], v[216:219], v[20:23]
	v_mfma_f32_16x16x32_bf16 v[64:67], v[156:159], v[188:191], v[64:67]
	v_mfma_f32_16x16x32_bf16 v[60:63], v[164:167], v[188:191], v[60:63]
	v_mfma_f32_16x16x32_bf16 v[56:59], v[156:159], v[204:207], v[56:59]
	v_mfma_f32_16x16x32_bf16 v[52:55], v[164:167], v[204:207], v[52:55]
	v_mfma_f32_16x16x32_bf16 v[40:43], v[156:159], v[212:215], v[40:43]
	v_mfma_f32_16x16x32_bf16 v[36:39], v[164:167], v[212:215], v[36:39]
	v_mfma_f32_16x16x32_bf16 v[24:27], v[156:159], v[220:223], v[24:27]
	v_mfma_f32_16x16x32_bf16 v[20:23], v[164:167], v[220:223], v[20:23]
	v_mfma_f32_16x16x32_bf16 v[48:51], v[168:171], v[184:187], v[48:51]
	v_mfma_f32_16x16x32_bf16 v[44:47], v[176:179], v[184:187], v[44:47]
	v_mfma_f32_16x16x32_bf16 v[32:35], v[168:171], v[192:195], v[32:35]
	v_mfma_f32_16x16x32_bf16 v[28:31], v[176:179], v[192:195], v[28:31]
	v_mfma_f32_16x16x32_bf16 v[16:19], v[168:171], v[208:211], v[16:19]
	v_mfma_f32_16x16x32_bf16 v[12:15], v[176:179], v[208:211], v[12:15]
	v_mfma_f32_16x16x32_bf16 v[8:11], v[168:171], v[216:219], v[8:11]
	v_mfma_f32_16x16x32_bf16 v[4:7], v[176:179], v[216:219], v[4:7]
	v_mfma_f32_16x16x32_bf16 v[48:51], v[172:175], v[188:191], v[48:51]
	v_mfma_f32_16x16x32_bf16 v[44:47], v[180:183], v[188:191], v[44:47]
	v_mfma_f32_16x16x32_bf16 v[32:35], v[172:175], v[204:207], v[32:35]
	v_mfma_f32_16x16x32_bf16 v[28:31], v[180:183], v[204:207], v[28:31]
	v_mfma_f32_16x16x32_bf16 v[16:19], v[172:175], v[212:215], v[16:19]
	v_mfma_f32_16x16x32_bf16 v[12:15], v[180:183], v[212:215], v[12:15]
	v_mfma_f32_16x16x32_bf16 v[8:11], v[172:175], v[220:223], v[8:11]
	v_mfma_f32_16x16x32_bf16 v[4:7], v[180:183], v[220:223], v[4:7]
	s_barrier
	s_add_i32 s68, s68, 2
	s_add_u32 s48, s48, 0x100
	s_addc_u32 s49, s49, 0
	s_cmp_gt_u32 s68, 13
	s_cbranch_scc0 .LBB0_311
	s_and_b64 vcc, exec, s[18:19]
	s_mov_b32 s62, 0x18000
	s_mov_b32 s63, 0x1a000
	s_cbranch_vccz .LBB0_314
	s_barrier

.LBB0_382:
	s_ashr_i32 s51, s50, 31
	s_lshl_b64 s[4:5], s[50:51], 19
	s_add_u32 s64, s8, s4
	s_addc_u32 s65, s9, s5
	s_and_b64 s[4:5], s[38:39], exec
	s_cselect_b32 s51, s65, s41
	s_cselect_b32 s71, s64, s40
	s_ashr_i32 s11, s10, 31
	s_lshl_b64 s[4:5], s[10:11], 18
	s_add_u32 s36, s16, s4
	s_addc_u32 s37, s17, s5
	s_and_b64 s[4:5], s[38:39], exec
	s_cselect_b32 s11, s37, s43
	s_cselect_b32 s74, s36, s42
	s_add_u32 s75, s71, 0x80
	s_addc_u32 s76, s51, 0
	s_add_u32 s4, s40, 0x40080
	s_addc_u32 s5, s41, 0
	s_add_u32 s77, s42, 0x100
	v_lshl_add_u64 v[100:101], s[4:5], 0, v[176:177]
	v_lshl_add_u64 v[102:103], s[4:5], 0, v[178:179]
	s_addc_u32 s78, s43, 0
	s_mov_b32 s79, -2
	s_mov_b64 s[42:43], 0
	s_add_u32 s4, s40, s42
	s_addc_u32 s5, s41, s43
	s_add_u32 s80, s4, 0x100
	s_addc_u32 s81, s5, 0
	s_add_u32 s48, s77, s42
	s_addc_u32 s49, s78, s43
	s_add_u32 s4, s4, 0x180
	s_addc_u32 s5, s5, 0
	s_add_i32 s82, 0, 0x10000
	s_add_i32 s83, 0, 0x14000
	v_add_u32_e32 v2, s82, v203
	ds_read_b128 v[104:107], v2
	ds_read_b128 v[124:127], v2 offset:1024
	ds_read_b128 v[128:131], v2 offset:2048
	ds_read_b128 v[148:151], v2 offset:3072
	v_add_u32_e32 v2, s83, v203
	ds_read_b128 v[152:155], v2
	ds_read_b128 v[156:159], v2 offset:1024
	ds_read_b128 v[160:163], v2 offset:2048
	ds_read_b128 v[164:167], v2 offset:3072
	s_cmpk_eq_i32 s42, 0x300
	s_cselect_b32 s45, s76, s5
	s_cselect_b32 s44, s75, s4
	s_cselect_b32 s49, s11, s49
	s_cselect_b32 s48, s74, s48
	s_cselect_b32 s5, s51, s81
	s_cselect_b32 s4, s71, s80
	v_lshl_add_u64 v[196:197], v[100:101], 0, s[42:43]
	s_add_i32 m0, s47, 0xc000
	ds_read_b128 v[180:183], v210
	ds_read_b128 v[184:187], v210 offset:1024
	ds_read_b128 v[188:191], v210 offset:2048
	ds_read_b128 v[192:195], v210 offset:3072
	ds_read_b128 v[204:207], v210 offset:4096
	ds_read_b128 v[212:215], v210 offset:5120
	ds_read_b128 v[216:219], v210 offset:6144
	ds_read_b128 v[220:223], v210 offset:7168
	global_load_lds_dwordx4 v[196:197], off
	v_lshl_add_u64 v[196:197], v[102:103], 0, s[42:43]
	s_add_i32 m0, s47, 0xe000
	s_nop 0
	global_load_lds_dwordx4 v[196:197], off
	s_waitcnt vmcnt(8)
	s_waitcnt lgkmcnt(0)
	s_barrier
	v_mfma_f32_16x16x32_bf16 v[144:147], v[104:107], v[180:183], 0
	v_mfma_f32_16x16x32_bf16 v[140:143], v[128:131], v[180:183], 0
	v_mfma_f32_16x16x32_bf16 v[120:123], v[104:107], v[188:191], 0
	v_mfma_f32_16x16x32_bf16 v[116:119], v[128:131], v[188:191], 0
	v_mfma_f32_16x16x32_bf16 v[96:99], v[104:107], v[204:207], 0
	v_mfma_f32_16x16x32_bf16 v[92:95], v[128:131], v[204:207], 0
	v_mfma_f32_16x16x32_bf16 v[80:83], v[104:107], v[216:219], 0
	v_mfma_f32_16x16x32_bf16 v[76:79], v[128:131], v[216:219], 0
	v_mfma_f32_16x16x32_bf16 v[144:147], v[124:127], v[184:187], v[144:147]
	v_mfma_f32_16x16x32_bf16 v[140:143], v[148:151], v[184:187], v[140:143]
	v_mfma_f32_16x16x32_bf16 v[120:123], v[124:127], v[192:195], v[120:123]
	v_mfma_f32_16x16x32_bf16 v[116:119], v[148:151], v[192:195], v[116:119]
	v_mfma_f32_16x16x32_bf16 v[96:99], v[124:127], v[212:215], v[96:99]
	v_mfma_f32_16x16x32_bf16 v[92:95], v[148:151], v[212:215], v[92:95]
	v_mfma_f32_16x16x32_bf16 v[80:83], v[124:127], v[220:223], v[80:83]
	v_mfma_f32_16x16x32_bf16 v[76:79], v[148:151], v[220:223], v[76:79]
	v_mfma_f32_16x16x32_bf16 v[136:139], v[152:155], v[180:183], 0
	v_mfma_f32_16x16x32_bf16 v[132:135], v[160:163], v[180:183], 0
	v_mfma_f32_16x16x32_bf16 v[112:115], v[152:155], v[188:191], 0
	v_mfma_f32_16x16x32_bf16 v[108:111], v[160:163], v[188:191], 0
	v_mfma_f32_16x16x32_bf16 v[88:91], v[152:155], v[204:207], 0
	v_mfma_f32_16x16x32_bf16 v[84:87], v[160:163], v[204:207], 0
	v_mfma_f32_16x16x32_bf16 v[72:75], v[152:155], v[216:219], 0
	v_mfma_f32_16x16x32_bf16 v[68:71], v[160:163], v[216:219], 0
	v_mfma_f32_16x16x32_bf16 v[136:139], v[156:159], v[184:187], v[136:139]
	v_mfma_f32_16x16x32_bf16 v[132:135], v[164:167], v[184:187], v[132:135]
	v_mfma_f32_16x16x32_bf16 v[112:115], v[156:159], v[192:195], v[112:115]
	v_mfma_f32_16x16x32_bf16 v[108:111], v[164:167], v[192:195], v[108:111]
	v_mfma_f32_16x16x32_bf16 v[88:91], v[156:159], v[212:215], v[88:91]
	v_mfma_f32_16x16x32_bf16 v[84:87], v[164:167], v[212:215], v[84:87]
	v_mfma_f32_16x16x32_bf16 v[72:75], v[156:159], v[220:223], v[72:75]
	v_mfma_f32_16x16x32_bf16 v[68:71], v[164:167], v[220:223], v[68:71]
	s_barrier
	s_add_i32 s80, s82, s46
	v_lshl_add_u64 v[196:197], s[48:49], 0, v[172:173]
	s_mov_b32 m0, s80
	ds_read_b128 v[180:183], v210 offset:16384
	ds_read_b128 v[184:187], v210 offset:17408
	ds_read_b128 v[188:191], v210 offset:18432
	ds_read_b128 v[192:195], v210 offset:19456
	ds_read_b128 v[204:207], v210 offset:20480
	ds_read_b128 v[212:215], v210 offset:21504
	ds_read_b128 v[216:219], v210 offset:22528
	ds_read_b128 v[220:223], v210 offset:23552
	global_load_lds_dwordx4 v[196:197], off
	s_add_i32 m0, s80, 0x2000
	s_add_u32 s80, s48, 0x20000
	v_lshl_add_u64 v[198:199], s[48:49], 0, v[168:169]
	s_addc_u32 s81, s49, 0
	s_add_i32 s82, s83, s46
	global_load_lds_dwordx4 v[198:199], off
	v_lshl_add_u64 v[208:209], s[80:81], 0, v[172:173]
	s_mov_b32 m0, s82
	s_nop 0
	global_load_lds_dwordx4 v[208:209], off
	v_lshl_add_u64 v[208:209], s[80:81], 0, v[168:169]
	s_add_i32 m0, s82, 0x2000
	s_nop 0
	global_load_lds_dwordx4 v[208:209], off
	v_lshl_add_u64 v[208:209], s[4:5], 0, v[174:175]
	s_mov_b32 m0, s47
	s_nop 0
	global_load_lds_dwordx4 v[208:209], off
	v_lshl_add_u64 v[208:209], s[4:5], 0, v[170:171]
	s_mov_b32 m0, s56
	s_nop 0
	global_load_lds_dwordx4 v[208:209], off
	s_waitcnt vmcnt(8)
	s_waitcnt lgkmcnt(0)
	s_barrier
	v_mfma_f32_16x16x32_bf16 v[64:67], v[104:107], v[180:183], 0
	v_mfma_f32_16x16x32_bf16 v[60:63], v[128:131], v[180:183], 0
	v_mfma_f32_16x16x32_bf16 v[48:51], v[104:107], v[188:191], 0
	v_mfma_f32_16x16x32_bf16 v[44:47], v[128:131], v[188:191], 0
	v_mfma_f32_16x16x32_bf16 v[32:35], v[104:107], v[204:207], 0
	v_mfma_f32_16x16x32_bf16 v[28:31], v[128:131], v[204:207], 0
	v_mfma_f32_16x16x32_bf16 v[16:19], v[104:107], v[216:219], 0
	v_mfma_f32_16x16x32_bf16 v[12:15], v[128:131], v[216:219], 0
	v_mfma_f32_16x16x32_bf16 v[64:67], v[124:127], v[184:187], v[64:67]
	v_mfma_f32_16x16x32_bf16 v[60:63], v[148:151], v[184:187], v[60:63]
	v_mfma_f32_16x16x32_bf16 v[48:51], v[124:127], v[192:195], v[48:51]
	v_mfma_f32_16x16x32_bf16 v[44:47], v[148:151], v[192:195], v[44:47]
	v_mfma_f32_16x16x32_bf16 v[32:35], v[124:127], v[212:215], v[32:35]
	v_mfma_f32_16x16x32_bf16 v[28:31], v[148:151], v[212:215], v[28:31]
	v_mfma_f32_16x16x32_bf16 v[16:19], v[124:127], v[220:223], v[16:19]
	v_mfma_f32_16x16x32_bf16 v[12:15], v[148:151], v[220:223], v[12:15]
	v_mfma_f32_16x16x32_bf16 v[56:59], v[152:155], v[180:183], 0
	v_mfma_f32_16x16x32_bf16 v[52:55], v[160:163], v[180:183], 0
	v_mfma_f32_16x16x32_bf16 v[40:43], v[152:155], v[188:191], 0
	v_mfma_f32_16x16x32_bf16 v[36:39], v[160:163], v[188:191], 0
	v_mfma_f32_16x16x32_bf16 v[24:27], v[152:155], v[204:207], 0
	v_mfma_f32_16x16x32_bf16 v[20:23], v[160:163], v[204:207], 0
	v_mfma_f32_16x16x32_bf16 v[8:11], v[152:155], v[216:219], 0
	v_mfma_f32_16x16x32_bf16 v[4:7], v[160:163], v[216:219], 0
	v_mfma_f32_16x16x32_bf16 v[56:59], v[156:159], v[184:187], v[56:59]
	v_mfma_f32_16x16x32_bf16 v[52:55], v[164:167], v[184:187], v[52:55]
	v_mfma_f32_16x16x32_bf16 v[40:43], v[156:159], v[192:195], v[40:43]
	v_mfma_f32_16x16x32_bf16 v[36:39], v[164:167], v[192:195], v[36:39]
	v_mfma_f32_16x16x32_bf16 v[24:27], v[156:159], v[212:215], v[24:27]
	v_mfma_f32_16x16x32_bf16 v[20:23], v[164:167], v[212:215], v[20:23]
	v_mfma_f32_16x16x32_bf16 v[8:11], v[156:159], v[220:223], v[8:11]
	v_mfma_f32_16x16x32_bf16 v[4:7], v[164:167], v[220:223], v[4:7]
	s_barrier
	s_add_i32 s80, 0, 0x18000
	v_add_u32_e32 v2, s80, v203
	s_add_i32 s81, 0, 0x1c000
	ds_read_b128 v[104:107], v2
	ds_read_b128 v[124:127], v2 offset:1024
	ds_read_b128 v[128:131], v2 offset:2048
	ds_read_b128 v[148:151], v2 offset:3072
	v_add_u32_e32 v2, s81, v203
	ds_read_b128 v[152:155], v2
	ds_read_b128 v[156:159], v2 offset:1024
	ds_read_b128 v[160:163], v2 offset:2048
	ds_read_b128 v[164:167], v2 offset:3072
	s_add_u32 s4, s4, 0x40000
	s_addc_u32 s5, s5, 0
	s_mov_b32 m0, s58
	v_lshl_add_u64 v[208:209], s[4:5], 0, v[174:175]
	ds_read_b128 v[180:183], v210 offset:32768
	ds_read_b128 v[184:187], v210 offset:33792
	ds_read_b128 v[188:191], v210 offset:34816
	ds_read_b128 v[192:195], v210 offset:35840
	ds_read_b128 v[204:207], v210 offset:36864
	ds_read_b128 v[212:215], v210 offset:37888
	ds_read_b128 v[216:219], v210 offset:38912
	ds_read_b128 v[220:223], v210 offset:39936
	global_load_lds_dwordx4 v[208:209], off
	v_lshl_add_u64 v[208:209], s[4:5], 0, v[170:171]
	s_mov_b32 m0, s59
	s_nop 0
	global_load_lds_dwordx4 v[208:209], off
	s_waitcnt vmcnt(8)
	s_waitcnt lgkmcnt(0)
	s_barrier
	v_mfma_f32_16x16x32_bf16 v[144:147], v[104:107], v[180:183], v[144:147]
	v_mfma_f32_16x16x32_bf16 v[140:143], v[128:131], v[180:183], v[140:143]
	v_mfma_f32_16x16x32_bf16 v[120:123], v[104:107], v[188:191], v[120:123]
	v_mfma_f32_16x16x32_bf16 v[116:119], v[128:131], v[188:191], v[116:119]
	v_mfma_f32_16x16x32_bf16 v[96:99], v[104:107], v[204:207], v[96:99]
	v_mfma_f32_16x16x32_bf16 v[92:95], v[128:131], v[204:207], v[92:95]
	v_mfma_f32_16x16x32_bf16 v[80:83], v[104:107], v[216:219], v[80:83]
	v_mfma_f32_16x16x32_bf16 v[76:79], v[128:131], v[216:219], v[76:79]
	v_mfma_f32_16x16x32_bf16 v[144:147], v[124:127], v[184:187], v[144:147]
	v_mfma_f32_16x16x32_bf16 v[140:143], v[148:151], v[184:187], v[140:143]
	v_mfma_f32_16x16x32_bf16 v[120:123], v[124:127], v[192:195], v[120:123]
	v_mfma_f32_16x16x32_bf16 v[116:119], v[148:151], v[192:195], v[116:119]
	v_mfma_f32_16x16x32_bf16 v[96:99], v[124:127], v[212:215], v[96:99]
	v_mfma_f32_16x16x32_bf16 v[92:95], v[148:151], v[212:215], v[92:95]
	v_mfma_f32_16x16x32_bf16 v[80:83], v[124:127], v[220:223], v[80:83]
	v_mfma_f32_16x16x32_bf16 v[76:79], v[148:151], v[220:223], v[76:79]
	v_mfma_f32_16x16x32_bf16 v[136:139], v[152:155], v[180:183], v[136:139]
	v_mfma_f32_16x16x32_bf16 v[132:135], v[160:163], v[180:183], v[132:135]
	v_mfma_f32_16x16x32_bf16 v[112:115], v[152:155], v[188:191], v[112:115]
	v_mfma_f32_16x16x32_bf16 v[108:111], v[160:163], v[188:191], v[108:111]
	v_mfma_f32_16x16x32_bf16 v[88:91], v[152:155], v[204:207], v[88:91]
	v_mfma_f32_16x16x32_bf16 v[84:87], v[160:163], v[204:207], v[84:87]
	v_mfma_f32_16x16x32_bf16 v[72:75], v[152:155], v[216:219], v[72:75]
	v_mfma_f32_16x16x32_bf16 v[68:71], v[160:163], v[216:219], v[68:71]
	v_mfma_f32_16x16x32_bf16 v[136:139], v[156:159], v[184:187], v[136:139]
	v_mfma_f32_16x16x32_bf16 v[132:135], v[164:167], v[184:187], v[132:135]
	v_mfma_f32_16x16x32_bf16 v[112:115], v[156:159], v[192:195], v[112:115]
	v_mfma_f32_16x16x32_bf16 v[108:111], v[164:167], v[192:195], v[108:111]
	v_mfma_f32_16x16x32_bf16 v[88:91], v[156:159], v[212:215], v[88:91]
	v_mfma_f32_16x16x32_bf16 v[84:87], v[164:167], v[212:215], v[84:87]
	v_mfma_f32_16x16x32_bf16 v[72:75], v[156:159], v[220:223], v[72:75]
	v_mfma_f32_16x16x32_bf16 v[68:71], v[164:167], v[220:223], v[68:71]
	s_barrier
	s_add_i32 s4, s80, s46
	v_lshl_add_u64 v[196:197], v[196:197], 0, s[34:35]
	s_mov_b32 m0, s4
	ds_read_b128 v[180:183], v210 offset:49152
	ds_read_b128 v[184:187], v210 offset:50176
	ds_read_b128 v[188:191], v210 offset:51200
	ds_read_b128 v[192:195], v210 offset:52224
	ds_read_b128 v[204:207], v210 offset:53248
	ds_read_b128 v[212:215], v210 offset:54272
	ds_read_b128 v[216:219], v210 offset:55296
	ds_read_b128 v[220:223], v210 offset:56320
	global_load_lds_dwordx4 v[196:197], off
	s_add_i32 m0, s4, 0x2000
	s_add_u32 s4, s48, 0x20080
	v_lshl_add_u64 v[196:197], v[198:199], 0, s[34:35]
	s_addc_u32 s5, s49, 0
	s_add_i32 s48, s81, s46
	global_load_lds_dwordx4 v[196:197], off
	v_lshl_add_u64 v[196:197], s[4:5], 0, v[172:173]
	s_mov_b32 m0, s48
	s_nop 0
	global_load_lds_dwordx4 v[196:197], off
	v_lshl_add_u64 v[196:197], s[4:5], 0, v[168:169]
	s_add_i32 m0, s48, 0x2000
	s_nop 0
	global_load_lds_dwordx4 v[196:197], off
	v_lshl_add_u64 v[196:197], s[44:45], 0, v[174:175]
	s_mov_b32 m0, s68
	s_nop 0
	global_load_lds_dwordx4 v[196:197], off
	v_lshl_add_u64 v[196:197], s[44:45], 0, v[170:171]
	s_mov_b32 m0, s69
	s_nop 0
	global_load_lds_dwordx4 v[196:197], off
	s_waitcnt vmcnt(8)
	s_waitcnt lgkmcnt(0)
	s_barrier
	v_mfma_f32_16x16x32_bf16 v[64:67], v[104:107], v[180:183], v[64:67]
	v_mfma_f32_16x16x32_bf16 v[60:63], v[128:131], v[180:183], v[60:63]
	v_mfma_f32_16x16x32_bf16 v[48:51], v[104:107], v[188:191], v[48:51]
	v_mfma_f32_16x16x32_bf16 v[44:47], v[128:131], v[188:191], v[44:47]
	v_mfma_f32_16x16x32_bf16 v[32:35], v[104:107], v[204:207], v[32:35]
	v_mfma_f32_16x16x32_bf16 v[28:31], v[128:131], v[204:207], v[28:31]
	v_mfma_f32_16x16x32_bf16 v[16:19], v[104:107], v[216:219], v[16:19]
	v_mfma_f32_16x16x32_bf16 v[12:15], v[128:131], v[216:219], v[12:15]
	v_mfma_f32_16x16x32_bf16 v[64:67], v[124:127], v[184:187], v[64:67]
	v_mfma_f32_16x16x32_bf16 v[60:63], v[148:151], v[184:187], v[60:63]
	v_mfma_f32_16x16x32_bf16 v[48:51], v[124:127], v[192:195], v[48:51]
	v_mfma_f32_16x16x32_bf16 v[44:47], v[148:151], v[192:195], v[44:47]
	v_mfma_f32_16x16x32_bf16 v[32:35], v[124:127], v[212:215], v[32:35]
	v_mfma_f32_16x16x32_bf16 v[28:31], v[148:151], v[212:215], v[28:31]
	v_mfma_f32_16x16x32_bf16 v[16:19], v[124:127], v[220:223], v[16:19]
	v_mfma_f32_16x16x32_bf16 v[12:15], v[148:151], v[220:223], v[12:15]
	v_mfma_f32_16x16x32_bf16 v[56:59], v[152:155], v[180:183], v[56:59]
	v_mfma_f32_16x16x32_bf16 v[52:55], v[160:163], v[180:183], v[52:55]
	v_mfma_f32_16x16x32_bf16 v[40:43], v[152:155], v[188:191], v[40:43]
	v_mfma_f32_16x16x32_bf16 v[36:39], v[160:163], v[188:191], v[36:39]
	v_mfma_f32_16x16x32_bf16 v[24:27], v[152:155], v[204:207], v[24:27]
	v_mfma_f32_16x16x32_bf16 v[20:23], v[160:163], v[204:207], v[20:23]
	v_mfma_f32_16x16x32_bf16 v[8:11], v[152:155], v[216:219], v[8:11]
	v_mfma_f32_16x16x32_bf16 v[4:7], v[160:163], v[216:219], v[4:7]
	v_mfma_f32_16x16x32_bf16 v[56:59], v[156:159], v[184:187], v[56:59]
	v_mfma_f32_16x16x32_bf16 v[52:55], v[164:167], v[184:187], v[52:55]
	v_mfma_f32_16x16x32_bf16 v[40:43], v[156:159], v[192:195], v[40:43]
	v_mfma_f32_16x16x32_bf16 v[36:39], v[164:167], v[192:195], v[36:39]
	v_mfma_f32_16x16x32_bf16 v[24:27], v[156:159], v[212:215], v[24:27]
	v_mfma_f32_16x16x32_bf16 v[20:23], v[164:167], v[212:215], v[20:23]
	v_mfma_f32_16x16x32_bf16 v[8:11], v[156:159], v[220:223], v[8:11]
	v_mfma_f32_16x16x32_bf16 v[4:7], v[164:167], v[220:223], v[4:7]
	s_barrier
	s_add_i32 s79, s79, 2
	s_add_u32 s42, s42, 0x100
	s_addc_u32 s43, s43, 0
	s_cmp_gt_u32 s79, 5
.LBB0_383:
	s_add_u32 s4, s40, s42
	s_addc_u32 s5, s41, s43
	s_add_u32 s80, s4, 0x100
	s_addc_u32 s81, s5, 0
	s_add_u32 s48, s77, s42
	s_addc_u32 s49, s78, s43
	s_add_u32 s4, s4, 0x180
	s_addc_u32 s5, s5, 0
	s_add_i32 s82, 0, 0x10000
	s_add_i32 s83, 0, 0x14000
	v_add_u32_e32 v2, s82, v203
	ds_read_b128 v[104:107], v2
	ds_read_b128 v[124:127], v2 offset:1024
	ds_read_b128 v[128:131], v2 offset:2048
	ds_read_b128 v[148:151], v2 offset:3072
	v_add_u32_e32 v2, s83, v203
	ds_read_b128 v[152:155], v2
	ds_read_b128 v[156:159], v2 offset:1024
	ds_read_b128 v[160:163], v2 offset:2048
	ds_read_b128 v[164:167], v2 offset:3072
	s_cmpk_eq_i32 s42, 0x300
	s_cselect_b32 s45, s76, s5
	s_cselect_b32 s44, s75, s4
	s_cselect_b32 s49, s11, s49
	s_cselect_b32 s48, s74, s48
	s_cselect_b32 s5, s51, s81
	s_cselect_b32 s4, s71, s80
	v_lshl_add_u64 v[196:197], v[100:101], 0, s[42:43]
	s_add_i32 m0, s47, 0xc000
	ds_read_b128 v[180:183], v210
	ds_read_b128 v[184:187], v210 offset:1024
	ds_read_b128 v[188:191], v210 offset:2048
	ds_read_b128 v[192:195], v210 offset:3072
	ds_read_b128 v[204:207], v210 offset:4096
	ds_read_b128 v[212:215], v210 offset:5120
	ds_read_b128 v[216:219], v210 offset:6144
	ds_read_b128 v[220:223], v210 offset:7168
	global_load_lds_dwordx4 v[196:197], off
	v_lshl_add_u64 v[196:197], v[102:103], 0, s[42:43]
	s_add_i32 m0, s47, 0xe000
	s_nop 0
	global_load_lds_dwordx4 v[196:197], off
	s_waitcnt vmcnt(8)
	s_waitcnt lgkmcnt(0)
	s_barrier
	v_mfma_f32_16x16x32_bf16 v[144:147], v[104:107], v[180:183], v[144:147]
	v_mfma_f32_16x16x32_bf16 v[140:143], v[128:131], v[180:183], v[140:143]
	v_mfma_f32_16x16x32_bf16 v[120:123], v[104:107], v[188:191], v[120:123]
	v_mfma_f32_16x16x32_bf16 v[116:119], v[128:131], v[188:191], v[116:119]
	v_mfma_f32_16x16x32_bf16 v[96:99], v[104:107], v[204:207], v[96:99]
	v_mfma_f32_16x16x32_bf16 v[92:95], v[128:131], v[204:207], v[92:95]
	v_mfma_f32_16x16x32_bf16 v[80:83], v[104:107], v[216:219], v[80:83]
	v_mfma_f32_16x16x32_bf16 v[76:79], v[128:131], v[216:219], v[76:79]
	v_mfma_f32_16x16x32_bf16 v[144:147], v[124:127], v[184:187], v[144:147]
	v_mfma_f32_16x16x32_bf16 v[140:143], v[148:151], v[184:187], v[140:143]
	v_mfma_f32_16x16x32_bf16 v[120:123], v[124:127], v[192:195], v[120:123]
	v_mfma_f32_16x16x32_bf16 v[116:119], v[148:151], v[192:195], v[116:119]
	v_mfma_f32_16x16x32_bf16 v[96:99], v[124:127], v[212:215], v[96:99]
	v_mfma_f32_16x16x32_bf16 v[92:95], v[148:151], v[212:215], v[92:95]
	v_mfma_f32_16x16x32_bf16 v[80:83], v[124:127], v[220:223], v[80:83]
	v_mfma_f32_16x16x32_bf16 v[76:79], v[148:151], v[220:223], v[76:79]
	v_mfma_f32_16x16x32_bf16 v[136:139], v[152:155], v[180:183], v[136:139]
	v_mfma_f32_16x16x32_bf16 v[132:135], v[160:163], v[180:183], v[132:135]
	v_mfma_f32_16x16x32_bf16 v[112:115], v[152:155], v[188:191], v[112:115]
	v_mfma_f32_16x16x32_bf16 v[108:111], v[160:163], v[188:191], v[108:111]
	v_mfma_f32_16x16x32_bf16 v[88:91], v[152:155], v[204:207], v[88:91]
	v_mfma_f32_16x16x32_bf16 v[84:87], v[160:163], v[204:207], v[84:87]
	v_mfma_f32_16x16x32_bf16 v[72:75], v[152:155], v[216:219], v[72:75]
	v_mfma_f32_16x16x32_bf16 v[68:71], v[160:163], v[216:219], v[68:71]
	v_mfma_f32_16x16x32_bf16 v[136:139], v[156:159], v[184:187], v[136:139]
	v_mfma_f32_16x16x32_bf16 v[132:135], v[164:167], v[184:187], v[132:135]
	v_mfma_f32_16x16x32_bf16 v[112:115], v[156:159], v[192:195], v[112:115]
	v_mfma_f32_16x16x32_bf16 v[108:111], v[164:167], v[192:195], v[108:111]
	v_mfma_f32_16x16x32_bf16 v[88:91], v[156:159], v[212:215], v[88:91]
	v_mfma_f32_16x16x32_bf16 v[84:87], v[164:167], v[212:215], v[84:87]
	v_mfma_f32_16x16x32_bf16 v[72:75], v[156:159], v[220:223], v[72:75]
	v_mfma_f32_16x16x32_bf16 v[68:71], v[164:167], v[220:223], v[68:71]
	s_barrier
	s_add_i32 s80, s82, s46
	v_lshl_add_u64 v[196:197], s[48:49], 0, v[172:173]
	s_mov_b32 m0, s80
	ds_read_b128 v[180:183], v210 offset:16384
	ds_read_b128 v[184:187], v210 offset:17408
	ds_read_b128 v[188:191], v210 offset:18432
	ds_read_b128 v[192:195], v210 offset:19456
	ds_read_b128 v[204:207], v210 offset:20480
	ds_read_b128 v[212:215], v210 offset:21504
	ds_read_b128 v[216:219], v210 offset:22528
	ds_read_b128 v[220:223], v210 offset:23552
	global_load_lds_dwordx4 v[196:197], off
	s_add_i32 m0, s80, 0x2000
	s_add_u32 s80, s48, 0x20000
	v_lshl_add_u64 v[198:199], s[48:49], 0, v[168:169]
	s_addc_u32 s81, s49, 0
	s_add_i32 s82, s83, s46
	global_load_lds_dwordx4 v[198:199], off
	v_lshl_add_u64 v[208:209], s[80:81], 0, v[172:173]
	s_mov_b32 m0, s82
	s_nop 0
	global_load_lds_dwordx4 v[208:209], off
	v_lshl_add_u64 v[208:209], s[80:81], 0, v[168:169]
	s_add_i32 m0, s82, 0x2000
	s_nop 0
	global_load_lds_dwordx4 v[208:209], off
	v_lshl_add_u64 v[208:209], s[4:5], 0, v[174:175]
	s_mov_b32 m0, s47
	s_nop 0
	global_load_lds_dwordx4 v[208:209], off
	v_lshl_add_u64 v[208:209], s[4:5], 0, v[170:171]
	s_mov_b32 m0, s56
	s_nop 0
	global_load_lds_dwordx4 v[208:209], off
	s_waitcnt vmcnt(8)
	s_waitcnt lgkmcnt(0)
	s_barrier
	v_mfma_f32_16x16x32_bf16 v[64:67], v[104:107], v[180:183], v[64:67]
	v_mfma_f32_16x16x32_bf16 v[60:63], v[128:131], v[180:183], v[60:63]
	v_mfma_f32_16x16x32_bf16 v[48:51], v[104:107], v[188:191], v[48:51]
	v_mfma_f32_16x16x32_bf16 v[44:47], v[128:131], v[188:191], v[44:47]
	v_mfma_f32_16x16x32_bf16 v[32:35], v[104:107], v[204:207], v[32:35]
	v_mfma_f32_16x16x32_bf16 v[28:31], v[128:131], v[204:207], v[28:31]
	v_mfma_f32_16x16x32_bf16 v[16:19], v[104:107], v[216:219], v[16:19]
	v_mfma_f32_16x16x32_bf16 v[12:15], v[128:131], v[216:219], v[12:15]
	v_mfma_f32_16x16x32_bf16 v[64:67], v[124:127], v[184:187], v[64:67]
	v_mfma_f32_16x16x32_bf16 v[60:63], v[148:151], v[184:187], v[60:63]
	v_mfma_f32_16x16x32_bf16 v[48:51], v[124:127], v[192:195], v[48:51]
	v_mfma_f32_16x16x32_bf16 v[44:47], v[148:151], v[192:195], v[44:47]
	v_mfma_f32_16x16x32_bf16 v[32:35], v[124:127], v[212:215], v[32:35]
	v_mfma_f32_16x16x32_bf16 v[28:31], v[148:151], v[212:215], v[28:31]
	v_mfma_f32_16x16x32_bf16 v[16:19], v[124:127], v[220:223], v[16:19]
	v_mfma_f32_16x16x32_bf16 v[12:15], v[148:151], v[220:223], v[12:15]
	v_mfma_f32_16x16x32_bf16 v[56:59], v[152:155], v[180:183], v[56:59]
	v_mfma_f32_16x16x32_bf16 v[52:55], v[160:163], v[180:183], v[52:55]
	v_mfma_f32_16x16x32_bf16 v[40:43], v[152:155], v[188:191], v[40:43]
	v_mfma_f32_16x16x32_bf16 v[36:39], v[160:163], v[188:191], v[36:39]
	v_mfma_f32_16x16x32_bf16 v[24:27], v[152:155], v[204:207], v[24:27]
	v_mfma_f32_16x16x32_bf16 v[20:23], v[160:163], v[204:207], v[20:23]
	v_mfma_f32_16x16x32_bf16 v[8:11], v[152:155], v[216:219], v[8:11]
	v_mfma_f32_16x16x32_bf16 v[4:7], v[160:163], v[216:219], v[4:7]
	v_mfma_f32_16x16x32_bf16 v[56:59], v[156:159], v[184:187], v[56:59]
	v_mfma_f32_16x16x32_bf16 v[52:55], v[164:167], v[184:187], v[52:55]
	v_mfma_f32_16x16x32_bf16 v[40:43], v[156:159], v[192:195], v[40:43]
	v_mfma_f32_16x16x32_bf16 v[36:39], v[164:167], v[192:195], v[36:39]
	v_mfma_f32_16x16x32_bf16 v[24:27], v[156:159], v[212:215], v[24:27]
	v_mfma_f32_16x16x32_bf16 v[20:23], v[164:167], v[212:215], v[20:23]
	v_mfma_f32_16x16x32_bf16 v[8:11], v[156:159], v[220:223], v[8:11]
	v_mfma_f32_16x16x32_bf16 v[4:7], v[164:167], v[220:223], v[4:7]
	s_barrier
	s_add_i32 s80, 0, 0x18000
	v_add_u32_e32 v2, s80, v203
	s_add_i32 s81, 0, 0x1c000
	ds_read_b128 v[104:107], v2
	ds_read_b128 v[124:127], v2 offset:1024
	ds_read_b128 v[128:131], v2 offset:2048
	ds_read_b128 v[148:151], v2 offset:3072
	v_add_u32_e32 v2, s81, v203
	ds_read_b128 v[152:155], v2
	ds_read_b128 v[156:159], v2 offset:1024
	ds_read_b128 v[160:163], v2 offset:2048
	ds_read_b128 v[164:167], v2 offset:3072
	s_add_u32 s4, s4, 0x40000
	s_addc_u32 s5, s5, 0
	s_mov_b32 m0, s58
	v_lshl_add_u64 v[208:209], s[4:5], 0, v[174:175]
	ds_read_b128 v[180:183], v210 offset:32768
	ds_read_b128 v[184:187], v210 offset:33792
	ds_read_b128 v[188:191], v210 offset:34816
	ds_read_b128 v[192:195], v210 offset:35840
	ds_read_b128 v[204:207], v210 offset:36864
	ds_read_b128 v[212:215], v210 offset:37888
	ds_read_b128 v[216:219], v210 offset:38912
	ds_read_b128 v[220:223], v210 offset:39936
	global_load_lds_dwordx4 v[208:209], off
	v_lshl_add_u64 v[208:209], s[4:5], 0, v[170:171]
	s_mov_b32 m0, s59
	s_nop 0
	global_load_lds_dwordx4 v[208:209], off
	s_waitcnt vmcnt(8)
	s_waitcnt lgkmcnt(0)
	s_barrier
	v_mfma_f32_16x16x32_bf16 v[144:147], v[104:107], v[180:183], v[144:147]
	v_mfma_f32_16x16x32_bf16 v[140:143], v[128:131], v[180:183], v[140:143]
	v_mfma_f32_16x16x32_bf16 v[120:123], v[104:107], v[188:191], v[120:123]
	v_mfma_f32_16x16x32_bf16 v[116:119], v[128:131], v[188:191], v[116:119]
	v_mfma_f32_16x16x32_bf16 v[96:99], v[104:107], v[204:207], v[96:99]
	v_mfma_f32_16x16x32_bf16 v[92:95], v[128:131], v[204:207], v[92:95]
	v_mfma_f32_16x16x32_bf16 v[80:83], v[104:107], v[216:219], v[80:83]
	v_mfma_f32_16x16x32_bf16 v[76:79], v[128:131], v[216:219], v[76:79]
	v_mfma_f32_16x16x32_bf16 v[144:147], v[124:127], v[184:187], v[144:147]
	v_mfma_f32_16x16x32_bf16 v[140:143], v[148:151], v[184:187], v[140:143]
	v_mfma_f32_16x16x32_bf16 v[120:123], v[124:127], v[192:195], v[120:123]
	v_mfma_f32_16x16x32_bf16 v[116:119], v[148:151], v[192:195], v[116:119]
	v_mfma_f32_16x16x32_bf16 v[96:99], v[124:127], v[212:215], v[96:99]
	v_mfma_f32_16x16x32_bf16 v[92:95], v[148:151], v[212:215], v[92:95]
	v_mfma_f32_16x16x32_bf16 v[80:83], v[124:127], v[220:223], v[80:83]
	v_mfma_f32_16x16x32_bf16 v[76:79], v[148:151], v[220:223], v[76:79]
	v_mfma_f32_16x16x32_bf16 v[136:139], v[152:155], v[180:183], v[136:139]
	v_mfma_f32_16x16x32_bf16 v[132:135], v[160:163], v[180:183], v[132:135]
	v_mfma_f32_16x16x32_bf16 v[112:115], v[152:155], v[188:191], v[112:115]
	v_mfma_f32_16x16x32_bf16 v[108:111], v[160:163], v[188:191], v[108:111]
	v_mfma_f32_16x16x32_bf16 v[88:91], v[152:155], v[204:207], v[88:91]
	v_mfma_f32_16x16x32_bf16 v[84:87], v[160:163], v[204:207], v[84:87]
	v_mfma_f32_16x16x32_bf16 v[72:75], v[152:155], v[216:219], v[72:75]
	v_mfma_f32_16x16x32_bf16 v[68:71], v[160:163], v[216:219], v[68:71]
	v_mfma_f32_16x16x32_bf16 v[136:139], v[156:159], v[184:187], v[136:139]
	v_mfma_f32_16x16x32_bf16 v[132:135], v[164:167], v[184:187], v[132:135]
	v_mfma_f32_16x16x32_bf16 v[112:115], v[156:159], v[192:195], v[112:115]
	v_mfma_f32_16x16x32_bf16 v[108:111], v[164:167], v[192:195], v[108:111]
	v_mfma_f32_16x16x32_bf16 v[88:91], v[156:159], v[212:215], v[88:91]
	v_mfma_f32_16x16x32_bf16 v[84:87], v[164:167], v[212:215], v[84:87]
	v_mfma_f32_16x16x32_bf16 v[72:75], v[156:159], v[220:223], v[72:75]
	v_mfma_f32_16x16x32_bf16 v[68:71], v[164:167], v[220:223], v[68:71]
	s_barrier
	s_add_i32 s4, s80, s46
	v_lshl_add_u64 v[196:197], v[196:197], 0, s[34:35]
	s_mov_b32 m0, s4
	ds_read_b128 v[180:183], v210 offset:49152
	ds_read_b128 v[184:187], v210 offset:50176
	ds_read_b128 v[188:191], v210 offset:51200
	ds_read_b128 v[192:195], v210 offset:52224
	ds_read_b128 v[204:207], v210 offset:53248
	ds_read_b128 v[212:215], v210 offset:54272
	ds_read_b128 v[216:219], v210 offset:55296
	ds_read_b128 v[220:223], v210 offset:56320
	global_load_lds_dwordx4 v[196:197], off
	s_add_i32 m0, s4, 0x2000
	s_add_u32 s4, s48, 0x20080
	v_lshl_add_u64 v[196:197], v[198:199], 0, s[34:35]
	s_addc_u32 s5, s49, 0
	s_add_i32 s48, s81, s46
	global_load_lds_dwordx4 v[196:197], off
	v_lshl_add_u64 v[196:197], s[4:5], 0, v[172:173]
	s_mov_b32 m0, s48
	s_nop 0
	global_load_lds_dwordx4 v[196:197], off
	v_lshl_add_u64 v[196:197], s[4:5], 0, v[168:169]
	s_add_i32 m0, s48, 0x2000
	s_nop 0
	global_load_lds_dwordx4 v[196:197], off
	v_lshl_add_u64 v[196:197], s[44:45], 0, v[174:175]
	s_mov_b32 m0, s68
	s_nop 0
	global_load_lds_dwordx4 v[196:197], off
	v_lshl_add_u64 v[196:197], s[44:45], 0, v[170:171]
	s_mov_b32 m0, s69
	s_nop 0
	global_load_lds_dwordx4 v[196:197], off
	s_waitcnt vmcnt(8)
	s_waitcnt lgkmcnt(0)
	s_barrier
	v_mfma_f32_16x16x32_bf16 v[64:67], v[104:107], v[180:183], v[64:67]
	v_mfma_f32_16x16x32_bf16 v[60:63], v[128:131], v[180:183], v[60:63]
	v_mfma_f32_16x16x32_bf16 v[48:51], v[104:107], v[188:191], v[48:51]
	v_mfma_f32_16x16x32_bf16 v[44:47], v[128:131], v[188:191], v[44:47]
	v_mfma_f32_16x16x32_bf16 v[32:35], v[104:107], v[204:207], v[32:35]
	v_mfma_f32_16x16x32_bf16 v[28:31], v[128:131], v[204:207], v[28:31]
	v_mfma_f32_16x16x32_bf16 v[16:19], v[104:107], v[216:219], v[16:19]
	v_mfma_f32_16x16x32_bf16 v[12:15], v[128:131], v[216:219], v[12:15]
	v_mfma_f32_16x16x32_bf16 v[64:67], v[124:127], v[184:187], v[64:67]
	v_mfma_f32_16x16x32_bf16 v[60:63], v[148:151], v[184:187], v[60:63]
	v_mfma_f32_16x16x32_bf16 v[48:51], v[124:127], v[192:195], v[48:51]
	v_mfma_f32_16x16x32_bf16 v[44:47], v[148:151], v[192:195], v[44:47]
	v_mfma_f32_16x16x32_bf16 v[32:35], v[124:127], v[212:215], v[32:35]
	v_mfma_f32_16x16x32_bf16 v[28:31], v[148:151], v[212:215], v[28:31]
	v_mfma_f32_16x16x32_bf16 v[16:19], v[124:127], v[220:223], v[16:19]
	v_mfma_f32_16x16x32_bf16 v[12:15], v[148:151], v[220:223], v[12:15]
	v_mfma_f32_16x16x32_bf16 v[56:59], v[152:155], v[180:183], v[56:59]
	v_mfma_f32_16x16x32_bf16 v[52:55], v[160:163], v[180:183], v[52:55]
	v_mfma_f32_16x16x32_bf16 v[40:43], v[152:155], v[188:191], v[40:43]
	v_mfma_f32_16x16x32_bf16 v[36:39], v[160:163], v[188:191], v[36:39]
	v_mfma_f32_16x16x32_bf16 v[24:27], v[152:155], v[204:207], v[24:27]
	v_mfma_f32_16x16x32_bf16 v[20:23], v[160:163], v[204:207], v[20:23]
	v_mfma_f32_16x16x32_bf16 v[8:11], v[152:155], v[216:219], v[8:11]
	v_mfma_f32_16x16x32_bf16 v[4:7], v[160:163], v[216:219], v[4:7]
	v_mfma_f32_16x16x32_bf16 v[56:59], v[156:159], v[184:187], v[56:59]
	v_mfma_f32_16x16x32_bf16 v[52:55], v[164:167], v[184:187], v[52:55]
	v_mfma_f32_16x16x32_bf16 v[40:43], v[156:159], v[192:195], v[40:43]
	v_mfma_f32_16x16x32_bf16 v[36:39], v[164:167], v[192:195], v[36:39]
	v_mfma_f32_16x16x32_bf16 v[24:27], v[156:159], v[212:215], v[24:27]
	v_mfma_f32_16x16x32_bf16 v[20:23], v[164:167], v[212:215], v[20:23]
	v_mfma_f32_16x16x32_bf16 v[8:11], v[156:159], v[220:223], v[8:11]
	v_mfma_f32_16x16x32_bf16 v[4:7], v[164:167], v[220:223], v[4:7]
	s_barrier
	s_add_i32 s79, s79, 2
	s_add_u32 s42, s42, 0x100
	s_addc_u32 s43, s43, 0
	s_cmp_gt_u32 s79, 5
	s_cbranch_scc0 .LBB0_383
	s_and_b64 vcc, exec, s[72:73]
	s_cbranch_vccz .LBB0_386
	s_barrier

.LBB0_1043:
	s_ashr_i32 s41, s40, 31
	s_lshl_b64 s[4:5], s[40:41], 19
	s_add_u32 s42, s6, s4
	s_addc_u32 s43, s7, s5
	s_and_b64 s[4:5], s[38:39], exec
	s_cselect_b32 s41, s43, s49
	s_cselect_b32 s65, s42, s48
	s_ashr_i32 s37, s36, 31
	s_lshl_b64 s[4:5], s[36:37], 19
	s_add_u32 s44, s8, s4
	s_addc_u32 s45, s9, s5
	s_and_b64 s[4:5], s[38:39], exec
	s_cselect_b32 s37, s45, s51
	s_cselect_b32 s68, s44, s50
	s_add_u32 s69, s65, 0x80
	s_addc_u32 s70, s41, 0
	s_add_u32 s4, s48, 0x40080
	s_addc_u32 s5, s49, 0
	s_add_u32 s71, s50, 0x100
	v_lshl_add_u64 v[140:141], s[4:5], 0, v[136:137]
	v_lshl_add_u64 v[142:143], s[4:5], 0, v[138:139]
	s_addc_u32 s72, s51, 0
	s_mov_b32 s73, -2
	s_mov_b64 s[50:51], 0
	s_waitcnt vmcnt(0)
	s_add_u32 s4, s48, s50
	s_addc_u32 s5, s49, s51
	s_add_u32 s74, s4, 0x100
	s_addc_u32 s75, s5, 0
	s_add_u32 s52, s71, s50
	s_addc_u32 s53, s72, s51
	s_add_u32 s4, s4, 0x180
	s_addc_u32 s5, s5, 0
	s_add_i32 s76, 0, 0x10000
	s_add_i32 s77, 0, 0x14000
	v_add_u32_e32 v2, s76, v203
	ds_read_b128 v[144:147], v2
	ds_read_b128 v[148:151], v2 offset:1024
	ds_read_b128 v[152:155], v2 offset:2048
	ds_read_b128 v[156:159], v2 offset:3072
	v_add_u32_e32 v2, s77, v203
	ds_read_b128 v[160:163], v2
	ds_read_b128 v[164:167], v2 offset:1024
	ds_read_b128 v[168:171], v2 offset:2048
	ds_read_b128 v[172:175], v2 offset:3072
	s_cmpk_eq_i32 s50, 0x700
	s_cselect_b32 s13, s70, s5
	s_cselect_b32 s12, s69, s4
	s_cselect_b32 s53, s37, s53
	s_cselect_b32 s52, s68, s52
	s_cselect_b32 s5, s41, s75
	s_cselect_b32 s4, s65, s74
	v_lshl_add_u64 v[212:213], v[140:141], 0, s[50:51]
	s_add_i32 m0, s17, 0xc000
	ds_read_b128 v[176:179], v224
	ds_read_b128 v[180:183], v224 offset:1024
	ds_read_b128 v[184:187], v224 offset:2048
	ds_read_b128 v[188:191], v224 offset:3072
	ds_read_b128 v[192:195], v224 offset:4096
	ds_read_b128 v[196:199], v224 offset:5120
	ds_read_b128 v[204:207], v224 offset:6144
	ds_read_b128 v[208:211], v224 offset:7168
	global_load_lds_dwordx4 v[212:213], off
	v_lshl_add_u64 v[212:213], v[142:143], 0, s[50:51]
	s_add_i32 m0, s17, 0xe000
	s_nop 0
	global_load_lds_dwordx4 v[212:213], off
	s_waitcnt vmcnt(8)
	s_waitcnt lgkmcnt(0)
	s_barrier
	v_mfma_f32_16x16x32_bf16 v[128:131], v[144:147], v[176:179], 0
	v_mfma_f32_16x16x32_bf16 v[124:127], v[152:155], v[176:179], 0
	v_mfma_f32_16x16x32_bf16 v[112:115], v[144:147], v[184:187], 0
	v_mfma_f32_16x16x32_bf16 v[108:111], v[152:155], v[184:187], 0
	v_mfma_f32_16x16x32_bf16 v[96:99], v[144:147], v[192:195], 0
	v_mfma_f32_16x16x32_bf16 v[92:95], v[152:155], v[192:195], 0
	v_mfma_f32_16x16x32_bf16 v[80:83], v[144:147], v[204:207], 0
	v_mfma_f32_16x16x32_bf16 v[76:79], v[152:155], v[204:207], 0
	v_mfma_f32_16x16x32_bf16 v[128:131], v[148:151], v[180:183], v[128:131]
	v_mfma_f32_16x16x32_bf16 v[124:127], v[156:159], v[180:183], v[124:127]
	v_mfma_f32_16x16x32_bf16 v[112:115], v[148:151], v[188:191], v[112:115]
	v_mfma_f32_16x16x32_bf16 v[108:111], v[156:159], v[188:191], v[108:111]
	v_mfma_f32_16x16x32_bf16 v[96:99], v[148:151], v[196:199], v[96:99]
	v_mfma_f32_16x16x32_bf16 v[92:95], v[156:159], v[196:199], v[92:95]
	v_mfma_f32_16x16x32_bf16 v[80:83], v[148:151], v[208:211], v[80:83]
	v_mfma_f32_16x16x32_bf16 v[76:79], v[156:159], v[208:211], v[76:79]
	v_mfma_f32_16x16x32_bf16 v[120:123], v[160:163], v[176:179], 0
	v_mfma_f32_16x16x32_bf16 v[116:119], v[168:171], v[176:179], 0
	v_mfma_f32_16x16x32_bf16 v[104:107], v[160:163], v[184:187], 0
	v_mfma_f32_16x16x32_bf16 v[100:103], v[168:171], v[184:187], 0
	v_mfma_f32_16x16x32_bf16 v[88:91], v[160:163], v[192:195], 0
	v_mfma_f32_16x16x32_bf16 v[84:87], v[168:171], v[192:195], 0
	v_mfma_f32_16x16x32_bf16 v[72:75], v[160:163], v[204:207], 0
	v_mfma_f32_16x16x32_bf16 v[68:71], v[168:171], v[204:207], 0
	v_mfma_f32_16x16x32_bf16 v[120:123], v[164:167], v[180:183], v[120:123]
	v_mfma_f32_16x16x32_bf16 v[116:119], v[172:175], v[180:183], v[116:119]
	v_mfma_f32_16x16x32_bf16 v[104:107], v[164:167], v[188:191], v[104:107]
	v_mfma_f32_16x16x32_bf16 v[100:103], v[172:175], v[188:191], v[100:103]
	v_mfma_f32_16x16x32_bf16 v[88:91], v[164:167], v[196:199], v[88:91]
	v_mfma_f32_16x16x32_bf16 v[84:87], v[172:175], v[196:199], v[84:87]
	v_mfma_f32_16x16x32_bf16 v[72:75], v[164:167], v[208:211], v[72:75]
	v_mfma_f32_16x16x32_bf16 v[68:71], v[172:175], v[208:211], v[68:71]
	s_barrier
	s_add_i32 s74, s76, s16
	v_lshl_add_u64 v[212:213], s[52:53], 0, v[134:135]
	s_mov_b32 m0, s74
	ds_read_b128 v[176:179], v224 offset:16384
	ds_read_b128 v[180:183], v224 offset:17408
	ds_read_b128 v[184:187], v224 offset:18432
	ds_read_b128 v[188:191], v224 offset:19456
	ds_read_b128 v[192:195], v224 offset:20480
	ds_read_b128 v[196:199], v224 offset:21504
	ds_read_b128 v[204:207], v224 offset:22528
	ds_read_b128 v[208:211], v224 offset:23552
	global_load_lds_dwordx4 v[212:213], off
	s_add_i32 m0, s74, 0x2000
	s_add_u32 s74, s52, 0x40000
	v_lshl_add_u64 v[214:215], s[52:53], 0, v[132:133]
	s_addc_u32 s75, s53, 0
	s_add_i32 s76, s77, s16
	global_load_lds_dwordx4 v[214:215], off
	v_lshl_add_u64 v[216:217], s[74:75], 0, v[134:135]
	s_mov_b32 m0, s76
	s_nop 0
	global_load_lds_dwordx4 v[216:217], off
	v_lshl_add_u64 v[216:217], s[74:75], 0, v[132:133]
	s_add_i32 m0, s76, 0x2000
	s_nop 0
	global_load_lds_dwordx4 v[216:217], off
	v_lshl_add_u64 v[216:217], s[4:5], 0, v[134:135]
	s_mov_b32 m0, s17
	s_nop 0
	global_load_lds_dwordx4 v[216:217], off
	v_lshl_add_u64 v[216:217], s[4:5], 0, v[132:133]
	s_mov_b32 m0, s46
	s_nop 0
	global_load_lds_dwordx4 v[216:217], off
	s_waitcnt vmcnt(8)
	s_waitcnt lgkmcnt(0)
	s_barrier
	v_mfma_f32_16x16x32_bf16 v[64:67], v[144:147], v[176:179], 0
	v_mfma_f32_16x16x32_bf16 v[60:63], v[152:155], v[176:179], 0
	v_mfma_f32_16x16x32_bf16 v[48:51], v[144:147], v[184:187], 0
	v_mfma_f32_16x16x32_bf16 v[44:47], v[152:155], v[184:187], 0
	v_mfma_f32_16x16x32_bf16 v[32:35], v[144:147], v[192:195], 0
	v_mfma_f32_16x16x32_bf16 v[28:31], v[152:155], v[192:195], 0
	v_mfma_f32_16x16x32_bf16 v[16:19], v[144:147], v[204:207], 0
	v_mfma_f32_16x16x32_bf16 v[12:15], v[152:155], v[204:207], 0
	v_mfma_f32_16x16x32_bf16 v[64:67], v[148:151], v[180:183], v[64:67]
	v_mfma_f32_16x16x32_bf16 v[60:63], v[156:159], v[180:183], v[60:63]
	v_mfma_f32_16x16x32_bf16 v[48:51], v[148:151], v[188:191], v[48:51]
	v_mfma_f32_16x16x32_bf16 v[44:47], v[156:159], v[188:191], v[44:47]
	v_mfma_f32_16x16x32_bf16 v[32:35], v[148:151], v[196:199], v[32:35]
	v_mfma_f32_16x16x32_bf16 v[28:31], v[156:159], v[196:199], v[28:31]
	v_mfma_f32_16x16x32_bf16 v[16:19], v[148:151], v[208:211], v[16:19]
	v_mfma_f32_16x16x32_bf16 v[12:15], v[156:159], v[208:211], v[12:15]
	v_mfma_f32_16x16x32_bf16 v[56:59], v[160:163], v[176:179], 0
	v_mfma_f32_16x16x32_bf16 v[52:55], v[168:171], v[176:179], 0
	v_mfma_f32_16x16x32_bf16 v[40:43], v[160:163], v[184:187], 0
	v_mfma_f32_16x16x32_bf16 v[36:39], v[168:171], v[184:187], 0
	v_mfma_f32_16x16x32_bf16 v[24:27], v[160:163], v[192:195], 0
	v_mfma_f32_16x16x32_bf16 v[20:23], v[168:171], v[192:195], 0
	v_mfma_f32_16x16x32_bf16 v[8:11], v[160:163], v[204:207], 0
	v_mfma_f32_16x16x32_bf16 v[4:7], v[168:171], v[204:207], 0
	v_mfma_f32_16x16x32_bf16 v[56:59], v[164:167], v[180:183], v[56:59]
	v_mfma_f32_16x16x32_bf16 v[52:55], v[172:175], v[180:183], v[52:55]
	v_mfma_f32_16x16x32_bf16 v[40:43], v[164:167], v[188:191], v[40:43]
	v_mfma_f32_16x16x32_bf16 v[36:39], v[172:175], v[188:191], v[36:39]
	v_mfma_f32_16x16x32_bf16 v[24:27], v[164:167], v[196:199], v[24:27]
	v_mfma_f32_16x16x32_bf16 v[20:23], v[172:175], v[196:199], v[20:23]
	v_mfma_f32_16x16x32_bf16 v[8:11], v[164:167], v[208:211], v[8:11]
	v_mfma_f32_16x16x32_bf16 v[4:7], v[172:175], v[208:211], v[4:7]
	s_barrier
	s_add_i32 s74, 0, 0x18000
	v_add_u32_e32 v2, s74, v203
	s_add_i32 s75, 0, 0x1c000
	ds_read_b128 v[144:147], v2
	ds_read_b128 v[148:151], v2 offset:1024
	ds_read_b128 v[152:155], v2 offset:2048
	ds_read_b128 v[156:159], v2 offset:3072
	v_add_u32_e32 v2, s75, v203
	ds_read_b128 v[160:163], v2
	ds_read_b128 v[164:167], v2 offset:1024
	ds_read_b128 v[168:171], v2 offset:2048
	ds_read_b128 v[172:175], v2 offset:3072
	s_add_u32 s4, s4, 0x40000
	s_addc_u32 s5, s5, 0
	s_mov_b32 m0, s47
	v_lshl_add_u64 v[216:217], s[4:5], 0, v[134:135]
	ds_read_b128 v[176:179], v224 offset:32768
	ds_read_b128 v[180:183], v224 offset:33792
	ds_read_b128 v[184:187], v224 offset:34816
	ds_read_b128 v[188:191], v224 offset:35840
	ds_read_b128 v[192:195], v224 offset:36864
	ds_read_b128 v[196:199], v224 offset:37888
	ds_read_b128 v[204:207], v224 offset:38912
	ds_read_b128 v[208:211], v224 offset:39936
	global_load_lds_dwordx4 v[216:217], off
	v_lshl_add_u64 v[216:217], s[4:5], 0, v[132:133]
	s_mov_b32 m0, s56
	s_nop 0
	global_load_lds_dwordx4 v[216:217], off
	s_waitcnt vmcnt(8)
	s_waitcnt lgkmcnt(0)
	s_barrier
	v_mfma_f32_16x16x32_bf16 v[128:131], v[144:147], v[176:179], v[128:131]
	v_mfma_f32_16x16x32_bf16 v[124:127], v[152:155], v[176:179], v[124:127]
	v_mfma_f32_16x16x32_bf16 v[112:115], v[144:147], v[184:187], v[112:115]
	v_mfma_f32_16x16x32_bf16 v[108:111], v[152:155], v[184:187], v[108:111]
	v_mfma_f32_16x16x32_bf16 v[96:99], v[144:147], v[192:195], v[96:99]
	v_mfma_f32_16x16x32_bf16 v[92:95], v[152:155], v[192:195], v[92:95]
	v_mfma_f32_16x16x32_bf16 v[80:83], v[144:147], v[204:207], v[80:83]
	v_mfma_f32_16x16x32_bf16 v[76:79], v[152:155], v[204:207], v[76:79]
	v_mfma_f32_16x16x32_bf16 v[128:131], v[148:151], v[180:183], v[128:131]
	v_mfma_f32_16x16x32_bf16 v[124:127], v[156:159], v[180:183], v[124:127]
	v_mfma_f32_16x16x32_bf16 v[112:115], v[148:151], v[188:191], v[112:115]
	v_mfma_f32_16x16x32_bf16 v[108:111], v[156:159], v[188:191], v[108:111]
	v_mfma_f32_16x16x32_bf16 v[96:99], v[148:151], v[196:199], v[96:99]
	v_mfma_f32_16x16x32_bf16 v[92:95], v[156:159], v[196:199], v[92:95]
	v_mfma_f32_16x16x32_bf16 v[80:83], v[148:151], v[208:211], v[80:83]
	v_mfma_f32_16x16x32_bf16 v[76:79], v[156:159], v[208:211], v[76:79]
	v_mfma_f32_16x16x32_bf16 v[120:123], v[160:163], v[176:179], v[120:123]
	v_mfma_f32_16x16x32_bf16 v[116:119], v[168:171], v[176:179], v[116:119]
	v_mfma_f32_16x16x32_bf16 v[104:107], v[160:163], v[184:187], v[104:107]
	v_mfma_f32_16x16x32_bf16 v[100:103], v[168:171], v[184:187], v[100:103]
	v_mfma_f32_16x16x32_bf16 v[88:91], v[160:163], v[192:195], v[88:91]
	v_mfma_f32_16x16x32_bf16 v[84:87], v[168:171], v[192:195], v[84:87]
	v_mfma_f32_16x16x32_bf16 v[72:75], v[160:163], v[204:207], v[72:75]
	v_mfma_f32_16x16x32_bf16 v[68:71], v[168:171], v[204:207], v[68:71]
	v_mfma_f32_16x16x32_bf16 v[120:123], v[164:167], v[180:183], v[120:123]
	v_mfma_f32_16x16x32_bf16 v[116:119], v[172:175], v[180:183], v[116:119]
	v_mfma_f32_16x16x32_bf16 v[104:107], v[164:167], v[188:191], v[104:107]
	v_mfma_f32_16x16x32_bf16 v[100:103], v[172:175], v[188:191], v[100:103]
	v_mfma_f32_16x16x32_bf16 v[88:91], v[164:167], v[196:199], v[88:91]
	v_mfma_f32_16x16x32_bf16 v[84:87], v[172:175], v[196:199], v[84:87]
	v_mfma_f32_16x16x32_bf16 v[72:75], v[164:167], v[208:211], v[72:75]
	v_mfma_f32_16x16x32_bf16 v[68:71], v[172:175], v[208:211], v[68:71]
	s_barrier
	s_add_i32 s4, s74, s16
	v_lshl_add_u64 v[212:213], v[212:213], 0, s[34:35]
	s_mov_b32 m0, s4
	ds_read_b128 v[176:179], v224 offset:49152
	ds_read_b128 v[180:183], v224 offset:50176
	ds_read_b128 v[184:187], v224 offset:51200
	ds_read_b128 v[188:191], v224 offset:52224
	ds_read_b128 v[192:195], v224 offset:53248
	ds_read_b128 v[196:199], v224 offset:54272
	ds_read_b128 v[204:207], v224 offset:55296
	ds_read_b128 v[208:211], v224 offset:56320
	global_load_lds_dwordx4 v[212:213], off
	s_add_i32 m0, s4, 0x2000
	s_add_u32 s4, s52, 0x40080
	v_lshl_add_u64 v[212:213], v[214:215], 0, s[34:35]
	s_addc_u32 s5, s53, 0
	s_add_i32 s52, s75, s16
	global_load_lds_dwordx4 v[212:213], off
	v_lshl_add_u64 v[212:213], s[4:5], 0, v[134:135]
	s_mov_b32 m0, s52
	s_nop 0
	global_load_lds_dwordx4 v[212:213], off
	v_lshl_add_u64 v[212:213], s[4:5], 0, v[132:133]
	s_add_i32 m0, s52, 0x2000
	s_nop 0
	global_load_lds_dwordx4 v[212:213], off
	v_lshl_add_u64 v[212:213], s[12:13], 0, v[134:135]
	s_mov_b32 m0, s59
	s_nop 0
	global_load_lds_dwordx4 v[212:213], off
	v_lshl_add_u64 v[212:213], s[12:13], 0, v[132:133]
	s_mov_b32 m0, s60
	s_nop 0
	global_load_lds_dwordx4 v[212:213], off
	s_waitcnt vmcnt(8)
	s_waitcnt lgkmcnt(0)
	s_barrier
	v_mfma_f32_16x16x32_bf16 v[64:67], v[144:147], v[176:179], v[64:67]
	v_mfma_f32_16x16x32_bf16 v[60:63], v[152:155], v[176:179], v[60:63]
	v_mfma_f32_16x16x32_bf16 v[48:51], v[144:147], v[184:187], v[48:51]
	v_mfma_f32_16x16x32_bf16 v[44:47], v[152:155], v[184:187], v[44:47]
	v_mfma_f32_16x16x32_bf16 v[32:35], v[144:147], v[192:195], v[32:35]
	v_mfma_f32_16x16x32_bf16 v[28:31], v[152:155], v[192:195], v[28:31]
	v_mfma_f32_16x16x32_bf16 v[16:19], v[144:147], v[204:207], v[16:19]
	v_mfma_f32_16x16x32_bf16 v[12:15], v[152:155], v[204:207], v[12:15]
	v_mfma_f32_16x16x32_bf16 v[64:67], v[148:151], v[180:183], v[64:67]
	v_mfma_f32_16x16x32_bf16 v[60:63], v[156:159], v[180:183], v[60:63]
	v_mfma_f32_16x16x32_bf16 v[48:51], v[148:151], v[188:191], v[48:51]
	v_mfma_f32_16x16x32_bf16 v[44:47], v[156:159], v[188:191], v[44:47]
	v_mfma_f32_16x16x32_bf16 v[32:35], v[148:151], v[196:199], v[32:35]
	v_mfma_f32_16x16x32_bf16 v[28:31], v[156:159], v[196:199], v[28:31]
	v_mfma_f32_16x16x32_bf16 v[16:19], v[148:151], v[208:211], v[16:19]
	v_mfma_f32_16x16x32_bf16 v[12:15], v[156:159], v[208:211], v[12:15]
	v_mfma_f32_16x16x32_bf16 v[56:59], v[160:163], v[176:179], v[56:59]
	v_mfma_f32_16x16x32_bf16 v[52:55], v[168:171], v[176:179], v[52:55]
	v_mfma_f32_16x16x32_bf16 v[40:43], v[160:163], v[184:187], v[40:43]
	v_mfma_f32_16x16x32_bf16 v[36:39], v[168:171], v[184:187], v[36:39]
	v_mfma_f32_16x16x32_bf16 v[24:27], v[160:163], v[192:195], v[24:27]
	v_mfma_f32_16x16x32_bf16 v[20:23], v[168:171], v[192:195], v[20:23]
	v_mfma_f32_16x16x32_bf16 v[8:11], v[160:163], v[204:207], v[8:11]
	v_mfma_f32_16x16x32_bf16 v[4:7], v[168:171], v[204:207], v[4:7]
	v_mfma_f32_16x16x32_bf16 v[56:59], v[164:167], v[180:183], v[56:59]
	v_mfma_f32_16x16x32_bf16 v[52:55], v[172:175], v[180:183], v[52:55]
	v_mfma_f32_16x16x32_bf16 v[40:43], v[164:167], v[188:191], v[40:43]
	v_mfma_f32_16x16x32_bf16 v[36:39], v[172:175], v[188:191], v[36:39]
	v_mfma_f32_16x16x32_bf16 v[24:27], v[164:167], v[196:199], v[24:27]
	v_mfma_f32_16x16x32_bf16 v[20:23], v[172:175], v[196:199], v[20:23]
	v_mfma_f32_16x16x32_bf16 v[8:11], v[164:167], v[208:211], v[8:11]
	v_mfma_f32_16x16x32_bf16 v[4:7], v[172:175], v[208:211], v[4:7]
	s_barrier
	s_add_i32 s73, s73, 2
	s_add_u32 s50, s50, 0x100
	s_addc_u32 s51, s51, 0
	s_cmp_gt_u32 s73, 13
.LBB0_1044:
	s_add_u32 s4, s48, s50
	s_addc_u32 s5, s49, s51
	s_add_u32 s74, s4, 0x100
	s_addc_u32 s75, s5, 0
	s_add_u32 s52, s71, s50
	s_addc_u32 s53, s72, s51
	s_add_u32 s4, s4, 0x180
	s_addc_u32 s5, s5, 0
	s_add_i32 s76, 0, 0x10000
	s_add_i32 s77, 0, 0x14000
	v_add_u32_e32 v2, s76, v203
	ds_read_b128 v[144:147], v2
	ds_read_b128 v[148:151], v2 offset:1024
	ds_read_b128 v[152:155], v2 offset:2048
	ds_read_b128 v[156:159], v2 offset:3072
	v_add_u32_e32 v2, s77, v203
	ds_read_b128 v[160:163], v2
	ds_read_b128 v[164:167], v2 offset:1024
	ds_read_b128 v[168:171], v2 offset:2048
	ds_read_b128 v[172:175], v2 offset:3072
	s_cmpk_eq_i32 s50, 0x700
	s_cselect_b32 s13, s70, s5
	s_cselect_b32 s12, s69, s4
	s_cselect_b32 s53, s37, s53
	s_cselect_b32 s52, s68, s52
	s_cselect_b32 s5, s41, s75
	s_cselect_b32 s4, s65, s74
	v_lshl_add_u64 v[212:213], v[140:141], 0, s[50:51]
	s_add_i32 m0, s17, 0xc000
	ds_read_b128 v[176:179], v224
	ds_read_b128 v[180:183], v224 offset:1024
	ds_read_b128 v[184:187], v224 offset:2048
	ds_read_b128 v[188:191], v224 offset:3072
	ds_read_b128 v[192:195], v224 offset:4096
	ds_read_b128 v[196:199], v224 offset:5120
	ds_read_b128 v[204:207], v224 offset:6144
	ds_read_b128 v[208:211], v224 offset:7168
	global_load_lds_dwordx4 v[212:213], off
	v_lshl_add_u64 v[212:213], v[142:143], 0, s[50:51]
	s_add_i32 m0, s17, 0xe000
	s_nop 0
	global_load_lds_dwordx4 v[212:213], off
	s_waitcnt vmcnt(8)
	s_waitcnt lgkmcnt(0)
	s_barrier
	v_mfma_f32_16x16x32_bf16 v[128:131], v[144:147], v[176:179], v[128:131]
	v_mfma_f32_16x16x32_bf16 v[124:127], v[152:155], v[176:179], v[124:127]
	v_mfma_f32_16x16x32_bf16 v[112:115], v[144:147], v[184:187], v[112:115]
	v_mfma_f32_16x16x32_bf16 v[108:111], v[152:155], v[184:187], v[108:111]
	v_mfma_f32_16x16x32_bf16 v[96:99], v[144:147], v[192:195], v[96:99]
	v_mfma_f32_16x16x32_bf16 v[92:95], v[152:155], v[192:195], v[92:95]
	v_mfma_f32_16x16x32_bf16 v[80:83], v[144:147], v[204:207], v[80:83]
	v_mfma_f32_16x16x32_bf16 v[76:79], v[152:155], v[204:207], v[76:79]
	v_mfma_f32_16x16x32_bf16 v[128:131], v[148:151], v[180:183], v[128:131]
	v_mfma_f32_16x16x32_bf16 v[124:127], v[156:159], v[180:183], v[124:127]
	v_mfma_f32_16x16x32_bf16 v[112:115], v[148:151], v[188:191], v[112:115]
	v_mfma_f32_16x16x32_bf16 v[108:111], v[156:159], v[188:191], v[108:111]
	v_mfma_f32_16x16x32_bf16 v[96:99], v[148:151], v[196:199], v[96:99]
	v_mfma_f32_16x16x32_bf16 v[92:95], v[156:159], v[196:199], v[92:95]
	v_mfma_f32_16x16x32_bf16 v[80:83], v[148:151], v[208:211], v[80:83]
	v_mfma_f32_16x16x32_bf16 v[76:79], v[156:159], v[208:211], v[76:79]
	v_mfma_f32_16x16x32_bf16 v[120:123], v[160:163], v[176:179], v[120:123]
	v_mfma_f32_16x16x32_bf16 v[116:119], v[168:171], v[176:179], v[116:119]
	v_mfma_f32_16x16x32_bf16 v[104:107], v[160:163], v[184:187], v[104:107]
	v_mfma_f32_16x16x32_bf16 v[100:103], v[168:171], v[184:187], v[100:103]
	v_mfma_f32_16x16x32_bf16 v[88:91], v[160:163], v[192:195], v[88:91]
	v_mfma_f32_16x16x32_bf16 v[84:87], v[168:171], v[192:195], v[84:87]
	v_mfma_f32_16x16x32_bf16 v[72:75], v[160:163], v[204:207], v[72:75]
	v_mfma_f32_16x16x32_bf16 v[68:71], v[168:171], v[204:207], v[68:71]
	v_mfma_f32_16x16x32_bf16 v[120:123], v[164:167], v[180:183], v[120:123]
	v_mfma_f32_16x16x32_bf16 v[116:119], v[172:175], v[180:183], v[116:119]
	v_mfma_f32_16x16x32_bf16 v[104:107], v[164:167], v[188:191], v[104:107]
	v_mfma_f32_16x16x32_bf16 v[100:103], v[172:175], v[188:191], v[100:103]
	v_mfma_f32_16x16x32_bf16 v[88:91], v[164:167], v[196:199], v[88:91]
	v_mfma_f32_16x16x32_bf16 v[84:87], v[172:175], v[196:199], v[84:87]
	v_mfma_f32_16x16x32_bf16 v[72:75], v[164:167], v[208:211], v[72:75]
	v_mfma_f32_16x16x32_bf16 v[68:71], v[172:175], v[208:211], v[68:71]
	s_barrier
	s_add_i32 s74, s76, s16
	v_lshl_add_u64 v[212:213], s[52:53], 0, v[134:135]
	s_mov_b32 m0, s74
	ds_read_b128 v[176:179], v224 offset:16384
	ds_read_b128 v[180:183], v224 offset:17408
	ds_read_b128 v[184:187], v224 offset:18432
	ds_read_b128 v[188:191], v224 offset:19456
	ds_read_b128 v[192:195], v224 offset:20480
	ds_read_b128 v[196:199], v224 offset:21504
	ds_read_b128 v[204:207], v224 offset:22528
	ds_read_b128 v[208:211], v224 offset:23552
	global_load_lds_dwordx4 v[212:213], off
	s_add_i32 m0, s74, 0x2000
	s_add_u32 s74, s52, 0x40000
	v_lshl_add_u64 v[214:215], s[52:53], 0, v[132:133]
	s_addc_u32 s75, s53, 0
	s_add_i32 s76, s77, s16
	global_load_lds_dwordx4 v[214:215], off
	v_lshl_add_u64 v[216:217], s[74:75], 0, v[134:135]
	s_mov_b32 m0, s76
	s_nop 0
	global_load_lds_dwordx4 v[216:217], off
	v_lshl_add_u64 v[216:217], s[74:75], 0, v[132:133]
	s_add_i32 m0, s76, 0x2000
	s_nop 0
	global_load_lds_dwordx4 v[216:217], off
	v_lshl_add_u64 v[216:217], s[4:5], 0, v[134:135]
	s_mov_b32 m0, s17
	s_nop 0
	global_load_lds_dwordx4 v[216:217], off
	v_lshl_add_u64 v[216:217], s[4:5], 0, v[132:133]
	s_mov_b32 m0, s46
	s_nop 0
	global_load_lds_dwordx4 v[216:217], off
	s_waitcnt vmcnt(8)
	s_waitcnt lgkmcnt(0)
	s_barrier
	v_mfma_f32_16x16x32_bf16 v[64:67], v[144:147], v[176:179], v[64:67]
	v_mfma_f32_16x16x32_bf16 v[60:63], v[152:155], v[176:179], v[60:63]
	v_mfma_f32_16x16x32_bf16 v[48:51], v[144:147], v[184:187], v[48:51]
	v_mfma_f32_16x16x32_bf16 v[44:47], v[152:155], v[184:187], v[44:47]
	v_mfma_f32_16x16x32_bf16 v[32:35], v[144:147], v[192:195], v[32:35]
	v_mfma_f32_16x16x32_bf16 v[28:31], v[152:155], v[192:195], v[28:31]
	v_mfma_f32_16x16x32_bf16 v[16:19], v[144:147], v[204:207], v[16:19]
	v_mfma_f32_16x16x32_bf16 v[12:15], v[152:155], v[204:207], v[12:15]
	v_mfma_f32_16x16x32_bf16 v[64:67], v[148:151], v[180:183], v[64:67]
	v_mfma_f32_16x16x32_bf16 v[60:63], v[156:159], v[180:183], v[60:63]
	v_mfma_f32_16x16x32_bf16 v[48:51], v[148:151], v[188:191], v[48:51]
	v_mfma_f32_16x16x32_bf16 v[44:47], v[156:159], v[188:191], v[44:47]
	v_mfma_f32_16x16x32_bf16 v[32:35], v[148:151], v[196:199], v[32:35]
	v_mfma_f32_16x16x32_bf16 v[28:31], v[156:159], v[196:199], v[28:31]
	v_mfma_f32_16x16x32_bf16 v[16:19], v[148:151], v[208:211], v[16:19]
	v_mfma_f32_16x16x32_bf16 v[12:15], v[156:159], v[208:211], v[12:15]
	v_mfma_f32_16x16x32_bf16 v[56:59], v[160:163], v[176:179], v[56:59]
	v_mfma_f32_16x16x32_bf16 v[52:55], v[168:171], v[176:179], v[52:55]
	v_mfma_f32_16x16x32_bf16 v[40:43], v[160:163], v[184:187], v[40:43]
	v_mfma_f32_16x16x32_bf16 v[36:39], v[168:171], v[184:187], v[36:39]
	v_mfma_f32_16x16x32_bf16 v[24:27], v[160:163], v[192:195], v[24:27]
	v_mfma_f32_16x16x32_bf16 v[20:23], v[168:171], v[192:195], v[20:23]
	v_mfma_f32_16x16x32_bf16 v[8:11], v[160:163], v[204:207], v[8:11]
	v_mfma_f32_16x16x32_bf16 v[4:7], v[168:171], v[204:207], v[4:7]
	v_mfma_f32_16x16x32_bf16 v[56:59], v[164:167], v[180:183], v[56:59]
	v_mfma_f32_16x16x32_bf16 v[52:55], v[172:175], v[180:183], v[52:55]
	v_mfma_f32_16x16x32_bf16 v[40:43], v[164:167], v[188:191], v[40:43]
	v_mfma_f32_16x16x32_bf16 v[36:39], v[172:175], v[188:191], v[36:39]
	v_mfma_f32_16x16x32_bf16 v[24:27], v[164:167], v[196:199], v[24:27]
	v_mfma_f32_16x16x32_bf16 v[20:23], v[172:175], v[196:199], v[20:23]
	v_mfma_f32_16x16x32_bf16 v[8:11], v[164:167], v[208:211], v[8:11]
	v_mfma_f32_16x16x32_bf16 v[4:7], v[172:175], v[208:211], v[4:7]
	s_barrier
	s_add_i32 s74, 0, 0x18000
	v_add_u32_e32 v2, s74, v203
	s_add_i32 s75, 0, 0x1c000
	ds_read_b128 v[144:147], v2
	ds_read_b128 v[148:151], v2 offset:1024
	ds_read_b128 v[152:155], v2 offset:2048
	ds_read_b128 v[156:159], v2 offset:3072
	v_add_u32_e32 v2, s75, v203
	ds_read_b128 v[160:163], v2
	ds_read_b128 v[164:167], v2 offset:1024
	ds_read_b128 v[168:171], v2 offset:2048
	ds_read_b128 v[172:175], v2 offset:3072
	s_add_u32 s4, s4, 0x40000
	s_addc_u32 s5, s5, 0
	s_mov_b32 m0, s47
	v_lshl_add_u64 v[216:217], s[4:5], 0, v[134:135]
	ds_read_b128 v[176:179], v224 offset:32768
	ds_read_b128 v[180:183], v224 offset:33792
	ds_read_b128 v[184:187], v224 offset:34816
	ds_read_b128 v[188:191], v224 offset:35840
	ds_read_b128 v[192:195], v224 offset:36864
	ds_read_b128 v[196:199], v224 offset:37888
	ds_read_b128 v[204:207], v224 offset:38912
	ds_read_b128 v[208:211], v224 offset:39936
	global_load_lds_dwordx4 v[216:217], off
	v_lshl_add_u64 v[216:217], s[4:5], 0, v[132:133]
	s_mov_b32 m0, s56
	s_nop 0
	global_load_lds_dwordx4 v[216:217], off
	s_waitcnt vmcnt(8)
	s_waitcnt lgkmcnt(0)
	s_barrier
	v_mfma_f32_16x16x32_bf16 v[128:131], v[144:147], v[176:179], v[128:131]
	v_mfma_f32_16x16x32_bf16 v[124:127], v[152:155], v[176:179], v[124:127]
	v_mfma_f32_16x16x32_bf16 v[112:115], v[144:147], v[184:187], v[112:115]
	v_mfma_f32_16x16x32_bf16 v[108:111], v[152:155], v[184:187], v[108:111]
	v_mfma_f32_16x16x32_bf16 v[96:99], v[144:147], v[192:195], v[96:99]
	v_mfma_f32_16x16x32_bf16 v[92:95], v[152:155], v[192:195], v[92:95]
	v_mfma_f32_16x16x32_bf16 v[80:83], v[144:147], v[204:207], v[80:83]
	v_mfma_f32_16x16x32_bf16 v[76:79], v[152:155], v[204:207], v[76:79]
	v_mfma_f32_16x16x32_bf16 v[128:131], v[148:151], v[180:183], v[128:131]
	v_mfma_f32_16x16x32_bf16 v[124:127], v[156:159], v[180:183], v[124:127]
	v_mfma_f32_16x16x32_bf16 v[112:115], v[148:151], v[188:191], v[112:115]
	v_mfma_f32_16x16x32_bf16 v[108:111], v[156:159], v[188:191], v[108:111]
	v_mfma_f32_16x16x32_bf16 v[96:99], v[148:151], v[196:199], v[96:99]
	v_mfma_f32_16x16x32_bf16 v[92:95], v[156:159], v[196:199], v[92:95]
	v_mfma_f32_16x16x32_bf16 v[80:83], v[148:151], v[208:211], v[80:83]
	v_mfma_f32_16x16x32_bf16 v[76:79], v[156:159], v[208:211], v[76:79]
	v_mfma_f32_16x16x32_bf16 v[120:123], v[160:163], v[176:179], v[120:123]
	v_mfma_f32_16x16x32_bf16 v[116:119], v[168:171], v[176:179], v[116:119]
	v_mfma_f32_16x16x32_bf16 v[104:107], v[160:163], v[184:187], v[104:107]
	v_mfma_f32_16x16x32_bf16 v[100:103], v[168:171], v[184:187], v[100:103]
	v_mfma_f32_16x16x32_bf16 v[88:91], v[160:163], v[192:195], v[88:91]
	v_mfma_f32_16x16x32_bf16 v[84:87], v[168:171], v[192:195], v[84:87]
	v_mfma_f32_16x16x32_bf16 v[72:75], v[160:163], v[204:207], v[72:75]
	v_mfma_f32_16x16x32_bf16 v[68:71], v[168:171], v[204:207], v[68:71]
	v_mfma_f32_16x16x32_bf16 v[120:123], v[164:167], v[180:183], v[120:123]
	v_mfma_f32_16x16x32_bf16 v[116:119], v[172:175], v[180:183], v[116:119]
	v_mfma_f32_16x16x32_bf16 v[104:107], v[164:167], v[188:191], v[104:107]
	v_mfma_f32_16x16x32_bf16 v[100:103], v[172:175], v[188:191], v[100:103]
	v_mfma_f32_16x16x32_bf16 v[88:91], v[164:167], v[196:199], v[88:91]
	v_mfma_f32_16x16x32_bf16 v[84:87], v[172:175], v[196:199], v[84:87]
	v_mfma_f32_16x16x32_bf16 v[72:75], v[164:167], v[208:211], v[72:75]
	v_mfma_f32_16x16x32_bf16 v[68:71], v[172:175], v[208:211], v[68:71]
	s_barrier
	s_add_i32 s4, s74, s16
	v_lshl_add_u64 v[212:213], v[212:213], 0, s[34:35]
	s_mov_b32 m0, s4
	ds_read_b128 v[176:179], v224 offset:49152
	ds_read_b128 v[180:183], v224 offset:50176
	ds_read_b128 v[184:187], v224 offset:51200
	ds_read_b128 v[188:191], v224 offset:52224
	ds_read_b128 v[192:195], v224 offset:53248
	ds_read_b128 v[196:199], v224 offset:54272
	ds_read_b128 v[204:207], v224 offset:55296
	ds_read_b128 v[208:211], v224 offset:56320
	global_load_lds_dwordx4 v[212:213], off
	s_add_i32 m0, s4, 0x2000
	s_add_u32 s4, s52, 0x40080
	v_lshl_add_u64 v[212:213], v[214:215], 0, s[34:35]
	s_addc_u32 s5, s53, 0
	s_add_i32 s52, s75, s16
	global_load_lds_dwordx4 v[212:213], off
	v_lshl_add_u64 v[212:213], s[4:5], 0, v[134:135]
	s_mov_b32 m0, s52
	s_nop 0
	global_load_lds_dwordx4 v[212:213], off
	v_lshl_add_u64 v[212:213], s[4:5], 0, v[132:133]
	s_add_i32 m0, s52, 0x2000
	s_nop 0
	global_load_lds_dwordx4 v[212:213], off
	v_lshl_add_u64 v[212:213], s[12:13], 0, v[134:135]
	s_mov_b32 m0, s59
	s_nop 0
	global_load_lds_dwordx4 v[212:213], off
	v_lshl_add_u64 v[212:213], s[12:13], 0, v[132:133]
	s_mov_b32 m0, s60
	s_nop 0
	global_load_lds_dwordx4 v[212:213], off
	s_waitcnt vmcnt(8)
	s_waitcnt lgkmcnt(0)
	s_barrier
	v_mfma_f32_16x16x32_bf16 v[64:67], v[144:147], v[176:179], v[64:67]
	v_mfma_f32_16x16x32_bf16 v[60:63], v[152:155], v[176:179], v[60:63]
	v_mfma_f32_16x16x32_bf16 v[48:51], v[144:147], v[184:187], v[48:51]
	v_mfma_f32_16x16x32_bf16 v[44:47], v[152:155], v[184:187], v[44:47]
	v_mfma_f32_16x16x32_bf16 v[32:35], v[144:147], v[192:195], v[32:35]
	v_mfma_f32_16x16x32_bf16 v[28:31], v[152:155], v[192:195], v[28:31]
	v_mfma_f32_16x16x32_bf16 v[16:19], v[144:147], v[204:207], v[16:19]
	v_mfma_f32_16x16x32_bf16 v[12:15], v[152:155], v[204:207], v[12:15]
	v_mfma_f32_16x16x32_bf16 v[64:67], v[148:151], v[180:183], v[64:67]
	v_mfma_f32_16x16x32_bf16 v[60:63], v[156:159], v[180:183], v[60:63]
	v_mfma_f32_16x16x32_bf16 v[48:51], v[148:151], v[188:191], v[48:51]
	v_mfma_f32_16x16x32_bf16 v[44:47], v[156:159], v[188:191], v[44:47]
	v_mfma_f32_16x16x32_bf16 v[32:35], v[148:151], v[196:199], v[32:35]
	v_mfma_f32_16x16x32_bf16 v[28:31], v[156:159], v[196:199], v[28:31]
	v_mfma_f32_16x16x32_bf16 v[16:19], v[148:151], v[208:211], v[16:19]
	v_mfma_f32_16x16x32_bf16 v[12:15], v[156:159], v[208:211], v[12:15]
	v_mfma_f32_16x16x32_bf16 v[56:59], v[160:163], v[176:179], v[56:59]
	v_mfma_f32_16x16x32_bf16 v[52:55], v[168:171], v[176:179], v[52:55]
	v_mfma_f32_16x16x32_bf16 v[40:43], v[160:163], v[184:187], v[40:43]
	v_mfma_f32_16x16x32_bf16 v[36:39], v[168:171], v[184:187], v[36:39]
	v_mfma_f32_16x16x32_bf16 v[24:27], v[160:163], v[192:195], v[24:27]
	v_mfma_f32_16x16x32_bf16 v[20:23], v[168:171], v[192:195], v[20:23]
	v_mfma_f32_16x16x32_bf16 v[8:11], v[160:163], v[204:207], v[8:11]
	v_mfma_f32_16x16x32_bf16 v[4:7], v[168:171], v[204:207], v[4:7]
	v_mfma_f32_16x16x32_bf16 v[56:59], v[164:167], v[180:183], v[56:59]
	v_mfma_f32_16x16x32_bf16 v[52:55], v[172:175], v[180:183], v[52:55]
	v_mfma_f32_16x16x32_bf16 v[40:43], v[164:167], v[188:191], v[40:43]
	v_mfma_f32_16x16x32_bf16 v[36:39], v[172:175], v[188:191], v[36:39]
	v_mfma_f32_16x16x32_bf16 v[24:27], v[164:167], v[196:199], v[24:27]
	v_mfma_f32_16x16x32_bf16 v[20:23], v[172:175], v[196:199], v[20:23]
	v_mfma_f32_16x16x32_bf16 v[8:11], v[164:167], v[208:211], v[8:11]
	v_mfma_f32_16x16x32_bf16 v[4:7], v[172:175], v[208:211], v[4:7]
	s_barrier
	s_add_i32 s73, s73, 2
	s_add_u32 s50, s50, 0x100
	s_addc_u32 s51, s51, 0
	s_cmp_gt_u32 s73, 13
	s_cbranch_scc0 .LBB0_1044
	s_and_b64 vcc, exec, s[22:23]
	s_cbranch_vccz .LBB0_1047
	s_barrier

.LBB0_1117:
	s_ashr_i32 s37, s36, 31
	s_lshl_b64 s[4:5], s[36:37], 19
	s_add_u32 s40, s6, s4
	s_addc_u32 s41, s7, s5
	s_and_b64 s[4:5], s[38:39], exec
	s_cselect_b32 s37, s41, s45
	s_cselect_b32 s64, s40, s44
	s_ashr_i32 s23, s22, 31
	s_lshl_b64 s[4:5], s[22:23], 19
	s_add_u32 s42, s8, s4
	s_addc_u32 s43, s9, s5
	s_and_b64 s[4:5], s[38:39], exec
	s_cselect_b32 s23, s43, s49
	s_cselect_b32 s65, s42, s48
	s_add_u32 s68, s64, 0x80
	s_addc_u32 s69, s37, 0
	s_add_u32 s70, s48, 0x100
	s_addc_u32 s71, s49, 0
	s_add_u32 s4, s44, 0x40080
	s_addc_u32 s5, s45, 0
	v_lshl_add_u64 v[108:109], s[4:5], 0, v[210:211]
	v_lshl_add_u64 v[110:111], s[4:5], 0, v[212:213]
	s_mov_b32 s72, -2
	s_mov_b64 s[48:49], 0
	s_waitcnt lgkmcnt(0)
	s_waitcnt vmcnt(0)
	s_add_u32 s4, s44, s48
	s_addc_u32 s5, s45, s49
	s_add_u32 s73, s4, 0x100
	s_addc_u32 s74, s5, 0
	s_add_u32 s50, s70, s48
	s_addc_u32 s51, s71, s49
	s_add_u32 s4, s4, 0x180
	s_addc_u32 s5, s5, 0
	s_add_i32 s75, 0, 0x10000
	s_add_i32 s76, 0, 0x14000
	v_add_u32_e32 v148, s75, v203
	v_add_u32_e32 v164, s76, v203
	ds_read_b128 v[116:119], v148
	ds_read_b128 v[128:131], v148 offset:1024
	ds_read_b128 v[136:139], v148 offset:2048
	ds_read_b128 v[148:151], v148 offset:3072
	ds_read_b128 v[152:155], v164
	ds_read_b128 v[156:159], v164 offset:1024
	ds_read_b128 v[160:163], v164 offset:2048
	ds_read_b128 v[164:167], v164 offset:3072
	s_cmpk_eq_i32 s48, 0x700
	s_cselect_b32 s13, s69, s5
	s_cselect_b32 s12, s68, s4
	s_cselect_b32 s51, s23, s51
	s_cselect_b32 s50, s65, s50
	s_cselect_b32 s5, s37, s74
	s_cselect_b32 s4, s64, s73
	v_lshl_add_u64 v[214:215], v[108:109], 0, s[48:49]
	s_add_i32 m0, s17, 0xc000
	ds_read_b128 v[168:171], v236
	ds_read_b128 v[172:175], v236 offset:1024
	ds_read_b128 v[176:179], v236 offset:2048
	ds_read_b128 v[180:183], v236 offset:3072
	ds_read_b128 v[184:187], v236 offset:4096
	ds_read_b128 v[188:191], v236 offset:5120
	ds_read_b128 v[192:195], v236 offset:6144
	ds_read_b128 v[196:199], v236 offset:7168
	global_load_lds_dwordx4 v[214:215], off
	v_lshl_add_u64 v[214:215], v[110:111], 0, s[48:49]
	s_add_i32 m0, s17, 0xe000
	s_nop 0
	global_load_lds_dwordx4 v[214:215], off
	s_waitcnt vmcnt(8)
	s_waitcnt lgkmcnt(0)
	s_barrier
	v_mfma_f32_16x16x32_bf16 v[144:147], v[116:119], v[168:171], 0
	v_mfma_f32_16x16x32_bf16 v[140:143], v[136:139], v[168:171], 0
	v_mfma_f32_16x16x32_bf16 v[120:123], v[116:119], v[176:179], 0
	v_mfma_f32_16x16x32_bf16 v[112:115], v[136:139], v[176:179], 0
	v_mfma_f32_16x16x32_bf16 v[96:99], v[116:119], v[184:187], 0
	v_mfma_f32_16x16x32_bf16 v[92:95], v[136:139], v[184:187], 0
	v_mfma_f32_16x16x32_bf16 v[80:83], v[116:119], v[192:195], 0
	v_mfma_f32_16x16x32_bf16 v[76:79], v[136:139], v[192:195], 0
	v_mfma_f32_16x16x32_bf16 v[144:147], v[128:131], v[172:175], v[144:147]
	v_mfma_f32_16x16x32_bf16 v[140:143], v[148:151], v[172:175], v[140:143]
	v_mfma_f32_16x16x32_bf16 v[120:123], v[128:131], v[180:183], v[120:123]
	v_mfma_f32_16x16x32_bf16 v[112:115], v[148:151], v[180:183], v[112:115]
	v_mfma_f32_16x16x32_bf16 v[96:99], v[128:131], v[188:191], v[96:99]
	v_mfma_f32_16x16x32_bf16 v[92:95], v[148:151], v[188:191], v[92:95]
	v_mfma_f32_16x16x32_bf16 v[80:83], v[128:131], v[196:199], v[80:83]
	v_mfma_f32_16x16x32_bf16 v[76:79], v[148:151], v[196:199], v[76:79]
	v_mfma_f32_16x16x32_bf16 v[132:135], v[152:155], v[168:171], 0
	v_mfma_f32_16x16x32_bf16 v[124:127], v[160:163], v[168:171], 0
	v_mfma_f32_16x16x32_bf16 v[104:107], v[152:155], v[176:179], 0
	v_mfma_f32_16x16x32_bf16 v[100:103], v[160:163], v[176:179], 0
	v_mfma_f32_16x16x32_bf16 v[88:91], v[152:155], v[184:187], 0
	v_mfma_f32_16x16x32_bf16 v[84:87], v[160:163], v[184:187], 0
	v_mfma_f32_16x16x32_bf16 v[72:75], v[152:155], v[192:195], 0
	v_mfma_f32_16x16x32_bf16 v[68:71], v[160:163], v[192:195], 0
	v_mfma_f32_16x16x32_bf16 v[132:135], v[156:159], v[172:175], v[132:135]
	v_mfma_f32_16x16x32_bf16 v[124:127], v[164:167], v[172:175], v[124:127]
	v_mfma_f32_16x16x32_bf16 v[104:107], v[156:159], v[180:183], v[104:107]
	v_mfma_f32_16x16x32_bf16 v[100:103], v[164:167], v[180:183], v[100:103]
	v_mfma_f32_16x16x32_bf16 v[88:91], v[156:159], v[188:191], v[88:91]
	v_mfma_f32_16x16x32_bf16 v[84:87], v[164:167], v[188:191], v[84:87]
	v_mfma_f32_16x16x32_bf16 v[72:75], v[156:159], v[196:199], v[72:75]
	v_mfma_f32_16x16x32_bf16 v[68:71], v[164:167], v[196:199], v[68:71]
	s_barrier
	s_add_i32 s73, s75, s16
	v_lshl_add_u64 v[214:215], s[50:51], 0, v[2:3]
	s_mov_b32 m0, s73
	ds_read_b128 v[168:171], v236 offset:16384
	ds_read_b128 v[172:175], v236 offset:17408
	ds_read_b128 v[176:179], v236 offset:18432
	ds_read_b128 v[180:183], v236 offset:19456
	ds_read_b128 v[184:187], v236 offset:20480
	ds_read_b128 v[188:191], v236 offset:21504
	ds_read_b128 v[192:195], v236 offset:22528
	ds_read_b128 v[196:199], v236 offset:23552
	global_load_lds_dwordx4 v[214:215], off
	s_add_i32 m0, s73, 0x2000
	s_add_u32 s74, s50, 0x40000
	v_lshl_add_u64 v[216:217], s[50:51], 0, v[204:205]
	s_addc_u32 s75, s51, 0
	s_add_i32 s73, s76, s16
	global_load_lds_dwordx4 v[216:217], off
	v_lshl_add_u64 v[218:219], s[74:75], 0, v[2:3]
	s_mov_b32 m0, s73
	s_nop 0
	global_load_lds_dwordx4 v[218:219], off
	v_lshl_add_u64 v[218:219], s[74:75], 0, v[204:205]
	s_add_i32 m0, s73, 0x2000
	s_nop 0
	global_load_lds_dwordx4 v[218:219], off
	v_lshl_add_u64 v[218:219], s[4:5], 0, v[208:209]
	s_mov_b32 m0, s17
	s_nop 0
	global_load_lds_dwordx4 v[218:219], off
	v_lshl_add_u64 v[218:219], s[4:5], 0, v[206:207]
	s_mov_b32 m0, s46
	s_nop 0
	global_load_lds_dwordx4 v[218:219], off
	s_waitcnt vmcnt(8)
	s_waitcnt lgkmcnt(0)
	s_barrier
	v_mfma_f32_16x16x32_bf16 v[64:67], v[116:119], v[168:171], 0
	v_mfma_f32_16x16x32_bf16 v[60:63], v[136:139], v[168:171], 0
	v_mfma_f32_16x16x32_bf16 v[48:51], v[116:119], v[176:179], 0
	v_mfma_f32_16x16x32_bf16 v[44:47], v[136:139], v[176:179], 0
	v_mfma_f32_16x16x32_bf16 v[32:35], v[116:119], v[184:187], 0
	v_mfma_f32_16x16x32_bf16 v[28:31], v[136:139], v[184:187], 0
	v_mfma_f32_16x16x32_bf16 v[16:19], v[116:119], v[192:195], 0
	v_mfma_f32_16x16x32_bf16 v[12:15], v[136:139], v[192:195], 0
	v_mfma_f32_16x16x32_bf16 v[64:67], v[128:131], v[172:175], v[64:67]
	v_mfma_f32_16x16x32_bf16 v[60:63], v[148:151], v[172:175], v[60:63]
	v_mfma_f32_16x16x32_bf16 v[48:51], v[128:131], v[180:183], v[48:51]
	v_mfma_f32_16x16x32_bf16 v[44:47], v[148:151], v[180:183], v[44:47]
	v_mfma_f32_16x16x32_bf16 v[32:35], v[128:131], v[188:191], v[32:35]
	v_mfma_f32_16x16x32_bf16 v[28:31], v[148:151], v[188:191], v[28:31]
	v_mfma_f32_16x16x32_bf16 v[16:19], v[128:131], v[196:199], v[16:19]
	v_mfma_f32_16x16x32_bf16 v[12:15], v[148:151], v[196:199], v[12:15]
	v_mfma_f32_16x16x32_bf16 v[56:59], v[152:155], v[168:171], 0
	v_mfma_f32_16x16x32_bf16 v[52:55], v[160:163], v[168:171], 0
	v_mfma_f32_16x16x32_bf16 v[40:43], v[152:155], v[176:179], 0
	v_mfma_f32_16x16x32_bf16 v[36:39], v[160:163], v[176:179], 0
	v_mfma_f32_16x16x32_bf16 v[24:27], v[152:155], v[184:187], 0
	v_mfma_f32_16x16x32_bf16 v[20:23], v[160:163], v[184:187], 0
	v_mfma_f32_16x16x32_bf16 v[8:11], v[152:155], v[192:195], 0
	v_mfma_f32_16x16x32_bf16 v[4:7], v[160:163], v[192:195], 0
	v_mfma_f32_16x16x32_bf16 v[56:59], v[156:159], v[172:175], v[56:59]
	v_mfma_f32_16x16x32_bf16 v[52:55], v[164:167], v[172:175], v[52:55]
	v_mfma_f32_16x16x32_bf16 v[40:43], v[156:159], v[180:183], v[40:43]
	v_mfma_f32_16x16x32_bf16 v[36:39], v[164:167], v[180:183], v[36:39]
	v_mfma_f32_16x16x32_bf16 v[24:27], v[156:159], v[188:191], v[24:27]
	v_mfma_f32_16x16x32_bf16 v[20:23], v[164:167], v[188:191], v[20:23]
	v_mfma_f32_16x16x32_bf16 v[8:11], v[156:159], v[196:199], v[8:11]
	v_mfma_f32_16x16x32_bf16 v[4:7], v[164:167], v[196:199], v[4:7]
	s_barrier
	s_add_i32 s73, 0, 0x18000
	s_add_i32 s74, 0, 0x1c000
	v_add_u32_e32 v148, s73, v203
	v_add_u32_e32 v164, s74, v203
	ds_read_b128 v[116:119], v148
	ds_read_b128 v[128:131], v148 offset:1024
	ds_read_b128 v[136:139], v148 offset:2048
	ds_read_b128 v[148:151], v148 offset:3072
	ds_read_b128 v[152:155], v164
	ds_read_b128 v[156:159], v164 offset:1024
	ds_read_b128 v[160:163], v164 offset:2048
	ds_read_b128 v[164:167], v164 offset:3072
	s_add_u32 s4, s4, 0x40000
	s_addc_u32 s5, s5, 0
	s_mov_b32 m0, s47
	v_lshl_add_u64 v[218:219], s[4:5], 0, v[208:209]
	ds_read_b128 v[168:171], v236 offset:32768
	ds_read_b128 v[172:175], v236 offset:33792
	ds_read_b128 v[176:179], v236 offset:34816
	ds_read_b128 v[180:183], v236 offset:35840
	ds_read_b128 v[184:187], v236 offset:36864
	ds_read_b128 v[188:191], v236 offset:37888
	ds_read_b128 v[192:195], v236 offset:38912
	ds_read_b128 v[196:199], v236 offset:39936
	global_load_lds_dwordx4 v[218:219], off
	v_lshl_add_u64 v[218:219], s[4:5], 0, v[206:207]
	s_mov_b32 m0, s52
	s_nop 0
	global_load_lds_dwordx4 v[218:219], off
	s_waitcnt vmcnt(8)
	s_waitcnt lgkmcnt(0)
	s_barrier
	v_mfma_f32_16x16x32_bf16 v[144:147], v[116:119], v[168:171], v[144:147]
	v_mfma_f32_16x16x32_bf16 v[140:143], v[136:139], v[168:171], v[140:143]
	v_mfma_f32_16x16x32_bf16 v[120:123], v[116:119], v[176:179], v[120:123]
	v_mfma_f32_16x16x32_bf16 v[112:115], v[136:139], v[176:179], v[112:115]
	v_mfma_f32_16x16x32_bf16 v[96:99], v[116:119], v[184:187], v[96:99]
	v_mfma_f32_16x16x32_bf16 v[92:95], v[136:139], v[184:187], v[92:95]
	v_mfma_f32_16x16x32_bf16 v[80:83], v[116:119], v[192:195], v[80:83]
	v_mfma_f32_16x16x32_bf16 v[76:79], v[136:139], v[192:195], v[76:79]
	v_mfma_f32_16x16x32_bf16 v[144:147], v[128:131], v[172:175], v[144:147]
	v_mfma_f32_16x16x32_bf16 v[140:143], v[148:151], v[172:175], v[140:143]
	v_mfma_f32_16x16x32_bf16 v[120:123], v[128:131], v[180:183], v[120:123]
	v_mfma_f32_16x16x32_bf16 v[112:115], v[148:151], v[180:183], v[112:115]
	v_mfma_f32_16x16x32_bf16 v[96:99], v[128:131], v[188:191], v[96:99]
	v_mfma_f32_16x16x32_bf16 v[92:95], v[148:151], v[188:191], v[92:95]
	v_mfma_f32_16x16x32_bf16 v[80:83], v[128:131], v[196:199], v[80:83]
	v_mfma_f32_16x16x32_bf16 v[76:79], v[148:151], v[196:199], v[76:79]
	v_mfma_f32_16x16x32_bf16 v[132:135], v[152:155], v[168:171], v[132:135]
	v_mfma_f32_16x16x32_bf16 v[124:127], v[160:163], v[168:171], v[124:127]
	v_mfma_f32_16x16x32_bf16 v[104:107], v[152:155], v[176:179], v[104:107]
	v_mfma_f32_16x16x32_bf16 v[100:103], v[160:163], v[176:179], v[100:103]
	v_mfma_f32_16x16x32_bf16 v[88:91], v[152:155], v[184:187], v[88:91]
	v_mfma_f32_16x16x32_bf16 v[84:87], v[160:163], v[184:187], v[84:87]
	v_mfma_f32_16x16x32_bf16 v[72:75], v[152:155], v[192:195], v[72:75]
	v_mfma_f32_16x16x32_bf16 v[68:71], v[160:163], v[192:195], v[68:71]
	v_mfma_f32_16x16x32_bf16 v[132:135], v[156:159], v[172:175], v[132:135]
	v_mfma_f32_16x16x32_bf16 v[124:127], v[164:167], v[172:175], v[124:127]
	v_mfma_f32_16x16x32_bf16 v[104:107], v[156:159], v[180:183], v[104:107]
	v_mfma_f32_16x16x32_bf16 v[100:103], v[164:167], v[180:183], v[100:103]
	v_mfma_f32_16x16x32_bf16 v[88:91], v[156:159], v[188:191], v[88:91]
	v_mfma_f32_16x16x32_bf16 v[84:87], v[164:167], v[188:191], v[84:87]
	v_mfma_f32_16x16x32_bf16 v[72:75], v[156:159], v[196:199], v[72:75]
	v_mfma_f32_16x16x32_bf16 v[68:71], v[164:167], v[196:199], v[68:71]
	s_barrier
	s_add_i32 s4, s73, s16
	v_lshl_add_u64 v[214:215], v[214:215], 0, s[34:35]
	s_mov_b32 m0, s4
	ds_read_b128 v[168:171], v236 offset:49152
	ds_read_b128 v[172:175], v236 offset:50176
	ds_read_b128 v[176:179], v236 offset:51200
	ds_read_b128 v[180:183], v236 offset:52224
	ds_read_b128 v[184:187], v236 offset:53248
	ds_read_b128 v[188:191], v236 offset:54272
	ds_read_b128 v[192:195], v236 offset:55296
	ds_read_b128 v[196:199], v236 offset:56320
	global_load_lds_dwordx4 v[214:215], off
	s_add_i32 m0, s4, 0x2000
	s_add_u32 s4, s50, 0x40080
	v_lshl_add_u64 v[214:215], v[216:217], 0, s[34:35]
	s_addc_u32 s5, s51, 0
	s_add_i32 s50, s74, s16
	global_load_lds_dwordx4 v[214:215], off
	v_lshl_add_u64 v[214:215], s[4:5], 0, v[2:3]
	s_mov_b32 m0, s50
	s_nop 0
	global_load_lds_dwordx4 v[214:215], off
	v_lshl_add_u64 v[214:215], s[4:5], 0, v[204:205]
	s_add_i32 m0, s50, 0x2000
	s_nop 0
	global_load_lds_dwordx4 v[214:215], off
	v_lshl_add_u64 v[214:215], s[12:13], 0, v[208:209]
	s_mov_b32 m0, s60
	s_nop 0
	global_load_lds_dwordx4 v[214:215], off
	v_lshl_add_u64 v[214:215], s[12:13], 0, v[206:207]
	s_mov_b32 m0, s61
	s_nop 0
	global_load_lds_dwordx4 v[214:215], off
	s_waitcnt vmcnt(8)
	s_waitcnt lgkmcnt(0)
	s_barrier
	v_mfma_f32_16x16x32_bf16 v[64:67], v[116:119], v[168:171], v[64:67]
	v_mfma_f32_16x16x32_bf16 v[60:63], v[136:139], v[168:171], v[60:63]
	v_mfma_f32_16x16x32_bf16 v[48:51], v[116:119], v[176:179], v[48:51]
	v_mfma_f32_16x16x32_bf16 v[44:47], v[136:139], v[176:179], v[44:47]
	v_mfma_f32_16x16x32_bf16 v[32:35], v[116:119], v[184:187], v[32:35]
	v_mfma_f32_16x16x32_bf16 v[28:31], v[136:139], v[184:187], v[28:31]
	v_mfma_f32_16x16x32_bf16 v[16:19], v[116:119], v[192:195], v[16:19]
	v_mfma_f32_16x16x32_bf16 v[12:15], v[136:139], v[192:195], v[12:15]
	v_mfma_f32_16x16x32_bf16 v[64:67], v[128:131], v[172:175], v[64:67]
	v_mfma_f32_16x16x32_bf16 v[60:63], v[148:151], v[172:175], v[60:63]
	v_mfma_f32_16x16x32_bf16 v[48:51], v[128:131], v[180:183], v[48:51]
	v_mfma_f32_16x16x32_bf16 v[44:47], v[148:151], v[180:183], v[44:47]
	v_mfma_f32_16x16x32_bf16 v[32:35], v[128:131], v[188:191], v[32:35]
	v_mfma_f32_16x16x32_bf16 v[28:31], v[148:151], v[188:191], v[28:31]
	v_mfma_f32_16x16x32_bf16 v[16:19], v[128:131], v[196:199], v[16:19]
	v_mfma_f32_16x16x32_bf16 v[12:15], v[148:151], v[196:199], v[12:15]
	v_mfma_f32_16x16x32_bf16 v[56:59], v[152:155], v[168:171], v[56:59]
	v_mfma_f32_16x16x32_bf16 v[52:55], v[160:163], v[168:171], v[52:55]
	v_mfma_f32_16x16x32_bf16 v[40:43], v[152:155], v[176:179], v[40:43]
	v_mfma_f32_16x16x32_bf16 v[36:39], v[160:163], v[176:179], v[36:39]
	v_mfma_f32_16x16x32_bf16 v[24:27], v[152:155], v[184:187], v[24:27]
	v_mfma_f32_16x16x32_bf16 v[20:23], v[160:163], v[184:187], v[20:23]
	v_mfma_f32_16x16x32_bf16 v[8:11], v[152:155], v[192:195], v[8:11]
	v_mfma_f32_16x16x32_bf16 v[4:7], v[160:163], v[192:195], v[4:7]
	v_mfma_f32_16x16x32_bf16 v[56:59], v[156:159], v[172:175], v[56:59]
	v_mfma_f32_16x16x32_bf16 v[52:55], v[164:167], v[172:175], v[52:55]
	v_mfma_f32_16x16x32_bf16 v[40:43], v[156:159], v[180:183], v[40:43]
	v_mfma_f32_16x16x32_bf16 v[36:39], v[164:167], v[180:183], v[36:39]
	v_mfma_f32_16x16x32_bf16 v[24:27], v[156:159], v[188:191], v[24:27]
	v_mfma_f32_16x16x32_bf16 v[20:23], v[164:167], v[188:191], v[20:23]
	v_mfma_f32_16x16x32_bf16 v[8:11], v[156:159], v[196:199], v[8:11]
	v_mfma_f32_16x16x32_bf16 v[4:7], v[164:167], v[196:199], v[4:7]
	s_barrier
	s_add_i32 s72, s72, 2
	s_add_u32 s48, s48, 0x100
	s_addc_u32 s49, s49, 0
	s_cmp_gt_u32 s72, 13
.LBB0_1118:
	s_add_u32 s4, s44, s48
	s_addc_u32 s5, s45, s49
	s_add_u32 s73, s4, 0x100
	s_addc_u32 s74, s5, 0
	s_add_u32 s50, s70, s48
	s_addc_u32 s51, s71, s49
	s_add_u32 s4, s4, 0x180
	s_addc_u32 s5, s5, 0
	s_add_i32 s75, 0, 0x10000
	s_add_i32 s76, 0, 0x14000
	v_add_u32_e32 v148, s75, v203
	v_add_u32_e32 v164, s76, v203
	ds_read_b128 v[116:119], v148
	ds_read_b128 v[128:131], v148 offset:1024
	ds_read_b128 v[136:139], v148 offset:2048
	ds_read_b128 v[148:151], v148 offset:3072
	ds_read_b128 v[152:155], v164
	ds_read_b128 v[156:159], v164 offset:1024
	ds_read_b128 v[160:163], v164 offset:2048
	ds_read_b128 v[164:167], v164 offset:3072
	s_cmpk_eq_i32 s48, 0x700
	s_cselect_b32 s13, s69, s5
	s_cselect_b32 s12, s68, s4
	s_cselect_b32 s51, s23, s51
	s_cselect_b32 s50, s65, s50
	s_cselect_b32 s5, s37, s74
	s_cselect_b32 s4, s64, s73
	v_lshl_add_u64 v[214:215], v[108:109], 0, s[48:49]
	s_add_i32 m0, s17, 0xc000
	ds_read_b128 v[168:171], v236
	ds_read_b128 v[172:175], v236 offset:1024
	ds_read_b128 v[176:179], v236 offset:2048
	ds_read_b128 v[180:183], v236 offset:3072
	ds_read_b128 v[184:187], v236 offset:4096
	ds_read_b128 v[188:191], v236 offset:5120
	ds_read_b128 v[192:195], v236 offset:6144
	ds_read_b128 v[196:199], v236 offset:7168
	global_load_lds_dwordx4 v[214:215], off
	v_lshl_add_u64 v[214:215], v[110:111], 0, s[48:49]
	s_add_i32 m0, s17, 0xe000
	s_nop 0
	global_load_lds_dwordx4 v[214:215], off
	s_waitcnt vmcnt(8)
	s_waitcnt lgkmcnt(0)
	s_barrier
	v_mfma_f32_16x16x32_bf16 v[144:147], v[116:119], v[168:171], v[144:147]
	v_mfma_f32_16x16x32_bf16 v[140:143], v[136:139], v[168:171], v[140:143]
	v_mfma_f32_16x16x32_bf16 v[120:123], v[116:119], v[176:179], v[120:123]
	v_mfma_f32_16x16x32_bf16 v[112:115], v[136:139], v[176:179], v[112:115]
	v_mfma_f32_16x16x32_bf16 v[96:99], v[116:119], v[184:187], v[96:99]
	v_mfma_f32_16x16x32_bf16 v[92:95], v[136:139], v[184:187], v[92:95]
	v_mfma_f32_16x16x32_bf16 v[80:83], v[116:119], v[192:195], v[80:83]
	v_mfma_f32_16x16x32_bf16 v[76:79], v[136:139], v[192:195], v[76:79]
	v_mfma_f32_16x16x32_bf16 v[144:147], v[128:131], v[172:175], v[144:147]
	v_mfma_f32_16x16x32_bf16 v[140:143], v[148:151], v[172:175], v[140:143]
	v_mfma_f32_16x16x32_bf16 v[120:123], v[128:131], v[180:183], v[120:123]
	v_mfma_f32_16x16x32_bf16 v[112:115], v[148:151], v[180:183], v[112:115]
	v_mfma_f32_16x16x32_bf16 v[96:99], v[128:131], v[188:191], v[96:99]
	v_mfma_f32_16x16x32_bf16 v[92:95], v[148:151], v[188:191], v[92:95]
	v_mfma_f32_16x16x32_bf16 v[80:83], v[128:131], v[196:199], v[80:83]
	v_mfma_f32_16x16x32_bf16 v[76:79], v[148:151], v[196:199], v[76:79]
	v_mfma_f32_16x16x32_bf16 v[132:135], v[152:155], v[168:171], v[132:135]
	v_mfma_f32_16x16x32_bf16 v[124:127], v[160:163], v[168:171], v[124:127]
	v_mfma_f32_16x16x32_bf16 v[104:107], v[152:155], v[176:179], v[104:107]
	v_mfma_f32_16x16x32_bf16 v[100:103], v[160:163], v[176:179], v[100:103]
	v_mfma_f32_16x16x32_bf16 v[88:91], v[152:155], v[184:187], v[88:91]
	v_mfma_f32_16x16x32_bf16 v[84:87], v[160:163], v[184:187], v[84:87]
	v_mfma_f32_16x16x32_bf16 v[72:75], v[152:155], v[192:195], v[72:75]
	v_mfma_f32_16x16x32_bf16 v[68:71], v[160:163], v[192:195], v[68:71]
	v_mfma_f32_16x16x32_bf16 v[132:135], v[156:159], v[172:175], v[132:135]
	v_mfma_f32_16x16x32_bf16 v[124:127], v[164:167], v[172:175], v[124:127]
	v_mfma_f32_16x16x32_bf16 v[104:107], v[156:159], v[180:183], v[104:107]
	v_mfma_f32_16x16x32_bf16 v[100:103], v[164:167], v[180:183], v[100:103]
	v_mfma_f32_16x16x32_bf16 v[88:91], v[156:159], v[188:191], v[88:91]
	v_mfma_f32_16x16x32_bf16 v[84:87], v[164:167], v[188:191], v[84:87]
	v_mfma_f32_16x16x32_bf16 v[72:75], v[156:159], v[196:199], v[72:75]
	v_mfma_f32_16x16x32_bf16 v[68:71], v[164:167], v[196:199], v[68:71]
	s_barrier
	s_add_i32 s73, s75, s16
	v_lshl_add_u64 v[214:215], s[50:51], 0, v[2:3]
	s_mov_b32 m0, s73
	ds_read_b128 v[168:171], v236 offset:16384
	ds_read_b128 v[172:175], v236 offset:17408
	ds_read_b128 v[176:179], v236 offset:18432
	ds_read_b128 v[180:183], v236 offset:19456
	ds_read_b128 v[184:187], v236 offset:20480
	ds_read_b128 v[188:191], v236 offset:21504
	ds_read_b128 v[192:195], v236 offset:22528
	ds_read_b128 v[196:199], v236 offset:23552
	global_load_lds_dwordx4 v[214:215], off
	s_add_i32 m0, s73, 0x2000
	s_add_u32 s74, s50, 0x40000
	v_lshl_add_u64 v[216:217], s[50:51], 0, v[204:205]
	s_addc_u32 s75, s51, 0
	s_add_i32 s73, s76, s16
	global_load_lds_dwordx4 v[216:217], off
	v_lshl_add_u64 v[218:219], s[74:75], 0, v[2:3]
	s_mov_b32 m0, s73
	s_nop 0
	global_load_lds_dwordx4 v[218:219], off
	v_lshl_add_u64 v[218:219], s[74:75], 0, v[204:205]
	s_add_i32 m0, s73, 0x2000
	s_nop 0
	global_load_lds_dwordx4 v[218:219], off
	v_lshl_add_u64 v[218:219], s[4:5], 0, v[208:209]
	s_mov_b32 m0, s17
	s_nop 0
	global_load_lds_dwordx4 v[218:219], off
	v_lshl_add_u64 v[218:219], s[4:5], 0, v[206:207]
	s_mov_b32 m0, s46
	s_nop 0
	global_load_lds_dwordx4 v[218:219], off
	s_waitcnt vmcnt(8)
	s_waitcnt lgkmcnt(0)
	s_barrier
	v_mfma_f32_16x16x32_bf16 v[64:67], v[116:119], v[168:171], v[64:67]
	v_mfma_f32_16x16x32_bf16 v[60:63], v[136:139], v[168:171], v[60:63]
	v_mfma_f32_16x16x32_bf16 v[48:51], v[116:119], v[176:179], v[48:51]
	v_mfma_f32_16x16x32_bf16 v[44:47], v[136:139], v[176:179], v[44:47]
	v_mfma_f32_16x16x32_bf16 v[32:35], v[116:119], v[184:187], v[32:35]
	v_mfma_f32_16x16x32_bf16 v[28:31], v[136:139], v[184:187], v[28:31]
	v_mfma_f32_16x16x32_bf16 v[16:19], v[116:119], v[192:195], v[16:19]
	v_mfma_f32_16x16x32_bf16 v[12:15], v[136:139], v[192:195], v[12:15]
	v_mfma_f32_16x16x32_bf16 v[64:67], v[128:131], v[172:175], v[64:67]
	v_mfma_f32_16x16x32_bf16 v[60:63], v[148:151], v[172:175], v[60:63]
	v_mfma_f32_16x16x32_bf16 v[48:51], v[128:131], v[180:183], v[48:51]
	v_mfma_f32_16x16x32_bf16 v[44:47], v[148:151], v[180:183], v[44:47]
	v_mfma_f32_16x16x32_bf16 v[32:35], v[128:131], v[188:191], v[32:35]
	v_mfma_f32_16x16x32_bf16 v[28:31], v[148:151], v[188:191], v[28:31]
	v_mfma_f32_16x16x32_bf16 v[16:19], v[128:131], v[196:199], v[16:19]
	v_mfma_f32_16x16x32_bf16 v[12:15], v[148:151], v[196:199], v[12:15]
	v_mfma_f32_16x16x32_bf16 v[56:59], v[152:155], v[168:171], v[56:59]
	v_mfma_f32_16x16x32_bf16 v[52:55], v[160:163], v[168:171], v[52:55]
	v_mfma_f32_16x16x32_bf16 v[40:43], v[152:155], v[176:179], v[40:43]
	v_mfma_f32_16x16x32_bf16 v[36:39], v[160:163], v[176:179], v[36:39]
	v_mfma_f32_16x16x32_bf16 v[24:27], v[152:155], v[184:187], v[24:27]
	v_mfma_f32_16x16x32_bf16 v[20:23], v[160:163], v[184:187], v[20:23]
	v_mfma_f32_16x16x32_bf16 v[8:11], v[152:155], v[192:195], v[8:11]
	v_mfma_f32_16x16x32_bf16 v[4:7], v[160:163], v[192:195], v[4:7]
	v_mfma_f32_16x16x32_bf16 v[56:59], v[156:159], v[172:175], v[56:59]
	v_mfma_f32_16x16x32_bf16 v[52:55], v[164:167], v[172:175], v[52:55]
	v_mfma_f32_16x16x32_bf16 v[40:43], v[156:159], v[180:183], v[40:43]
	v_mfma_f32_16x16x32_bf16 v[36:39], v[164:167], v[180:183], v[36:39]
	v_mfma_f32_16x16x32_bf16 v[24:27], v[156:159], v[188:191], v[24:27]
	v_mfma_f32_16x16x32_bf16 v[20:23], v[164:167], v[188:191], v[20:23]
	v_mfma_f32_16x16x32_bf16 v[8:11], v[156:159], v[196:199], v[8:11]
	v_mfma_f32_16x16x32_bf16 v[4:7], v[164:167], v[196:199], v[4:7]
	s_barrier
	s_add_i32 s73, 0, 0x18000
	s_add_i32 s74, 0, 0x1c000
	v_add_u32_e32 v148, s73, v203
	v_add_u32_e32 v164, s74, v203
	ds_read_b128 v[116:119], v148
	ds_read_b128 v[128:131], v148 offset:1024
	ds_read_b128 v[136:139], v148 offset:2048
	ds_read_b128 v[148:151], v148 offset:3072
	ds_read_b128 v[152:155], v164
	ds_read_b128 v[156:159], v164 offset:1024
	ds_read_b128 v[160:163], v164 offset:2048
	ds_read_b128 v[164:167], v164 offset:3072
	s_add_u32 s4, s4, 0x40000
	s_addc_u32 s5, s5, 0
	s_mov_b32 m0, s47
	v_lshl_add_u64 v[218:219], s[4:5], 0, v[208:209]
	ds_read_b128 v[168:171], v236 offset:32768
	ds_read_b128 v[172:175], v236 offset:33792
	ds_read_b128 v[176:179], v236 offset:34816
	ds_read_b128 v[180:183], v236 offset:35840
	ds_read_b128 v[184:187], v236 offset:36864
	ds_read_b128 v[188:191], v236 offset:37888
	ds_read_b128 v[192:195], v236 offset:38912
	ds_read_b128 v[196:199], v236 offset:39936
	global_load_lds_dwordx4 v[218:219], off
	v_lshl_add_u64 v[218:219], s[4:5], 0, v[206:207]
	s_mov_b32 m0, s52
	s_nop 0
	global_load_lds_dwordx4 v[218:219], off
	s_waitcnt vmcnt(8)
	s_waitcnt lgkmcnt(0)
	s_barrier
	v_mfma_f32_16x16x32_bf16 v[144:147], v[116:119], v[168:171], v[144:147]
	v_mfma_f32_16x16x32_bf16 v[140:143], v[136:139], v[168:171], v[140:143]
	v_mfma_f32_16x16x32_bf16 v[120:123], v[116:119], v[176:179], v[120:123]
	v_mfma_f32_16x16x32_bf16 v[112:115], v[136:139], v[176:179], v[112:115]
	v_mfma_f32_16x16x32_bf16 v[96:99], v[116:119], v[184:187], v[96:99]
	v_mfma_f32_16x16x32_bf16 v[92:95], v[136:139], v[184:187], v[92:95]
	v_mfma_f32_16x16x32_bf16 v[80:83], v[116:119], v[192:195], v[80:83]
	v_mfma_f32_16x16x32_bf16 v[76:79], v[136:139], v[192:195], v[76:79]
	v_mfma_f32_16x16x32_bf16 v[144:147], v[128:131], v[172:175], v[144:147]
	v_mfma_f32_16x16x32_bf16 v[140:143], v[148:151], v[172:175], v[140:143]
	v_mfma_f32_16x16x32_bf16 v[120:123], v[128:131], v[180:183], v[120:123]
	v_mfma_f32_16x16x32_bf16 v[112:115], v[148:151], v[180:183], v[112:115]
	v_mfma_f32_16x16x32_bf16 v[96:99], v[128:131], v[188:191], v[96:99]
	v_mfma_f32_16x16x32_bf16 v[92:95], v[148:151], v[188:191], v[92:95]
	v_mfma_f32_16x16x32_bf16 v[80:83], v[128:131], v[196:199], v[80:83]
	v_mfma_f32_16x16x32_bf16 v[76:79], v[148:151], v[196:199], v[76:79]
	v_mfma_f32_16x16x32_bf16 v[132:135], v[152:155], v[168:171], v[132:135]
	v_mfma_f32_16x16x32_bf16 v[124:127], v[160:163], v[168:171], v[124:127]
	v_mfma_f32_16x16x32_bf16 v[104:107], v[152:155], v[176:179], v[104:107]
	v_mfma_f32_16x16x32_bf16 v[100:103], v[160:163], v[176:179], v[100:103]
	v_mfma_f32_16x16x32_bf16 v[88:91], v[152:155], v[184:187], v[88:91]
	v_mfma_f32_16x16x32_bf16 v[84:87], v[160:163], v[184:187], v[84:87]
	v_mfma_f32_16x16x32_bf16 v[72:75], v[152:155], v[192:195], v[72:75]
	v_mfma_f32_16x16x32_bf16 v[68:71], v[160:163], v[192:195], v[68:71]
	v_mfma_f32_16x16x32_bf16 v[132:135], v[156:159], v[172:175], v[132:135]
	v_mfma_f32_16x16x32_bf16 v[124:127], v[164:167], v[172:175], v[124:127]
	v_mfma_f32_16x16x32_bf16 v[104:107], v[156:159], v[180:183], v[104:107]
	v_mfma_f32_16x16x32_bf16 v[100:103], v[164:167], v[180:183], v[100:103]
	v_mfma_f32_16x16x32_bf16 v[88:91], v[156:159], v[188:191], v[88:91]
	v_mfma_f32_16x16x32_bf16 v[84:87], v[164:167], v[188:191], v[84:87]
	v_mfma_f32_16x16x32_bf16 v[72:75], v[156:159], v[196:199], v[72:75]
	v_mfma_f32_16x16x32_bf16 v[68:71], v[164:167], v[196:199], v[68:71]
	s_barrier
	s_add_i32 s4, s73, s16
	v_lshl_add_u64 v[214:215], v[214:215], 0, s[34:35]
	s_mov_b32 m0, s4
	ds_read_b128 v[168:171], v236 offset:49152
	ds_read_b128 v[172:175], v236 offset:50176
	ds_read_b128 v[176:179], v236 offset:51200
	ds_read_b128 v[180:183], v236 offset:52224
	ds_read_b128 v[184:187], v236 offset:53248
	ds_read_b128 v[188:191], v236 offset:54272
	ds_read_b128 v[192:195], v236 offset:55296
	ds_read_b128 v[196:199], v236 offset:56320
	global_load_lds_dwordx4 v[214:215], off
	s_add_i32 m0, s4, 0x2000
	s_add_u32 s4, s50, 0x40080
	v_lshl_add_u64 v[214:215], v[216:217], 0, s[34:35]
	s_addc_u32 s5, s51, 0
	s_add_i32 s50, s74, s16
	global_load_lds_dwordx4 v[214:215], off
	v_lshl_add_u64 v[214:215], s[4:5], 0, v[2:3]
	s_mov_b32 m0, s50
	s_nop 0
	global_load_lds_dwordx4 v[214:215], off
	v_lshl_add_u64 v[214:215], s[4:5], 0, v[204:205]
	s_add_i32 m0, s50, 0x2000
	s_nop 0
	global_load_lds_dwordx4 v[214:215], off
	v_lshl_add_u64 v[214:215], s[12:13], 0, v[208:209]
	s_mov_b32 m0, s60
	s_nop 0
	global_load_lds_dwordx4 v[214:215], off
	v_lshl_add_u64 v[214:215], s[12:13], 0, v[206:207]
	s_mov_b32 m0, s61
	s_nop 0
	global_load_lds_dwordx4 v[214:215], off
	s_waitcnt vmcnt(8)
	s_waitcnt lgkmcnt(0)
	s_barrier
	v_mfma_f32_16x16x32_bf16 v[64:67], v[116:119], v[168:171], v[64:67]
	v_mfma_f32_16x16x32_bf16 v[60:63], v[136:139], v[168:171], v[60:63]
	v_mfma_f32_16x16x32_bf16 v[48:51], v[116:119], v[176:179], v[48:51]
	v_mfma_f32_16x16x32_bf16 v[44:47], v[136:139], v[176:179], v[44:47]
	v_mfma_f32_16x16x32_bf16 v[32:35], v[116:119], v[184:187], v[32:35]
	v_mfma_f32_16x16x32_bf16 v[28:31], v[136:139], v[184:187], v[28:31]
	v_mfma_f32_16x16x32_bf16 v[16:19], v[116:119], v[192:195], v[16:19]
	v_mfma_f32_16x16x32_bf16 v[12:15], v[136:139], v[192:195], v[12:15]
	v_mfma_f32_16x16x32_bf16 v[64:67], v[128:131], v[172:175], v[64:67]
	v_mfma_f32_16x16x32_bf16 v[60:63], v[148:151], v[172:175], v[60:63]
	v_mfma_f32_16x16x32_bf16 v[48:51], v[128:131], v[180:183], v[48:51]
	v_mfma_f32_16x16x32_bf16 v[44:47], v[148:151], v[180:183], v[44:47]
	v_mfma_f32_16x16x32_bf16 v[32:35], v[128:131], v[188:191], v[32:35]
	v_mfma_f32_16x16x32_bf16 v[28:31], v[148:151], v[188:191], v[28:31]
	v_mfma_f32_16x16x32_bf16 v[16:19], v[128:131], v[196:199], v[16:19]
	v_mfma_f32_16x16x32_bf16 v[12:15], v[148:151], v[196:199], v[12:15]
	v_mfma_f32_16x16x32_bf16 v[56:59], v[152:155], v[168:171], v[56:59]
	v_mfma_f32_16x16x32_bf16 v[52:55], v[160:163], v[168:171], v[52:55]
	v_mfma_f32_16x16x32_bf16 v[40:43], v[152:155], v[176:179], v[40:43]
	v_mfma_f32_16x16x32_bf16 v[36:39], v[160:163], v[176:179], v[36:39]
	v_mfma_f32_16x16x32_bf16 v[24:27], v[152:155], v[184:187], v[24:27]
	v_mfma_f32_16x16x32_bf16 v[20:23], v[160:163], v[184:187], v[20:23]
	v_mfma_f32_16x16x32_bf16 v[8:11], v[152:155], v[192:195], v[8:11]
	v_mfma_f32_16x16x32_bf16 v[4:7], v[160:163], v[192:195], v[4:7]
	v_mfma_f32_16x16x32_bf16 v[56:59], v[156:159], v[172:175], v[56:59]
	v_mfma_f32_16x16x32_bf16 v[52:55], v[164:167], v[172:175], v[52:55]
	v_mfma_f32_16x16x32_bf16 v[40:43], v[156:159], v[180:183], v[40:43]
	v_mfma_f32_16x16x32_bf16 v[36:39], v[164:167], v[180:183], v[36:39]
	v_mfma_f32_16x16x32_bf16 v[24:27], v[156:159], v[188:191], v[24:27]
	v_mfma_f32_16x16x32_bf16 v[20:23], v[164:167], v[188:191], v[20:23]
	v_mfma_f32_16x16x32_bf16 v[8:11], v[156:159], v[196:199], v[8:11]
	v_mfma_f32_16x16x32_bf16 v[4:7], v[164:167], v[196:199], v[4:7]
	s_barrier
	s_add_i32 s72, s72, 2
	s_add_u32 s48, s48, 0x100
	s_addc_u32 s49, s49, 0
	s_cmp_gt_u32 s72, 13
	s_cbranch_scc0 .LBB0_1118
	s_and_b64 vcc, exec, s[20:21]
	s_cbranch_vccz .LBB0_1121
	s_barrier

.LBB0_1205:
	s_ashr_i32 s37, s36, 31
	s_lshl_b64 s[4:5], s[36:37], 19
	s_add_u32 s40, s6, s4
	s_addc_u32 s41, s7, s5
	s_and_b64 s[4:5], s[38:39], exec
	s_cselect_b32 s37, s41, s23
	s_cselect_b32 s61, s40, s22
	s_ashr_i32 s21, s20, 31
	s_lshl_b64 s[4:5], s[20:21], 19
	s_add_u32 s42, s8, s4
	s_addc_u32 s43, s9, s5
	s_and_b64 s[4:5], s[38:39], exec
	s_cselect_b32 s21, s43, s45
	s_cselect_b32 s62, s42, s44
	s_add_u32 s63, s61, 0x80
	s_addc_u32 s64, s37, 0
	s_add_u32 s4, s22, 0x40080
	s_addc_u32 s5, s23, 0
	s_add_u32 s65, s44, 0x100
	v_lshl_add_u64 v[142:143], s[4:5], 0, v[138:139]
	v_lshl_add_u64 v[144:145], s[4:5], 0, v[140:141]
	s_addc_u32 s68, s45, 0
	s_mov_b32 s69, -2
	s_mov_b64 s[44:45], 0
	s_add_u32 s4, s22, s44
	s_addc_u32 s5, s23, s45
	s_add_u32 s70, s4, 0x100
	s_addc_u32 s71, s5, 0
	s_add_u32 s48, s65, s44
	s_addc_u32 s49, s68, s45
	s_add_u32 s4, s4, 0x180
	s_addc_u32 s5, s5, 0
	s_add_i32 s72, 0, 0x10000
	s_add_i32 s73, 0, 0x14000
	v_add_u32_e32 v160, s72, v146
	v_add_u32_e32 v176, s73, v146
	ds_read_b128 v[148:151], v160
	ds_read_b128 v[152:155], v160 offset:1024
	ds_read_b128 v[156:159], v160 offset:2048
	ds_read_b128 v[160:163], v160 offset:3072
	ds_read_b128 v[164:167], v176
	ds_read_b128 v[168:171], v176 offset:1024
	ds_read_b128 v[172:175], v176 offset:2048
	ds_read_b128 v[176:179], v176 offset:3072
	s_cmpk_eq_i32 s44, 0x700
	s_cselect_b32 s13, s64, s5
	s_cselect_b32 s12, s63, s4
	s_cselect_b32 s49, s21, s49
	s_cselect_b32 s48, s62, s48
	s_cselect_b32 s5, s37, s71
	s_cselect_b32 s4, s61, s70
	v_lshl_add_u64 v[216:217], v[142:143], 0, s[44:45]
	s_add_i32 m0, s17, 0xc000
	ds_read_b128 v[180:183], v147
	ds_read_b128 v[184:187], v147 offset:1024
	ds_read_b128 v[188:191], v147 offset:2048
	ds_read_b128 v[192:195], v147 offset:3072
	ds_read_b128 v[196:199], v147 offset:4096
	ds_read_b128 v[204:207], v147 offset:5120
	ds_read_b128 v[208:211], v147 offset:6144
	ds_read_b128 v[212:215], v147 offset:7168
	global_load_lds_dwordx4 v[216:217], off
	v_lshl_add_u64 v[216:217], v[144:145], 0, s[44:45]
	s_add_i32 m0, s17, 0xe000
	s_nop 0
	global_load_lds_dwordx4 v[216:217], off
	s_waitcnt vmcnt(8)
	s_waitcnt lgkmcnt(0)
	s_barrier
	v_mfma_f32_16x16x32_bf16 v[128:131], v[148:151], v[180:183], 0
	v_mfma_f32_16x16x32_bf16 v[124:127], v[156:159], v[180:183], 0
	v_mfma_f32_16x16x32_bf16 v[120:123], v[148:151], v[188:191], 0
	v_mfma_f32_16x16x32_bf16 v[116:119], v[156:159], v[188:191], 0
	v_mfma_f32_16x16x32_bf16 v[104:107], v[148:151], v[196:199], 0
	v_mfma_f32_16x16x32_bf16 v[100:103], v[156:159], v[196:199], 0
	v_mfma_f32_16x16x32_bf16 v[88:91], v[148:151], v[208:211], 0
	v_mfma_f32_16x16x32_bf16 v[84:87], v[156:159], v[208:211], 0
	v_mfma_f32_16x16x32_bf16 v[128:131], v[152:155], v[184:187], v[128:131]
	v_mfma_f32_16x16x32_bf16 v[124:127], v[160:163], v[184:187], v[124:127]
	v_mfma_f32_16x16x32_bf16 v[120:123], v[152:155], v[192:195], v[120:123]
	v_mfma_f32_16x16x32_bf16 v[116:119], v[160:163], v[192:195], v[116:119]
	v_mfma_f32_16x16x32_bf16 v[104:107], v[152:155], v[204:207], v[104:107]
	v_mfma_f32_16x16x32_bf16 v[100:103], v[160:163], v[204:207], v[100:103]
	v_mfma_f32_16x16x32_bf16 v[88:91], v[152:155], v[212:215], v[88:91]
	v_mfma_f32_16x16x32_bf16 v[84:87], v[160:163], v[212:215], v[84:87]
	v_mfma_f32_16x16x32_bf16 v[112:115], v[164:167], v[180:183], 0
	v_mfma_f32_16x16x32_bf16 v[108:111], v[172:175], v[180:183], 0
	v_mfma_f32_16x16x32_bf16 v[96:99], v[164:167], v[188:191], 0
	v_mfma_f32_16x16x32_bf16 v[92:95], v[172:175], v[188:191], 0
	v_mfma_f32_16x16x32_bf16 v[80:83], v[164:167], v[196:199], 0
	v_mfma_f32_16x16x32_bf16 v[76:79], v[172:175], v[196:199], 0
	v_mfma_f32_16x16x32_bf16 v[72:75], v[164:167], v[208:211], 0
	v_mfma_f32_16x16x32_bf16 v[68:71], v[172:175], v[208:211], 0
	v_mfma_f32_16x16x32_bf16 v[112:115], v[168:171], v[184:187], v[112:115]
	v_mfma_f32_16x16x32_bf16 v[108:111], v[176:179], v[184:187], v[108:111]
	v_mfma_f32_16x16x32_bf16 v[96:99], v[168:171], v[192:195], v[96:99]
	v_mfma_f32_16x16x32_bf16 v[92:95], v[176:179], v[192:195], v[92:95]
	v_mfma_f32_16x16x32_bf16 v[80:83], v[168:171], v[204:207], v[80:83]
	v_mfma_f32_16x16x32_bf16 v[76:79], v[176:179], v[204:207], v[76:79]
	v_mfma_f32_16x16x32_bf16 v[72:75], v[168:171], v[212:215], v[72:75]
	v_mfma_f32_16x16x32_bf16 v[68:71], v[176:179], v[212:215], v[68:71]
	s_barrier
	s_add_i32 s70, s72, s16
	v_lshl_add_u64 v[216:217], s[48:49], 0, v[2:3]
	s_mov_b32 m0, s70
	ds_read_b128 v[180:183], v147 offset:16384
	ds_read_b128 v[184:187], v147 offset:17408
	ds_read_b128 v[188:191], v147 offset:18432
	ds_read_b128 v[192:195], v147 offset:19456
	ds_read_b128 v[196:199], v147 offset:20480
	ds_read_b128 v[204:207], v147 offset:21504
	ds_read_b128 v[208:211], v147 offset:22528
	ds_read_b128 v[212:215], v147 offset:23552
	global_load_lds_dwordx4 v[216:217], off
	s_add_i32 m0, s70, 0x2000
	s_add_u32 s70, s48, 0x40000
	v_lshl_add_u64 v[218:219], s[48:49], 0, v[132:133]
	s_addc_u32 s71, s49, 0
	s_add_i32 s72, s73, s16
	global_load_lds_dwordx4 v[218:219], off
	v_lshl_add_u64 v[220:221], s[70:71], 0, v[2:3]
	s_mov_b32 m0, s72
	s_nop 0
	global_load_lds_dwordx4 v[220:221], off
	v_lshl_add_u64 v[220:221], s[70:71], 0, v[132:133]
	s_add_i32 m0, s72, 0x2000
	s_nop 0
	global_load_lds_dwordx4 v[220:221], off
	v_lshl_add_u64 v[220:221], s[4:5], 0, v[136:137]
	s_mov_b32 m0, s17
	s_nop 0
	global_load_lds_dwordx4 v[220:221], off
	v_lshl_add_u64 v[220:221], s[4:5], 0, v[134:135]
	s_mov_b32 m0, s46
	s_nop 0
	global_load_lds_dwordx4 v[220:221], off
	s_waitcnt vmcnt(8)
	s_waitcnt lgkmcnt(0)
	s_barrier
	v_mfma_f32_16x16x32_bf16 v[64:67], v[148:151], v[180:183], 0
	v_mfma_f32_16x16x32_bf16 v[60:63], v[156:159], v[180:183], 0
	v_mfma_f32_16x16x32_bf16 v[56:59], v[148:151], v[188:191], 0
	v_mfma_f32_16x16x32_bf16 v[52:55], v[156:159], v[188:191], 0
	v_mfma_f32_16x16x32_bf16 v[40:43], v[148:151], v[196:199], 0
	v_mfma_f32_16x16x32_bf16 v[36:39], v[156:159], v[196:199], 0
	v_mfma_f32_16x16x32_bf16 v[24:27], v[148:151], v[208:211], 0
	v_mfma_f32_16x16x32_bf16 v[20:23], v[156:159], v[208:211], 0
	v_mfma_f32_16x16x32_bf16 v[64:67], v[152:155], v[184:187], v[64:67]
	v_mfma_f32_16x16x32_bf16 v[60:63], v[160:163], v[184:187], v[60:63]
	v_mfma_f32_16x16x32_bf16 v[56:59], v[152:155], v[192:195], v[56:59]
	v_mfma_f32_16x16x32_bf16 v[52:55], v[160:163], v[192:195], v[52:55]
	v_mfma_f32_16x16x32_bf16 v[40:43], v[152:155], v[204:207], v[40:43]
	v_mfma_f32_16x16x32_bf16 v[36:39], v[160:163], v[204:207], v[36:39]
	v_mfma_f32_16x16x32_bf16 v[24:27], v[152:155], v[212:215], v[24:27]
	v_mfma_f32_16x16x32_bf16 v[20:23], v[160:163], v[212:215], v[20:23]
	v_mfma_f32_16x16x32_bf16 v[48:51], v[164:167], v[180:183], 0
	v_mfma_f32_16x16x32_bf16 v[44:47], v[172:175], v[180:183], 0
	v_mfma_f32_16x16x32_bf16 v[32:35], v[164:167], v[188:191], 0
	v_mfma_f32_16x16x32_bf16 v[28:31], v[172:175], v[188:191], 0
	v_mfma_f32_16x16x32_bf16 v[16:19], v[164:167], v[196:199], 0
	v_mfma_f32_16x16x32_bf16 v[12:15], v[172:175], v[196:199], 0
	v_mfma_f32_16x16x32_bf16 v[8:11], v[164:167], v[208:211], 0
	v_mfma_f32_16x16x32_bf16 v[4:7], v[172:175], v[208:211], 0
	v_mfma_f32_16x16x32_bf16 v[48:51], v[168:171], v[184:187], v[48:51]
	v_mfma_f32_16x16x32_bf16 v[44:47], v[176:179], v[184:187], v[44:47]
	v_mfma_f32_16x16x32_bf16 v[32:35], v[168:171], v[192:195], v[32:35]
	v_mfma_f32_16x16x32_bf16 v[28:31], v[176:179], v[192:195], v[28:31]
	v_mfma_f32_16x16x32_bf16 v[16:19], v[168:171], v[204:207], v[16:19]
	v_mfma_f32_16x16x32_bf16 v[12:15], v[176:179], v[204:207], v[12:15]
	v_mfma_f32_16x16x32_bf16 v[8:11], v[168:171], v[212:215], v[8:11]
	v_mfma_f32_16x16x32_bf16 v[4:7], v[176:179], v[212:215], v[4:7]
	s_barrier
	s_add_i32 s70, 0, 0x18000
	s_add_i32 s71, 0, 0x1c000
	v_add_u32_e32 v160, s70, v146
	v_add_u32_e32 v176, s71, v146
	ds_read_b128 v[148:151], v160
	ds_read_b128 v[152:155], v160 offset:1024
	ds_read_b128 v[156:159], v160 offset:2048
	ds_read_b128 v[160:163], v160 offset:3072
	ds_read_b128 v[164:167], v176
	ds_read_b128 v[168:171], v176 offset:1024
	ds_read_b128 v[172:175], v176 offset:2048
	ds_read_b128 v[176:179], v176 offset:3072
	s_add_u32 s4, s4, 0x40000
	s_addc_u32 s5, s5, 0
	s_mov_b32 m0, s47
	v_lshl_add_u64 v[220:221], s[4:5], 0, v[136:137]
	ds_read_b128 v[180:183], v147 offset:32768
	ds_read_b128 v[184:187], v147 offset:33792
	ds_read_b128 v[188:191], v147 offset:34816
	ds_read_b128 v[192:195], v147 offset:35840
	ds_read_b128 v[196:199], v147 offset:36864
	ds_read_b128 v[204:207], v147 offset:37888
	ds_read_b128 v[208:211], v147 offset:38912
	ds_read_b128 v[212:215], v147 offset:39936
	global_load_lds_dwordx4 v[220:221], off
	v_lshl_add_u64 v[220:221], s[4:5], 0, v[134:135]
	s_mov_b32 m0, s50
	s_nop 0
	global_load_lds_dwordx4 v[220:221], off
	s_waitcnt vmcnt(8)
	s_waitcnt lgkmcnt(0)
	s_barrier
	v_mfma_f32_16x16x32_bf16 v[128:131], v[148:151], v[180:183], v[128:131]
	v_mfma_f32_16x16x32_bf16 v[124:127], v[156:159], v[180:183], v[124:127]
	v_mfma_f32_16x16x32_bf16 v[120:123], v[148:151], v[188:191], v[120:123]
	v_mfma_f32_16x16x32_bf16 v[116:119], v[156:159], v[188:191], v[116:119]
	v_mfma_f32_16x16x32_bf16 v[104:107], v[148:151], v[196:199], v[104:107]
	v_mfma_f32_16x16x32_bf16 v[100:103], v[156:159], v[196:199], v[100:103]
	v_mfma_f32_16x16x32_bf16 v[88:91], v[148:151], v[208:211], v[88:91]
	v_mfma_f32_16x16x32_bf16 v[84:87], v[156:159], v[208:211], v[84:87]
	v_mfma_f32_16x16x32_bf16 v[128:131], v[152:155], v[184:187], v[128:131]
	v_mfma_f32_16x16x32_bf16 v[124:127], v[160:163], v[184:187], v[124:127]
	v_mfma_f32_16x16x32_bf16 v[120:123], v[152:155], v[192:195], v[120:123]
	v_mfma_f32_16x16x32_bf16 v[116:119], v[160:163], v[192:195], v[116:119]
	v_mfma_f32_16x16x32_bf16 v[104:107], v[152:155], v[204:207], v[104:107]
	v_mfma_f32_16x16x32_bf16 v[100:103], v[160:163], v[204:207], v[100:103]
	v_mfma_f32_16x16x32_bf16 v[88:91], v[152:155], v[212:215], v[88:91]
	v_mfma_f32_16x16x32_bf16 v[84:87], v[160:163], v[212:215], v[84:87]
	v_mfma_f32_16x16x32_bf16 v[112:115], v[164:167], v[180:183], v[112:115]
	v_mfma_f32_16x16x32_bf16 v[108:111], v[172:175], v[180:183], v[108:111]
	v_mfma_f32_16x16x32_bf16 v[96:99], v[164:167], v[188:191], v[96:99]
	v_mfma_f32_16x16x32_bf16 v[92:95], v[172:175], v[188:191], v[92:95]
	v_mfma_f32_16x16x32_bf16 v[80:83], v[164:167], v[196:199], v[80:83]
	v_mfma_f32_16x16x32_bf16 v[76:79], v[172:175], v[196:199], v[76:79]
	v_mfma_f32_16x16x32_bf16 v[72:75], v[164:167], v[208:211], v[72:75]
	v_mfma_f32_16x16x32_bf16 v[68:71], v[172:175], v[208:211], v[68:71]
	v_mfma_f32_16x16x32_bf16 v[112:115], v[168:171], v[184:187], v[112:115]
	v_mfma_f32_16x16x32_bf16 v[108:111], v[176:179], v[184:187], v[108:111]
	v_mfma_f32_16x16x32_bf16 v[96:99], v[168:171], v[192:195], v[96:99]
	v_mfma_f32_16x16x32_bf16 v[92:95], v[176:179], v[192:195], v[92:95]
	v_mfma_f32_16x16x32_bf16 v[80:83], v[168:171], v[204:207], v[80:83]
	v_mfma_f32_16x16x32_bf16 v[76:79], v[176:179], v[204:207], v[76:79]
	v_mfma_f32_16x16x32_bf16 v[72:75], v[168:171], v[212:215], v[72:75]
	v_mfma_f32_16x16x32_bf16 v[68:71], v[176:179], v[212:215], v[68:71]
	s_barrier
	s_add_i32 s4, s70, s16
	v_lshl_add_u64 v[216:217], v[216:217], 0, s[34:35]
	s_mov_b32 m0, s4
	ds_read_b128 v[180:183], v147 offset:49152
	ds_read_b128 v[184:187], v147 offset:50176
	ds_read_b128 v[188:191], v147 offset:51200
	ds_read_b128 v[192:195], v147 offset:52224
	ds_read_b128 v[196:199], v147 offset:53248
	ds_read_b128 v[204:207], v147 offset:54272
	ds_read_b128 v[208:211], v147 offset:55296
	ds_read_b128 v[212:215], v147 offset:56320
	global_load_lds_dwordx4 v[216:217], off
	s_add_i32 m0, s4, 0x2000
	s_add_u32 s4, s48, 0x40080
	v_lshl_add_u64 v[216:217], v[218:219], 0, s[34:35]
	s_addc_u32 s5, s49, 0
	s_add_i32 s48, s71, s16
	global_load_lds_dwordx4 v[216:217], off
	v_lshl_add_u64 v[216:217], s[4:5], 0, v[2:3]
	s_mov_b32 m0, s48
	s_nop 0
	global_load_lds_dwordx4 v[216:217], off
	v_lshl_add_u64 v[216:217], s[4:5], 0, v[132:133]
	s_add_i32 m0, s48, 0x2000
	s_nop 0
	global_load_lds_dwordx4 v[216:217], off
	v_lshl_add_u64 v[216:217], s[12:13], 0, v[136:137]
	s_mov_b32 m0, s53
	s_nop 0
	global_load_lds_dwordx4 v[216:217], off
	v_lshl_add_u64 v[216:217], s[12:13], 0, v[134:135]
	s_mov_b32 m0, s56
	s_nop 0
	global_load_lds_dwordx4 v[216:217], off
	s_waitcnt vmcnt(8)
	s_waitcnt lgkmcnt(0)
	s_barrier
	v_mfma_f32_16x16x32_bf16 v[64:67], v[148:151], v[180:183], v[64:67]
	v_mfma_f32_16x16x32_bf16 v[60:63], v[156:159], v[180:183], v[60:63]
	v_mfma_f32_16x16x32_bf16 v[56:59], v[148:151], v[188:191], v[56:59]
	v_mfma_f32_16x16x32_bf16 v[52:55], v[156:159], v[188:191], v[52:55]
	v_mfma_f32_16x16x32_bf16 v[40:43], v[148:151], v[196:199], v[40:43]
	v_mfma_f32_16x16x32_bf16 v[36:39], v[156:159], v[196:199], v[36:39]
	v_mfma_f32_16x16x32_bf16 v[24:27], v[148:151], v[208:211], v[24:27]
	v_mfma_f32_16x16x32_bf16 v[20:23], v[156:159], v[208:211], v[20:23]
	v_mfma_f32_16x16x32_bf16 v[64:67], v[152:155], v[184:187], v[64:67]
	v_mfma_f32_16x16x32_bf16 v[60:63], v[160:163], v[184:187], v[60:63]
	v_mfma_f32_16x16x32_bf16 v[56:59], v[152:155], v[192:195], v[56:59]
	v_mfma_f32_16x16x32_bf16 v[52:55], v[160:163], v[192:195], v[52:55]
	v_mfma_f32_16x16x32_bf16 v[40:43], v[152:155], v[204:207], v[40:43]
	v_mfma_f32_16x16x32_bf16 v[36:39], v[160:163], v[204:207], v[36:39]
	v_mfma_f32_16x16x32_bf16 v[24:27], v[152:155], v[212:215], v[24:27]
	v_mfma_f32_16x16x32_bf16 v[20:23], v[160:163], v[212:215], v[20:23]
	v_mfma_f32_16x16x32_bf16 v[48:51], v[164:167], v[180:183], v[48:51]
	v_mfma_f32_16x16x32_bf16 v[44:47], v[172:175], v[180:183], v[44:47]
	v_mfma_f32_16x16x32_bf16 v[32:35], v[164:167], v[188:191], v[32:35]
	v_mfma_f32_16x16x32_bf16 v[28:31], v[172:175], v[188:191], v[28:31]
	v_mfma_f32_16x16x32_bf16 v[16:19], v[164:167], v[196:199], v[16:19]
	v_mfma_f32_16x16x32_bf16 v[12:15], v[172:175], v[196:199], v[12:15]
	v_mfma_f32_16x16x32_bf16 v[8:11], v[164:167], v[208:211], v[8:11]
	v_mfma_f32_16x16x32_bf16 v[4:7], v[172:175], v[208:211], v[4:7]
	v_mfma_f32_16x16x32_bf16 v[48:51], v[168:171], v[184:187], v[48:51]
	v_mfma_f32_16x16x32_bf16 v[44:47], v[176:179], v[184:187], v[44:47]
	v_mfma_f32_16x16x32_bf16 v[32:35], v[168:171], v[192:195], v[32:35]
	v_mfma_f32_16x16x32_bf16 v[28:31], v[176:179], v[192:195], v[28:31]
	v_mfma_f32_16x16x32_bf16 v[16:19], v[168:171], v[204:207], v[16:19]
	v_mfma_f32_16x16x32_bf16 v[12:15], v[176:179], v[204:207], v[12:15]
	v_mfma_f32_16x16x32_bf16 v[8:11], v[168:171], v[212:215], v[8:11]
	v_mfma_f32_16x16x32_bf16 v[4:7], v[176:179], v[212:215], v[4:7]
	s_barrier
	s_add_i32 s69, s69, 2
	s_add_u32 s44, s44, 0x100
	s_addc_u32 s45, s45, 0
	s_cmp_gt_u32 s69, 13
.LBB0_1206:
	s_add_u32 s4, s22, s44
	s_addc_u32 s5, s23, s45
	s_add_u32 s70, s4, 0x100
	s_addc_u32 s71, s5, 0
	s_add_u32 s48, s65, s44
	s_addc_u32 s49, s68, s45
	s_add_u32 s4, s4, 0x180
	s_addc_u32 s5, s5, 0
	s_add_i32 s72, 0, 0x10000
	s_add_i32 s73, 0, 0x14000
	v_add_u32_e32 v160, s72, v146
	v_add_u32_e32 v176, s73, v146
	ds_read_b128 v[148:151], v160
	ds_read_b128 v[152:155], v160 offset:1024
	ds_read_b128 v[156:159], v160 offset:2048
	ds_read_b128 v[160:163], v160 offset:3072
	ds_read_b128 v[164:167], v176
	ds_read_b128 v[168:171], v176 offset:1024
	ds_read_b128 v[172:175], v176 offset:2048
	ds_read_b128 v[176:179], v176 offset:3072
	s_cmpk_eq_i32 s44, 0x700
	s_cselect_b32 s13, s64, s5
	s_cselect_b32 s12, s63, s4
	s_cselect_b32 s49, s21, s49
	s_cselect_b32 s48, s62, s48
	s_cselect_b32 s5, s37, s71
	s_cselect_b32 s4, s61, s70
	v_lshl_add_u64 v[216:217], v[142:143], 0, s[44:45]
	s_add_i32 m0, s17, 0xc000
	ds_read_b128 v[180:183], v147
	ds_read_b128 v[184:187], v147 offset:1024
	ds_read_b128 v[188:191], v147 offset:2048
	ds_read_b128 v[192:195], v147 offset:3072
	ds_read_b128 v[196:199], v147 offset:4096
	ds_read_b128 v[204:207], v147 offset:5120
	ds_read_b128 v[208:211], v147 offset:6144
	ds_read_b128 v[212:215], v147 offset:7168
	global_load_lds_dwordx4 v[216:217], off
	v_lshl_add_u64 v[216:217], v[144:145], 0, s[44:45]
	s_add_i32 m0, s17, 0xe000
	s_nop 0
	global_load_lds_dwordx4 v[216:217], off
	s_waitcnt vmcnt(8)
	s_waitcnt lgkmcnt(0)
	s_barrier
	v_mfma_f32_16x16x32_bf16 v[128:131], v[148:151], v[180:183], v[128:131]
	v_mfma_f32_16x16x32_bf16 v[124:127], v[156:159], v[180:183], v[124:127]
	v_mfma_f32_16x16x32_bf16 v[120:123], v[148:151], v[188:191], v[120:123]
	v_mfma_f32_16x16x32_bf16 v[116:119], v[156:159], v[188:191], v[116:119]
	v_mfma_f32_16x16x32_bf16 v[104:107], v[148:151], v[196:199], v[104:107]
	v_mfma_f32_16x16x32_bf16 v[100:103], v[156:159], v[196:199], v[100:103]
	v_mfma_f32_16x16x32_bf16 v[88:91], v[148:151], v[208:211], v[88:91]
	v_mfma_f32_16x16x32_bf16 v[84:87], v[156:159], v[208:211], v[84:87]
	v_mfma_f32_16x16x32_bf16 v[128:131], v[152:155], v[184:187], v[128:131]
	v_mfma_f32_16x16x32_bf16 v[124:127], v[160:163], v[184:187], v[124:127]
	v_mfma_f32_16x16x32_bf16 v[120:123], v[152:155], v[192:195], v[120:123]
	v_mfma_f32_16x16x32_bf16 v[116:119], v[160:163], v[192:195], v[116:119]
	v_mfma_f32_16x16x32_bf16 v[104:107], v[152:155], v[204:207], v[104:107]
	v_mfma_f32_16x16x32_bf16 v[100:103], v[160:163], v[204:207], v[100:103]
	v_mfma_f32_16x16x32_bf16 v[88:91], v[152:155], v[212:215], v[88:91]
	v_mfma_f32_16x16x32_bf16 v[84:87], v[160:163], v[212:215], v[84:87]
	v_mfma_f32_16x16x32_bf16 v[112:115], v[164:167], v[180:183], v[112:115]
	v_mfma_f32_16x16x32_bf16 v[108:111], v[172:175], v[180:183], v[108:111]
	v_mfma_f32_16x16x32_bf16 v[96:99], v[164:167], v[188:191], v[96:99]
	v_mfma_f32_16x16x32_bf16 v[92:95], v[172:175], v[188:191], v[92:95]
	v_mfma_f32_16x16x32_bf16 v[80:83], v[164:167], v[196:199], v[80:83]
	v_mfma_f32_16x16x32_bf16 v[76:79], v[172:175], v[196:199], v[76:79]
	v_mfma_f32_16x16x32_bf16 v[72:75], v[164:167], v[208:211], v[72:75]
	v_mfma_f32_16x16x32_bf16 v[68:71], v[172:175], v[208:211], v[68:71]
	v_mfma_f32_16x16x32_bf16 v[112:115], v[168:171], v[184:187], v[112:115]
	v_mfma_f32_16x16x32_bf16 v[108:111], v[176:179], v[184:187], v[108:111]
	v_mfma_f32_16x16x32_bf16 v[96:99], v[168:171], v[192:195], v[96:99]
	v_mfma_f32_16x16x32_bf16 v[92:95], v[176:179], v[192:195], v[92:95]
	v_mfma_f32_16x16x32_bf16 v[80:83], v[168:171], v[204:207], v[80:83]
	v_mfma_f32_16x16x32_bf16 v[76:79], v[176:179], v[204:207], v[76:79]
	v_mfma_f32_16x16x32_bf16 v[72:75], v[168:171], v[212:215], v[72:75]
	v_mfma_f32_16x16x32_bf16 v[68:71], v[176:179], v[212:215], v[68:71]
	s_barrier
	s_add_i32 s70, s72, s16
	v_lshl_add_u64 v[216:217], s[48:49], 0, v[2:3]
	s_mov_b32 m0, s70
	ds_read_b128 v[180:183], v147 offset:16384
	ds_read_b128 v[184:187], v147 offset:17408
	ds_read_b128 v[188:191], v147 offset:18432
	ds_read_b128 v[192:195], v147 offset:19456
	ds_read_b128 v[196:199], v147 offset:20480
	ds_read_b128 v[204:207], v147 offset:21504
	ds_read_b128 v[208:211], v147 offset:22528
	ds_read_b128 v[212:215], v147 offset:23552
	global_load_lds_dwordx4 v[216:217], off
	s_add_i32 m0, s70, 0x2000
	s_add_u32 s70, s48, 0x40000
	v_lshl_add_u64 v[218:219], s[48:49], 0, v[132:133]
	s_addc_u32 s71, s49, 0
	s_add_i32 s72, s73, s16
	global_load_lds_dwordx4 v[218:219], off
	v_lshl_add_u64 v[220:221], s[70:71], 0, v[2:3]
	s_mov_b32 m0, s72
	s_nop 0
	global_load_lds_dwordx4 v[220:221], off
	v_lshl_add_u64 v[220:221], s[70:71], 0, v[132:133]
	s_add_i32 m0, s72, 0x2000
	s_nop 0
	global_load_lds_dwordx4 v[220:221], off
	v_lshl_add_u64 v[220:221], s[4:5], 0, v[136:137]
	s_mov_b32 m0, s17
	s_nop 0
	global_load_lds_dwordx4 v[220:221], off
	v_lshl_add_u64 v[220:221], s[4:5], 0, v[134:135]
	s_mov_b32 m0, s46
	s_nop 0
	global_load_lds_dwordx4 v[220:221], off
	s_waitcnt vmcnt(8)
	s_waitcnt lgkmcnt(0)
	s_barrier
	v_mfma_f32_16x16x32_bf16 v[64:67], v[148:151], v[180:183], v[64:67]
	v_mfma_f32_16x16x32_bf16 v[60:63], v[156:159], v[180:183], v[60:63]
	v_mfma_f32_16x16x32_bf16 v[56:59], v[148:151], v[188:191], v[56:59]
	v_mfma_f32_16x16x32_bf16 v[52:55], v[156:159], v[188:191], v[52:55]
	v_mfma_f32_16x16x32_bf16 v[40:43], v[148:151], v[196:199], v[40:43]
	v_mfma_f32_16x16x32_bf16 v[36:39], v[156:159], v[196:199], v[36:39]
	v_mfma_f32_16x16x32_bf16 v[24:27], v[148:151], v[208:211], v[24:27]
	v_mfma_f32_16x16x32_bf16 v[20:23], v[156:159], v[208:211], v[20:23]
	v_mfma_f32_16x16x32_bf16 v[64:67], v[152:155], v[184:187], v[64:67]
	v_mfma_f32_16x16x32_bf16 v[60:63], v[160:163], v[184:187], v[60:63]
	v_mfma_f32_16x16x32_bf16 v[56:59], v[152:155], v[192:195], v[56:59]
	v_mfma_f32_16x16x32_bf16 v[52:55], v[160:163], v[192:195], v[52:55]
	v_mfma_f32_16x16x32_bf16 v[40:43], v[152:155], v[204:207], v[40:43]
	v_mfma_f32_16x16x32_bf16 v[36:39], v[160:163], v[204:207], v[36:39]
	v_mfma_f32_16x16x32_bf16 v[24:27], v[152:155], v[212:215], v[24:27]
	v_mfma_f32_16x16x32_bf16 v[20:23], v[160:163], v[212:215], v[20:23]
	v_mfma_f32_16x16x32_bf16 v[48:51], v[164:167], v[180:183], v[48:51]
	v_mfma_f32_16x16x32_bf16 v[44:47], v[172:175], v[180:183], v[44:47]
	v_mfma_f32_16x16x32_bf16 v[32:35], v[164:167], v[188:191], v[32:35]
	v_mfma_f32_16x16x32_bf16 v[28:31], v[172:175], v[188:191], v[28:31]
	v_mfma_f32_16x16x32_bf16 v[16:19], v[164:167], v[196:199], v[16:19]
	v_mfma_f32_16x16x32_bf16 v[12:15], v[172:175], v[196:199], v[12:15]
	v_mfma_f32_16x16x32_bf16 v[8:11], v[164:167], v[208:211], v[8:11]
	v_mfma_f32_16x16x32_bf16 v[4:7], v[172:175], v[208:211], v[4:7]
	v_mfma_f32_16x16x32_bf16 v[48:51], v[168:171], v[184:187], v[48:51]
	v_mfma_f32_16x16x32_bf16 v[44:47], v[176:179], v[184:187], v[44:47]
	v_mfma_f32_16x16x32_bf16 v[32:35], v[168:171], v[192:195], v[32:35]
	v_mfma_f32_16x16x32_bf16 v[28:31], v[176:179], v[192:195], v[28:31]
	v_mfma_f32_16x16x32_bf16 v[16:19], v[168:171], v[204:207], v[16:19]
	v_mfma_f32_16x16x32_bf16 v[12:15], v[176:179], v[204:207], v[12:15]
	v_mfma_f32_16x16x32_bf16 v[8:11], v[168:171], v[212:215], v[8:11]
	v_mfma_f32_16x16x32_bf16 v[4:7], v[176:179], v[212:215], v[4:7]
	s_barrier
	s_add_i32 s70, 0, 0x18000
	s_add_i32 s71, 0, 0x1c000
	v_add_u32_e32 v160, s70, v146
	v_add_u32_e32 v176, s71, v146
	ds_read_b128 v[148:151], v160
	ds_read_b128 v[152:155], v160 offset:1024
	ds_read_b128 v[156:159], v160 offset:2048
	ds_read_b128 v[160:163], v160 offset:3072
	ds_read_b128 v[164:167], v176
	ds_read_b128 v[168:171], v176 offset:1024
	ds_read_b128 v[172:175], v176 offset:2048
	ds_read_b128 v[176:179], v176 offset:3072
	s_add_u32 s4, s4, 0x40000
	s_addc_u32 s5, s5, 0
	s_mov_b32 m0, s47
	v_lshl_add_u64 v[220:221], s[4:5], 0, v[136:137]
	ds_read_b128 v[180:183], v147 offset:32768
	ds_read_b128 v[184:187], v147 offset:33792
	ds_read_b128 v[188:191], v147 offset:34816
	ds_read_b128 v[192:195], v147 offset:35840
	ds_read_b128 v[196:199], v147 offset:36864
	ds_read_b128 v[204:207], v147 offset:37888
	ds_read_b128 v[208:211], v147 offset:38912
	ds_read_b128 v[212:215], v147 offset:39936
	global_load_lds_dwordx4 v[220:221], off
	v_lshl_add_u64 v[220:221], s[4:5], 0, v[134:135]
	s_mov_b32 m0, s50
	s_nop 0
	global_load_lds_dwordx4 v[220:221], off
	s_waitcnt vmcnt(8)
	s_waitcnt lgkmcnt(0)
	s_barrier
	v_mfma_f32_16x16x32_bf16 v[128:131], v[148:151], v[180:183], v[128:131]
	v_mfma_f32_16x16x32_bf16 v[124:127], v[156:159], v[180:183], v[124:127]
	v_mfma_f32_16x16x32_bf16 v[120:123], v[148:151], v[188:191], v[120:123]
	v_mfma_f32_16x16x32_bf16 v[116:119], v[156:159], v[188:191], v[116:119]
	v_mfma_f32_16x16x32_bf16 v[104:107], v[148:151], v[196:199], v[104:107]
	v_mfma_f32_16x16x32_bf16 v[100:103], v[156:159], v[196:199], v[100:103]
	v_mfma_f32_16x16x32_bf16 v[88:91], v[148:151], v[208:211], v[88:91]
	v_mfma_f32_16x16x32_bf16 v[84:87], v[156:159], v[208:211], v[84:87]
	v_mfma_f32_16x16x32_bf16 v[128:131], v[152:155], v[184:187], v[128:131]
	v_mfma_f32_16x16x32_bf16 v[124:127], v[160:163], v[184:187], v[124:127]
	v_mfma_f32_16x16x32_bf16 v[120:123], v[152:155], v[192:195], v[120:123]
	v_mfma_f32_16x16x32_bf16 v[116:119], v[160:163], v[192:195], v[116:119]
	v_mfma_f32_16x16x32_bf16 v[104:107], v[152:155], v[204:207], v[104:107]
	v_mfma_f32_16x16x32_bf16 v[100:103], v[160:163], v[204:207], v[100:103]
	v_mfma_f32_16x16x32_bf16 v[88:91], v[152:155], v[212:215], v[88:91]
	v_mfma_f32_16x16x32_bf16 v[84:87], v[160:163], v[212:215], v[84:87]
	v_mfma_f32_16x16x32_bf16 v[112:115], v[164:167], v[180:183], v[112:115]
	v_mfma_f32_16x16x32_bf16 v[108:111], v[172:175], v[180:183], v[108:111]
	v_mfma_f32_16x16x32_bf16 v[96:99], v[164:167], v[188:191], v[96:99]
	v_mfma_f32_16x16x32_bf16 v[92:95], v[172:175], v[188:191], v[92:95]
	v_mfma_f32_16x16x32_bf16 v[80:83], v[164:167], v[196:199], v[80:83]
	v_mfma_f32_16x16x32_bf16 v[76:79], v[172:175], v[196:199], v[76:79]
	v_mfma_f32_16x16x32_bf16 v[72:75], v[164:167], v[208:211], v[72:75]
	v_mfma_f32_16x16x32_bf16 v[68:71], v[172:175], v[208:211], v[68:71]
	v_mfma_f32_16x16x32_bf16 v[112:115], v[168:171], v[184:187], v[112:115]
	v_mfma_f32_16x16x32_bf16 v[108:111], v[176:179], v[184:187], v[108:111]
	v_mfma_f32_16x16x32_bf16 v[96:99], v[168:171], v[192:195], v[96:99]
	v_mfma_f32_16x16x32_bf16 v[92:95], v[176:179], v[192:195], v[92:95]
	v_mfma_f32_16x16x32_bf16 v[80:83], v[168:171], v[204:207], v[80:83]
	v_mfma_f32_16x16x32_bf16 v[76:79], v[176:179], v[204:207], v[76:79]
	v_mfma_f32_16x16x32_bf16 v[72:75], v[168:171], v[212:215], v[72:75]
	v_mfma_f32_16x16x32_bf16 v[68:71], v[176:179], v[212:215], v[68:71]
	s_barrier
	s_add_i32 s4, s70, s16
	v_lshl_add_u64 v[216:217], v[216:217], 0, s[34:35]
	s_mov_b32 m0, s4
	ds_read_b128 v[180:183], v147 offset:49152
	ds_read_b128 v[184:187], v147 offset:50176
	ds_read_b128 v[188:191], v147 offset:51200
	ds_read_b128 v[192:195], v147 offset:52224
	ds_read_b128 v[196:199], v147 offset:53248
	ds_read_b128 v[204:207], v147 offset:54272
	ds_read_b128 v[208:211], v147 offset:55296
	ds_read_b128 v[212:215], v147 offset:56320
	global_load_lds_dwordx4 v[216:217], off
	s_add_i32 m0, s4, 0x2000
	s_add_u32 s4, s48, 0x40080
	v_lshl_add_u64 v[216:217], v[218:219], 0, s[34:35]
	s_addc_u32 s5, s49, 0
	s_add_i32 s48, s71, s16
	global_load_lds_dwordx4 v[216:217], off
	v_lshl_add_u64 v[216:217], s[4:5], 0, v[2:3]
	s_mov_b32 m0, s48
	s_nop 0
	global_load_lds_dwordx4 v[216:217], off
	v_lshl_add_u64 v[216:217], s[4:5], 0, v[132:133]
	s_add_i32 m0, s48, 0x2000
	s_nop 0
	global_load_lds_dwordx4 v[216:217], off
	v_lshl_add_u64 v[216:217], s[12:13], 0, v[136:137]
	s_mov_b32 m0, s53
	s_nop 0
	global_load_lds_dwordx4 v[216:217], off
	v_lshl_add_u64 v[216:217], s[12:13], 0, v[134:135]
	s_mov_b32 m0, s56
	s_nop 0
	global_load_lds_dwordx4 v[216:217], off
	s_waitcnt vmcnt(8)
	s_waitcnt lgkmcnt(0)
	s_barrier
	v_mfma_f32_16x16x32_bf16 v[64:67], v[148:151], v[180:183], v[64:67]
	v_mfma_f32_16x16x32_bf16 v[60:63], v[156:159], v[180:183], v[60:63]
	v_mfma_f32_16x16x32_bf16 v[56:59], v[148:151], v[188:191], v[56:59]
	v_mfma_f32_16x16x32_bf16 v[52:55], v[156:159], v[188:191], v[52:55]
	v_mfma_f32_16x16x32_bf16 v[40:43], v[148:151], v[196:199], v[40:43]
	v_mfma_f32_16x16x32_bf16 v[36:39], v[156:159], v[196:199], v[36:39]
	v_mfma_f32_16x16x32_bf16 v[24:27], v[148:151], v[208:211], v[24:27]
	v_mfma_f32_16x16x32_bf16 v[20:23], v[156:159], v[208:211], v[20:23]
	v_mfma_f32_16x16x32_bf16 v[64:67], v[152:155], v[184:187], v[64:67]
	v_mfma_f32_16x16x32_bf16 v[60:63], v[160:163], v[184:187], v[60:63]
	v_mfma_f32_16x16x32_bf16 v[56:59], v[152:155], v[192:195], v[56:59]
	v_mfma_f32_16x16x32_bf16 v[52:55], v[160:163], v[192:195], v[52:55]
	v_mfma_f32_16x16x32_bf16 v[40:43], v[152:155], v[204:207], v[40:43]
	v_mfma_f32_16x16x32_bf16 v[36:39], v[160:163], v[204:207], v[36:39]
	v_mfma_f32_16x16x32_bf16 v[24:27], v[152:155], v[212:215], v[24:27]
	v_mfma_f32_16x16x32_bf16 v[20:23], v[160:163], v[212:215], v[20:23]
	v_mfma_f32_16x16x32_bf16 v[48:51], v[164:167], v[180:183], v[48:51]
	v_mfma_f32_16x16x32_bf16 v[44:47], v[172:175], v[180:183], v[44:47]
	v_mfma_f32_16x16x32_bf16 v[32:35], v[164:167], v[188:191], v[32:35]
	v_mfma_f32_16x16x32_bf16 v[28:31], v[172:175], v[188:191], v[28:31]
	v_mfma_f32_16x16x32_bf16 v[16:19], v[164:167], v[196:199], v[16:19]
	v_mfma_f32_16x16x32_bf16 v[12:15], v[172:175], v[196:199], v[12:15]
	v_mfma_f32_16x16x32_bf16 v[8:11], v[164:167], v[208:211], v[8:11]
	v_mfma_f32_16x16x32_bf16 v[4:7], v[172:175], v[208:211], v[4:7]
	v_mfma_f32_16x16x32_bf16 v[48:51], v[168:171], v[184:187], v[48:51]
	v_mfma_f32_16x16x32_bf16 v[44:47], v[176:179], v[184:187], v[44:47]
	v_mfma_f32_16x16x32_bf16 v[32:35], v[168:171], v[192:195], v[32:35]
	v_mfma_f32_16x16x32_bf16 v[28:31], v[176:179], v[192:195], v[28:31]
	v_mfma_f32_16x16x32_bf16 v[16:19], v[168:171], v[204:207], v[16:19]
	v_mfma_f32_16x16x32_bf16 v[12:15], v[176:179], v[204:207], v[12:15]
	v_mfma_f32_16x16x32_bf16 v[8:11], v[168:171], v[212:215], v[8:11]
	v_mfma_f32_16x16x32_bf16 v[4:7], v[176:179], v[212:215], v[4:7]
	s_barrier
	s_add_i32 s69, s69, 2
	s_add_u32 s44, s44, 0x100
	s_addc_u32 s45, s45, 0
	s_cmp_gt_u32 s69, 13
	s_cbranch_scc0 .LBB0_1206
	s_and_b64 vcc, exec, s[18:19]
	s_mov_b32 s62, 0x18000
	s_mov_b32 s63, 0x1a000
	s_cbranch_vccz .LBB0_1209
	s_barrier

.LBB0_1379:
	s_ashr_i32 s43, s42, 31
	s_lshl_b64 s[4:5], s[42:43], 19
	s_add_u32 s44, s6, s4
	s_addc_u32 s45, s7, s5
	s_and_b64 s[4:5], s[38:39], exec
	s_cselect_b32 s43, s45, s41
	s_cselect_b32 s68, s44, s40
	s_ashr_i32 s37, s36, 31
	s_lshl_b64 s[4:5], s[36:37], 19
	s_add_u32 s48, s8, s4
	s_addc_u32 s49, s9, s5
	s_and_b64 s[4:5], s[38:39], exec
	s_cselect_b32 s37, s49, s51
	s_cselect_b32 s69, s48, s50
	s_add_u32 s70, s68, 0x80
	s_addc_u32 s71, s43, 0
	s_add_u32 s4, s40, 0x40080
	s_addc_u32 s5, s41, 0
	s_add_u32 s72, s50, 0x100
	v_lshl_add_u64 v[144:145], s[4:5], 0, v[140:141]
	v_lshl_add_u64 v[146:147], s[4:5], 0, v[142:143]
	s_addc_u32 s73, s51, 0
	s_mov_b32 s74, -2
	s_mov_b64 s[50:51], 0
	s_waitcnt vmcnt(0)
	s_add_u32 s4, s40, s50
	s_addc_u32 s5, s41, s51
	s_add_u32 s75, s4, 0x100
	s_addc_u32 s76, s5, 0
	s_add_u32 s52, s72, s50
	s_addc_u32 s53, s73, s51
	s_add_u32 s4, s4, 0x180
	s_addc_u32 s5, s5, 0
	s_add_i32 s77, 0, 0x10000
	s_add_i32 s78, 0, 0x14000
	v_add_u32_e32 v2, s77, v160
	ds_read_b128 v[148:151], v2
	ds_read_b128 v[152:155], v2 offset:1024
	ds_read_b128 v[156:159], v2 offset:2048
	ds_read_b128 v[162:165], v2 offset:3072
	v_add_u32_e32 v2, s78, v160
	ds_read_b128 v[166:169], v2
	s_waitcnt lgkmcnt(0)
	ds_read_b128 v[170:173], v2 offset:1024
	ds_read_b128 v[174:177], v2 offset:2048
	ds_read_b128 v[178:181], v2 offset:3072
	s_cmpk_eq_i32 s50, 0x700
	s_cselect_b32 s13, s71, s5
	s_cselect_b32 s12, s70, s4
	s_cselect_b32 s53, s37, s53
	s_cselect_b32 s52, s69, s52
	s_cselect_b32 s5, s43, s76
	s_cselect_b32 s4, s68, s75
	v_lshl_add_u64 v[198:199], v[144:145], 0, s[50:51]
	s_add_i32 m0, s17, 0xc000
	ds_read_b128 v[182:185], v161
	ds_read_b128 v[186:189], v161 offset:1024
	ds_read_b128 v[190:193], v161 offset:2048
	ds_read_b128 v[194:197], v161 offset:3072
	ds_read_b128 v[204:207], v161 offset:4096
	ds_read_b128 v[208:211], v161 offset:5120
	ds_read_b128 v[212:215], v161 offset:6144
	ds_read_b128 v[216:219], v161 offset:7168
	global_load_lds_dwordx4 v[198:199], off
	v_lshl_add_u64 v[198:199], v[146:147], 0, s[50:51]
	s_add_i32 m0, s17, 0xe000
	s_nop 0
	global_load_lds_dwordx4 v[198:199], off
	s_waitcnt vmcnt(8)
	s_waitcnt lgkmcnt(0)
	s_barrier
	v_mfma_f32_16x16x32_bf16 v[128:131], v[148:151], v[182:185], 0
	v_mfma_f32_16x16x32_bf16 v[124:127], v[156:159], v[182:185], 0
	v_mfma_f32_16x16x32_bf16 v[112:115], v[148:151], v[190:193], 0
	v_mfma_f32_16x16x32_bf16 v[108:111], v[156:159], v[190:193], 0
	v_mfma_f32_16x16x32_bf16 v[96:99], v[148:151], v[204:207], 0
	v_mfma_f32_16x16x32_bf16 v[92:95], v[156:159], v[204:207], 0
	v_mfma_f32_16x16x32_bf16 v[80:83], v[148:151], v[212:215], 0
	v_mfma_f32_16x16x32_bf16 v[76:79], v[156:159], v[212:215], 0
	v_mfma_f32_16x16x32_bf16 v[128:131], v[152:155], v[186:189], v[128:131]
	v_mfma_f32_16x16x32_bf16 v[124:127], v[162:165], v[186:189], v[124:127]
	v_mfma_f32_16x16x32_bf16 v[112:115], v[152:155], v[194:197], v[112:115]
	v_mfma_f32_16x16x32_bf16 v[108:111], v[162:165], v[194:197], v[108:111]
	v_mfma_f32_16x16x32_bf16 v[96:99], v[152:155], v[208:211], v[96:99]
	v_mfma_f32_16x16x32_bf16 v[92:95], v[162:165], v[208:211], v[92:95]
	v_mfma_f32_16x16x32_bf16 v[80:83], v[152:155], v[216:219], v[80:83]
	v_mfma_f32_16x16x32_bf16 v[76:79], v[162:165], v[216:219], v[76:79]
	v_mfma_f32_16x16x32_bf16 v[120:123], v[166:169], v[182:185], 0
	v_mfma_f32_16x16x32_bf16 v[116:119], v[174:177], v[182:185], 0
	v_mfma_f32_16x16x32_bf16 v[104:107], v[166:169], v[190:193], 0
	v_mfma_f32_16x16x32_bf16 v[100:103], v[174:177], v[190:193], 0
	v_mfma_f32_16x16x32_bf16 v[88:91], v[166:169], v[204:207], 0
	v_mfma_f32_16x16x32_bf16 v[84:87], v[174:177], v[204:207], 0
	v_mfma_f32_16x16x32_bf16 v[72:75], v[166:169], v[212:215], 0
	v_mfma_f32_16x16x32_bf16 v[68:71], v[174:177], v[212:215], 0
	v_mfma_f32_16x16x32_bf16 v[120:123], v[170:173], v[186:189], v[120:123]
	v_mfma_f32_16x16x32_bf16 v[116:119], v[178:181], v[186:189], v[116:119]
	v_mfma_f32_16x16x32_bf16 v[104:107], v[170:173], v[194:197], v[104:107]
	v_mfma_f32_16x16x32_bf16 v[100:103], v[178:181], v[194:197], v[100:103]
	v_mfma_f32_16x16x32_bf16 v[88:91], v[170:173], v[208:211], v[88:91]
	v_mfma_f32_16x16x32_bf16 v[84:87], v[178:181], v[208:211], v[84:87]
	v_mfma_f32_16x16x32_bf16 v[72:75], v[170:173], v[216:219], v[72:75]
	v_mfma_f32_16x16x32_bf16 v[68:71], v[178:181], v[216:219], v[68:71]
	s_barrier
	s_add_i32 s75, s77, s16
	v_lshl_add_u64 v[198:199], s[52:53], 0, v[136:137]
	s_mov_b32 m0, s75
	ds_read_b128 v[182:185], v161 offset:16384
	ds_read_b128 v[186:189], v161 offset:17408
	ds_read_b128 v[190:193], v161 offset:18432
	ds_read_b128 v[194:197], v161 offset:19456
	ds_read_b128 v[204:207], v161 offset:20480
	ds_read_b128 v[208:211], v161 offset:21504
	ds_read_b128 v[212:215], v161 offset:22528
	ds_read_b128 v[216:219], v161 offset:23552
	global_load_lds_dwordx4 v[198:199], off
	s_add_i32 m0, s75, 0x2000
	s_add_u32 s76, s52, 0x40000
	v_lshl_add_u64 v[220:221], s[52:53], 0, v[132:133]
	s_addc_u32 s77, s53, 0
	s_add_i32 s75, s78, s16
	global_load_lds_dwordx4 v[220:221], off
	v_lshl_add_u64 v[222:223], s[76:77], 0, v[136:137]
	s_mov_b32 m0, s75
	s_nop 0
	global_load_lds_dwordx4 v[222:223], off
	v_lshl_add_u64 v[222:223], s[76:77], 0, v[132:133]
	s_add_i32 m0, s75, 0x2000
	s_nop 0
	global_load_lds_dwordx4 v[222:223], off
	v_lshl_add_u64 v[222:223], s[4:5], 0, v[138:139]
	s_mov_b32 m0, s17
	s_nop 0
	global_load_lds_dwordx4 v[222:223], off
	v_lshl_add_u64 v[222:223], s[4:5], 0, v[134:135]
	s_mov_b32 m0, s46
	s_nop 0
	global_load_lds_dwordx4 v[222:223], off
	s_waitcnt vmcnt(8)
	s_waitcnt lgkmcnt(0)
	s_barrier
	v_mfma_f32_16x16x32_bf16 v[64:67], v[148:151], v[182:185], 0
	v_mfma_f32_16x16x32_bf16 v[60:63], v[156:159], v[182:185], 0
	v_mfma_f32_16x16x32_bf16 v[48:51], v[148:151], v[190:193], 0
	v_mfma_f32_16x16x32_bf16 v[44:47], v[156:159], v[190:193], 0
	v_mfma_f32_16x16x32_bf16 v[32:35], v[148:151], v[204:207], 0
	v_mfma_f32_16x16x32_bf16 v[28:31], v[156:159], v[204:207], 0
	v_mfma_f32_16x16x32_bf16 v[16:19], v[148:151], v[212:215], 0
	v_mfma_f32_16x16x32_bf16 v[12:15], v[156:159], v[212:215], 0
	v_mfma_f32_16x16x32_bf16 v[64:67], v[152:155], v[186:189], v[64:67]
	v_mfma_f32_16x16x32_bf16 v[60:63], v[162:165], v[186:189], v[60:63]
	v_mfma_f32_16x16x32_bf16 v[48:51], v[152:155], v[194:197], v[48:51]
	v_mfma_f32_16x16x32_bf16 v[44:47], v[162:165], v[194:197], v[44:47]
	v_mfma_f32_16x16x32_bf16 v[32:35], v[152:155], v[208:211], v[32:35]
	v_mfma_f32_16x16x32_bf16 v[28:31], v[162:165], v[208:211], v[28:31]
	v_mfma_f32_16x16x32_bf16 v[16:19], v[152:155], v[216:219], v[16:19]
	v_mfma_f32_16x16x32_bf16 v[12:15], v[162:165], v[216:219], v[12:15]
	v_mfma_f32_16x16x32_bf16 v[56:59], v[166:169], v[182:185], 0
	v_mfma_f32_16x16x32_bf16 v[52:55], v[174:177], v[182:185], 0
	v_mfma_f32_16x16x32_bf16 v[40:43], v[166:169], v[190:193], 0
	v_mfma_f32_16x16x32_bf16 v[36:39], v[174:177], v[190:193], 0
	v_mfma_f32_16x16x32_bf16 v[24:27], v[166:169], v[204:207], 0
	v_mfma_f32_16x16x32_bf16 v[20:23], v[174:177], v[204:207], 0
	v_mfma_f32_16x16x32_bf16 v[8:11], v[166:169], v[212:215], 0
	v_mfma_f32_16x16x32_bf16 v[4:7], v[174:177], v[212:215], 0
	v_mfma_f32_16x16x32_bf16 v[56:59], v[170:173], v[186:189], v[56:59]
	v_mfma_f32_16x16x32_bf16 v[52:55], v[178:181], v[186:189], v[52:55]
	v_mfma_f32_16x16x32_bf16 v[40:43], v[170:173], v[194:197], v[40:43]
	v_mfma_f32_16x16x32_bf16 v[36:39], v[178:181], v[194:197], v[36:39]
	v_mfma_f32_16x16x32_bf16 v[24:27], v[170:173], v[208:211], v[24:27]
	v_mfma_f32_16x16x32_bf16 v[20:23], v[178:181], v[208:211], v[20:23]
	v_mfma_f32_16x16x32_bf16 v[8:11], v[170:173], v[216:219], v[8:11]
	v_mfma_f32_16x16x32_bf16 v[4:7], v[178:181], v[216:219], v[4:7]
	s_barrier
	s_add_i32 s75, 0, 0x18000
	v_add_u32_e32 v2, s75, v160
	s_add_i32 s76, 0, 0x1c000
	ds_read_b128 v[148:151], v2
	ds_read_b128 v[152:155], v2 offset:1024
	ds_read_b128 v[156:159], v2 offset:2048
	ds_read_b128 v[162:165], v2 offset:3072
	v_add_u32_e32 v2, s76, v160
	ds_read_b128 v[166:169], v2
	ds_read_b128 v[170:173], v2 offset:1024
	ds_read_b128 v[174:177], v2 offset:2048
	ds_read_b128 v[178:181], v2 offset:3072
	s_add_u32 s4, s4, 0x40000
	s_addc_u32 s5, s5, 0
	s_mov_b32 m0, s47
	v_lshl_add_u64 v[222:223], s[4:5], 0, v[138:139]
	ds_read_b128 v[182:185], v161 offset:32768
	ds_read_b128 v[186:189], v161 offset:33792
	ds_read_b128 v[190:193], v161 offset:34816
	ds_read_b128 v[194:197], v161 offset:35840
	ds_read_b128 v[204:207], v161 offset:36864
	ds_read_b128 v[208:211], v161 offset:37888
	ds_read_b128 v[212:215], v161 offset:38912
	ds_read_b128 v[216:219], v161 offset:39936
	global_load_lds_dwordx4 v[222:223], off
	v_lshl_add_u64 v[222:223], s[4:5], 0, v[134:135]
	s_mov_b32 m0, s56
	s_nop 0
	global_load_lds_dwordx4 v[222:223], off
	s_waitcnt vmcnt(8)
	s_waitcnt lgkmcnt(0)
	s_barrier
	v_mfma_f32_16x16x32_bf16 v[128:131], v[148:151], v[182:185], v[128:131]
	v_mfma_f32_16x16x32_bf16 v[124:127], v[156:159], v[182:185], v[124:127]
	v_mfma_f32_16x16x32_bf16 v[112:115], v[148:151], v[190:193], v[112:115]
	v_mfma_f32_16x16x32_bf16 v[108:111], v[156:159], v[190:193], v[108:111]
	v_mfma_f32_16x16x32_bf16 v[96:99], v[148:151], v[204:207], v[96:99]
	v_mfma_f32_16x16x32_bf16 v[92:95], v[156:159], v[204:207], v[92:95]
	v_mfma_f32_16x16x32_bf16 v[80:83], v[148:151], v[212:215], v[80:83]
	v_mfma_f32_16x16x32_bf16 v[76:79], v[156:159], v[212:215], v[76:79]
	v_mfma_f32_16x16x32_bf16 v[128:131], v[152:155], v[186:189], v[128:131]
	v_mfma_f32_16x16x32_bf16 v[124:127], v[162:165], v[186:189], v[124:127]
	v_mfma_f32_16x16x32_bf16 v[112:115], v[152:155], v[194:197], v[112:115]
	v_mfma_f32_16x16x32_bf16 v[108:111], v[162:165], v[194:197], v[108:111]
	v_mfma_f32_16x16x32_bf16 v[96:99], v[152:155], v[208:211], v[96:99]
	v_mfma_f32_16x16x32_bf16 v[92:95], v[162:165], v[208:211], v[92:95]
	v_mfma_f32_16x16x32_bf16 v[80:83], v[152:155], v[216:219], v[80:83]
	v_mfma_f32_16x16x32_bf16 v[76:79], v[162:165], v[216:219], v[76:79]
	v_mfma_f32_16x16x32_bf16 v[120:123], v[166:169], v[182:185], v[120:123]
	v_mfma_f32_16x16x32_bf16 v[116:119], v[174:177], v[182:185], v[116:119]
	v_mfma_f32_16x16x32_bf16 v[104:107], v[166:169], v[190:193], v[104:107]
	v_mfma_f32_16x16x32_bf16 v[100:103], v[174:177], v[190:193], v[100:103]
	v_mfma_f32_16x16x32_bf16 v[88:91], v[166:169], v[204:207], v[88:91]
	v_mfma_f32_16x16x32_bf16 v[84:87], v[174:177], v[204:207], v[84:87]
	v_mfma_f32_16x16x32_bf16 v[72:75], v[166:169], v[212:215], v[72:75]
	v_mfma_f32_16x16x32_bf16 v[68:71], v[174:177], v[212:215], v[68:71]
	v_mfma_f32_16x16x32_bf16 v[120:123], v[170:173], v[186:189], v[120:123]
	v_mfma_f32_16x16x32_bf16 v[116:119], v[178:181], v[186:189], v[116:119]
	v_mfma_f32_16x16x32_bf16 v[104:107], v[170:173], v[194:197], v[104:107]
	v_mfma_f32_16x16x32_bf16 v[100:103], v[178:181], v[194:197], v[100:103]
	v_mfma_f32_16x16x32_bf16 v[88:91], v[170:173], v[208:211], v[88:91]
	v_mfma_f32_16x16x32_bf16 v[84:87], v[178:181], v[208:211], v[84:87]
	v_mfma_f32_16x16x32_bf16 v[72:75], v[170:173], v[216:219], v[72:75]
	v_mfma_f32_16x16x32_bf16 v[68:71], v[178:181], v[216:219], v[68:71]
	s_barrier
	s_add_i32 s4, s75, s16
	v_lshl_add_u64 v[198:199], v[198:199], 0, s[34:35]
	s_mov_b32 m0, s4
	ds_read_b128 v[182:185], v161 offset:49152
	ds_read_b128 v[186:189], v161 offset:50176
	ds_read_b128 v[190:193], v161 offset:51200
	ds_read_b128 v[194:197], v161 offset:52224
	ds_read_b128 v[204:207], v161 offset:53248
	ds_read_b128 v[208:211], v161 offset:54272
	ds_read_b128 v[212:215], v161 offset:55296
	ds_read_b128 v[216:219], v161 offset:56320
	global_load_lds_dwordx4 v[198:199], off
	s_add_i32 m0, s4, 0x2000
	s_add_u32 s4, s52, 0x40080
	v_lshl_add_u64 v[198:199], v[220:221], 0, s[34:35]
	s_addc_u32 s5, s53, 0
	s_add_i32 s52, s76, s16
	global_load_lds_dwordx4 v[198:199], off
	v_lshl_add_u64 v[198:199], s[4:5], 0, v[136:137]
	s_mov_b32 m0, s52
	s_nop 0
	global_load_lds_dwordx4 v[198:199], off
	v_lshl_add_u64 v[198:199], s[4:5], 0, v[132:133]
	s_add_i32 m0, s52, 0x2000
	s_nop 0
	global_load_lds_dwordx4 v[198:199], off
	v_lshl_add_u64 v[198:199], s[12:13], 0, v[138:139]
	s_mov_b32 m0, s61
	s_nop 0
	global_load_lds_dwordx4 v[198:199], off
	v_lshl_add_u64 v[198:199], s[12:13], 0, v[134:135]
	s_mov_b32 m0, s62
	s_nop 0
	global_load_lds_dwordx4 v[198:199], off
	s_waitcnt vmcnt(8)
	s_waitcnt lgkmcnt(0)
	s_barrier
	v_mfma_f32_16x16x32_bf16 v[64:67], v[148:151], v[182:185], v[64:67]
	v_mfma_f32_16x16x32_bf16 v[60:63], v[156:159], v[182:185], v[60:63]
	v_mfma_f32_16x16x32_bf16 v[48:51], v[148:151], v[190:193], v[48:51]
	v_mfma_f32_16x16x32_bf16 v[44:47], v[156:159], v[190:193], v[44:47]
	v_mfma_f32_16x16x32_bf16 v[32:35], v[148:151], v[204:207], v[32:35]
	v_mfma_f32_16x16x32_bf16 v[28:31], v[156:159], v[204:207], v[28:31]
	v_mfma_f32_16x16x32_bf16 v[16:19], v[148:151], v[212:215], v[16:19]
	v_mfma_f32_16x16x32_bf16 v[12:15], v[156:159], v[212:215], v[12:15]
	v_mfma_f32_16x16x32_bf16 v[64:67], v[152:155], v[186:189], v[64:67]
	v_mfma_f32_16x16x32_bf16 v[60:63], v[162:165], v[186:189], v[60:63]
	v_mfma_f32_16x16x32_bf16 v[48:51], v[152:155], v[194:197], v[48:51]
	v_mfma_f32_16x16x32_bf16 v[44:47], v[162:165], v[194:197], v[44:47]
	v_mfma_f32_16x16x32_bf16 v[32:35], v[152:155], v[208:211], v[32:35]
	v_mfma_f32_16x16x32_bf16 v[28:31], v[162:165], v[208:211], v[28:31]
	v_mfma_f32_16x16x32_bf16 v[16:19], v[152:155], v[216:219], v[16:19]
	v_mfma_f32_16x16x32_bf16 v[12:15], v[162:165], v[216:219], v[12:15]
	v_mfma_f32_16x16x32_bf16 v[56:59], v[166:169], v[182:185], v[56:59]
	v_mfma_f32_16x16x32_bf16 v[52:55], v[174:177], v[182:185], v[52:55]
	v_mfma_f32_16x16x32_bf16 v[40:43], v[166:169], v[190:193], v[40:43]
	v_mfma_f32_16x16x32_bf16 v[36:39], v[174:177], v[190:193], v[36:39]
	v_mfma_f32_16x16x32_bf16 v[24:27], v[166:169], v[204:207], v[24:27]
	v_mfma_f32_16x16x32_bf16 v[20:23], v[174:177], v[204:207], v[20:23]
	v_mfma_f32_16x16x32_bf16 v[8:11], v[166:169], v[212:215], v[8:11]
	v_mfma_f32_16x16x32_bf16 v[4:7], v[174:177], v[212:215], v[4:7]
	v_mfma_f32_16x16x32_bf16 v[56:59], v[170:173], v[186:189], v[56:59]
	v_mfma_f32_16x16x32_bf16 v[52:55], v[178:181], v[186:189], v[52:55]
	v_mfma_f32_16x16x32_bf16 v[40:43], v[170:173], v[194:197], v[40:43]
	v_mfma_f32_16x16x32_bf16 v[36:39], v[178:181], v[194:197], v[36:39]
	v_mfma_f32_16x16x32_bf16 v[24:27], v[170:173], v[208:211], v[24:27]
	v_mfma_f32_16x16x32_bf16 v[20:23], v[178:181], v[208:211], v[20:23]
	v_mfma_f32_16x16x32_bf16 v[8:11], v[170:173], v[216:219], v[8:11]
	v_mfma_f32_16x16x32_bf16 v[4:7], v[178:181], v[216:219], v[4:7]
	s_barrier
	s_add_i32 s74, s74, 2
	s_add_u32 s50, s50, 0x100
	s_addc_u32 s51, s51, 0
	s_cmp_gt_u32 s74, 13
.LBB0_1380:
	s_add_u32 s4, s40, s50
	s_addc_u32 s5, s41, s51
	s_add_u32 s75, s4, 0x100
	s_addc_u32 s76, s5, 0
	s_add_u32 s52, s72, s50
	s_addc_u32 s53, s73, s51
	s_add_u32 s4, s4, 0x180
	s_addc_u32 s5, s5, 0
	s_add_i32 s77, 0, 0x10000
	s_add_i32 s78, 0, 0x14000
	v_add_u32_e32 v2, s77, v160
	ds_read_b128 v[148:151], v2
	ds_read_b128 v[152:155], v2 offset:1024
	ds_read_b128 v[156:159], v2 offset:2048
	ds_read_b128 v[162:165], v2 offset:3072
	v_add_u32_e32 v2, s78, v160
	ds_read_b128 v[166:169], v2
	ds_read_b128 v[170:173], v2 offset:1024
	ds_read_b128 v[174:177], v2 offset:2048
	ds_read_b128 v[178:181], v2 offset:3072
	s_cmpk_eq_i32 s50, 0x700
	s_cselect_b32 s13, s71, s5
	s_cselect_b32 s12, s70, s4
	s_cselect_b32 s53, s37, s53
	s_cselect_b32 s52, s69, s52
	s_cselect_b32 s5, s43, s76
	s_cselect_b32 s4, s68, s75
	v_lshl_add_u64 v[198:199], v[144:145], 0, s[50:51]
	s_add_i32 m0, s17, 0xc000
	ds_read_b128 v[182:185], v161
	ds_read_b128 v[186:189], v161 offset:1024
	ds_read_b128 v[190:193], v161 offset:2048
	ds_read_b128 v[194:197], v161 offset:3072
	ds_read_b128 v[204:207], v161 offset:4096
	ds_read_b128 v[208:211], v161 offset:5120
	ds_read_b128 v[212:215], v161 offset:6144
	ds_read_b128 v[216:219], v161 offset:7168
	global_load_lds_dwordx4 v[198:199], off
	v_lshl_add_u64 v[198:199], v[146:147], 0, s[50:51]
	s_add_i32 m0, s17, 0xe000
	s_nop 0
	global_load_lds_dwordx4 v[198:199], off
	s_waitcnt vmcnt(8)
	s_waitcnt lgkmcnt(0)
	s_barrier
	v_mfma_f32_16x16x32_bf16 v[128:131], v[148:151], v[182:185], v[128:131]
	v_mfma_f32_16x16x32_bf16 v[124:127], v[156:159], v[182:185], v[124:127]
	v_mfma_f32_16x16x32_bf16 v[112:115], v[148:151], v[190:193], v[112:115]
	v_mfma_f32_16x16x32_bf16 v[108:111], v[156:159], v[190:193], v[108:111]
	v_mfma_f32_16x16x32_bf16 v[96:99], v[148:151], v[204:207], v[96:99]
	v_mfma_f32_16x16x32_bf16 v[92:95], v[156:159], v[204:207], v[92:95]
	v_mfma_f32_16x16x32_bf16 v[80:83], v[148:151], v[212:215], v[80:83]
	v_mfma_f32_16x16x32_bf16 v[76:79], v[156:159], v[212:215], v[76:79]
	v_mfma_f32_16x16x32_bf16 v[128:131], v[152:155], v[186:189], v[128:131]
	v_mfma_f32_16x16x32_bf16 v[124:127], v[162:165], v[186:189], v[124:127]
	v_mfma_f32_16x16x32_bf16 v[112:115], v[152:155], v[194:197], v[112:115]
	v_mfma_f32_16x16x32_bf16 v[108:111], v[162:165], v[194:197], v[108:111]
	v_mfma_f32_16x16x32_bf16 v[96:99], v[152:155], v[208:211], v[96:99]
	v_mfma_f32_16x16x32_bf16 v[92:95], v[162:165], v[208:211], v[92:95]
	v_mfma_f32_16x16x32_bf16 v[80:83], v[152:155], v[216:219], v[80:83]
	v_mfma_f32_16x16x32_bf16 v[76:79], v[162:165], v[216:219], v[76:79]
	v_mfma_f32_16x16x32_bf16 v[120:123], v[166:169], v[182:185], v[120:123]
	v_mfma_f32_16x16x32_bf16 v[116:119], v[174:177], v[182:185], v[116:119]
	v_mfma_f32_16x16x32_bf16 v[104:107], v[166:169], v[190:193], v[104:107]
	v_mfma_f32_16x16x32_bf16 v[100:103], v[174:177], v[190:193], v[100:103]
	v_mfma_f32_16x16x32_bf16 v[88:91], v[166:169], v[204:207], v[88:91]
	v_mfma_f32_16x16x32_bf16 v[84:87], v[174:177], v[204:207], v[84:87]
	v_mfma_f32_16x16x32_bf16 v[72:75], v[166:169], v[212:215], v[72:75]
	v_mfma_f32_16x16x32_bf16 v[68:71], v[174:177], v[212:215], v[68:71]
	v_mfma_f32_16x16x32_bf16 v[120:123], v[170:173], v[186:189], v[120:123]
	v_mfma_f32_16x16x32_bf16 v[116:119], v[178:181], v[186:189], v[116:119]
	v_mfma_f32_16x16x32_bf16 v[104:107], v[170:173], v[194:197], v[104:107]
	v_mfma_f32_16x16x32_bf16 v[100:103], v[178:181], v[194:197], v[100:103]
	v_mfma_f32_16x16x32_bf16 v[88:91], v[170:173], v[208:211], v[88:91]
	v_mfma_f32_16x16x32_bf16 v[84:87], v[178:181], v[208:211], v[84:87]
	v_mfma_f32_16x16x32_bf16 v[72:75], v[170:173], v[216:219], v[72:75]
	v_mfma_f32_16x16x32_bf16 v[68:71], v[178:181], v[216:219], v[68:71]
	s_barrier
	s_add_i32 s75, s77, s16
	v_lshl_add_u64 v[198:199], s[52:53], 0, v[136:137]
	s_mov_b32 m0, s75
	ds_read_b128 v[182:185], v161 offset:16384
	ds_read_b128 v[186:189], v161 offset:17408
	ds_read_b128 v[190:193], v161 offset:18432
	ds_read_b128 v[194:197], v161 offset:19456
	ds_read_b128 v[204:207], v161 offset:20480
	ds_read_b128 v[208:211], v161 offset:21504
	ds_read_b128 v[212:215], v161 offset:22528
	ds_read_b128 v[216:219], v161 offset:23552
	global_load_lds_dwordx4 v[198:199], off
	s_add_i32 m0, s75, 0x2000
	s_add_u32 s76, s52, 0x40000
	v_lshl_add_u64 v[220:221], s[52:53], 0, v[132:133]
	s_addc_u32 s77, s53, 0
	s_add_i32 s75, s78, s16
	global_load_lds_dwordx4 v[220:221], off
	v_lshl_add_u64 v[222:223], s[76:77], 0, v[136:137]
	s_mov_b32 m0, s75
	s_nop 0
	global_load_lds_dwordx4 v[222:223], off
	v_lshl_add_u64 v[222:223], s[76:77], 0, v[132:133]
	s_add_i32 m0, s75, 0x2000
	s_nop 0
	global_load_lds_dwordx4 v[222:223], off
	v_lshl_add_u64 v[222:223], s[4:5], 0, v[138:139]
	s_mov_b32 m0, s17
	s_nop 0
	global_load_lds_dwordx4 v[222:223], off
	v_lshl_add_u64 v[222:223], s[4:5], 0, v[134:135]
	s_mov_b32 m0, s46
	s_nop 0
	global_load_lds_dwordx4 v[222:223], off
	s_waitcnt vmcnt(8)
	s_waitcnt lgkmcnt(0)
	s_barrier
	v_mfma_f32_16x16x32_bf16 v[64:67], v[148:151], v[182:185], v[64:67]
	v_mfma_f32_16x16x32_bf16 v[60:63], v[156:159], v[182:185], v[60:63]
	v_mfma_f32_16x16x32_bf16 v[48:51], v[148:151], v[190:193], v[48:51]
	v_mfma_f32_16x16x32_bf16 v[44:47], v[156:159], v[190:193], v[44:47]
	v_mfma_f32_16x16x32_bf16 v[32:35], v[148:151], v[204:207], v[32:35]
	v_mfma_f32_16x16x32_bf16 v[28:31], v[156:159], v[204:207], v[28:31]
	v_mfma_f32_16x16x32_bf16 v[16:19], v[148:151], v[212:215], v[16:19]
	v_mfma_f32_16x16x32_bf16 v[12:15], v[156:159], v[212:215], v[12:15]
	v_mfma_f32_16x16x32_bf16 v[64:67], v[152:155], v[186:189], v[64:67]
	v_mfma_f32_16x16x32_bf16 v[60:63], v[162:165], v[186:189], v[60:63]
	v_mfma_f32_16x16x32_bf16 v[48:51], v[152:155], v[194:197], v[48:51]
	v_mfma_f32_16x16x32_bf16 v[44:47], v[162:165], v[194:197], v[44:47]
	v_mfma_f32_16x16x32_bf16 v[32:35], v[152:155], v[208:211], v[32:35]
	v_mfma_f32_16x16x32_bf16 v[28:31], v[162:165], v[208:211], v[28:31]
	v_mfma_f32_16x16x32_bf16 v[16:19], v[152:155], v[216:219], v[16:19]
	v_mfma_f32_16x16x32_bf16 v[12:15], v[162:165], v[216:219], v[12:15]
	v_mfma_f32_16x16x32_bf16 v[56:59], v[166:169], v[182:185], v[56:59]
	v_mfma_f32_16x16x32_bf16 v[52:55], v[174:177], v[182:185], v[52:55]
	v_mfma_f32_16x16x32_bf16 v[40:43], v[166:169], v[190:193], v[40:43]
	v_mfma_f32_16x16x32_bf16 v[36:39], v[174:177], v[190:193], v[36:39]
	v_mfma_f32_16x16x32_bf16 v[24:27], v[166:169], v[204:207], v[24:27]
	v_mfma_f32_16x16x32_bf16 v[20:23], v[174:177], v[204:207], v[20:23]
	v_mfma_f32_16x16x32_bf16 v[8:11], v[166:169], v[212:215], v[8:11]
	v_mfma_f32_16x16x32_bf16 v[4:7], v[174:177], v[212:215], v[4:7]
	v_mfma_f32_16x16x32_bf16 v[56:59], v[170:173], v[186:189], v[56:59]
	v_mfma_f32_16x16x32_bf16 v[52:55], v[178:181], v[186:189], v[52:55]
	v_mfma_f32_16x16x32_bf16 v[40:43], v[170:173], v[194:197], v[40:43]
	v_mfma_f32_16x16x32_bf16 v[36:39], v[178:181], v[194:197], v[36:39]
	v_mfma_f32_16x16x32_bf16 v[24:27], v[170:173], v[208:211], v[24:27]
	v_mfma_f32_16x16x32_bf16 v[20:23], v[178:181], v[208:211], v[20:23]
	v_mfma_f32_16x16x32_bf16 v[8:11], v[170:173], v[216:219], v[8:11]
	v_mfma_f32_16x16x32_bf16 v[4:7], v[178:181], v[216:219], v[4:7]
	s_barrier
	s_add_i32 s75, 0, 0x18000
	v_add_u32_e32 v2, s75, v160
	s_add_i32 s76, 0, 0x1c000
	ds_read_b128 v[148:151], v2
	ds_read_b128 v[152:155], v2 offset:1024
	ds_read_b128 v[156:159], v2 offset:2048
	ds_read_b128 v[162:165], v2 offset:3072
	v_add_u32_e32 v2, s76, v160
	ds_read_b128 v[166:169], v2
	ds_read_b128 v[170:173], v2 offset:1024
	ds_read_b128 v[174:177], v2 offset:2048
	ds_read_b128 v[178:181], v2 offset:3072
	s_add_u32 s4, s4, 0x40000
	s_addc_u32 s5, s5, 0
	s_mov_b32 m0, s47
	v_lshl_add_u64 v[222:223], s[4:5], 0, v[138:139]
	ds_read_b128 v[182:185], v161 offset:32768
	ds_read_b128 v[186:189], v161 offset:33792
	ds_read_b128 v[190:193], v161 offset:34816
	ds_read_b128 v[194:197], v161 offset:35840
	ds_read_b128 v[204:207], v161 offset:36864
	ds_read_b128 v[208:211], v161 offset:37888
	ds_read_b128 v[212:215], v161 offset:38912
	ds_read_b128 v[216:219], v161 offset:39936
	global_load_lds_dwordx4 v[222:223], off
	v_lshl_add_u64 v[222:223], s[4:5], 0, v[134:135]
	s_mov_b32 m0, s56
	s_nop 0
	global_load_lds_dwordx4 v[222:223], off
	s_waitcnt vmcnt(8)
	s_waitcnt lgkmcnt(0)
	s_barrier
	v_mfma_f32_16x16x32_bf16 v[128:131], v[148:151], v[182:185], v[128:131]
	v_mfma_f32_16x16x32_bf16 v[124:127], v[156:159], v[182:185], v[124:127]
	v_mfma_f32_16x16x32_bf16 v[112:115], v[148:151], v[190:193], v[112:115]
	v_mfma_f32_16x16x32_bf16 v[108:111], v[156:159], v[190:193], v[108:111]
	v_mfma_f32_16x16x32_bf16 v[96:99], v[148:151], v[204:207], v[96:99]
	v_mfma_f32_16x16x32_bf16 v[92:95], v[156:159], v[204:207], v[92:95]
	v_mfma_f32_16x16x32_bf16 v[80:83], v[148:151], v[212:215], v[80:83]
	v_mfma_f32_16x16x32_bf16 v[76:79], v[156:159], v[212:215], v[76:79]
	v_mfma_f32_16x16x32_bf16 v[128:131], v[152:155], v[186:189], v[128:131]
	v_mfma_f32_16x16x32_bf16 v[124:127], v[162:165], v[186:189], v[124:127]
	v_mfma_f32_16x16x32_bf16 v[112:115], v[152:155], v[194:197], v[112:115]
	v_mfma_f32_16x16x32_bf16 v[108:111], v[162:165], v[194:197], v[108:111]
	v_mfma_f32_16x16x32_bf16 v[96:99], v[152:155], v[208:211], v[96:99]
	v_mfma_f32_16x16x32_bf16 v[92:95], v[162:165], v[208:211], v[92:95]
	v_mfma_f32_16x16x32_bf16 v[80:83], v[152:155], v[216:219], v[80:83]
	v_mfma_f32_16x16x32_bf16 v[76:79], v[162:165], v[216:219], v[76:79]
	v_mfma_f32_16x16x32_bf16 v[120:123], v[166:169], v[182:185], v[120:123]
	v_mfma_f32_16x16x32_bf16 v[116:119], v[174:177], v[182:185], v[116:119]
	v_mfma_f32_16x16x32_bf16 v[104:107], v[166:169], v[190:193], v[104:107]
	v_mfma_f32_16x16x32_bf16 v[100:103], v[174:177], v[190:193], v[100:103]
	v_mfma_f32_16x16x32_bf16 v[88:91], v[166:169], v[204:207], v[88:91]
	v_mfma_f32_16x16x32_bf16 v[84:87], v[174:177], v[204:207], v[84:87]
	v_mfma_f32_16x16x32_bf16 v[72:75], v[166:169], v[212:215], v[72:75]
	v_mfma_f32_16x16x32_bf16 v[68:71], v[174:177], v[212:215], v[68:71]
	v_mfma_f32_16x16x32_bf16 v[120:123], v[170:173], v[186:189], v[120:123]
	v_mfma_f32_16x16x32_bf16 v[116:119], v[178:181], v[186:189], v[116:119]
	v_mfma_f32_16x16x32_bf16 v[104:107], v[170:173], v[194:197], v[104:107]
	v_mfma_f32_16x16x32_bf16 v[100:103], v[178:181], v[194:197], v[100:103]
	v_mfma_f32_16x16x32_bf16 v[88:91], v[170:173], v[208:211], v[88:91]
	v_mfma_f32_16x16x32_bf16 v[84:87], v[178:181], v[208:211], v[84:87]
	v_mfma_f32_16x16x32_bf16 v[72:75], v[170:173], v[216:219], v[72:75]
	v_mfma_f32_16x16x32_bf16 v[68:71], v[178:181], v[216:219], v[68:71]
	s_barrier
	s_add_i32 s4, s75, s16
	v_lshl_add_u64 v[198:199], v[198:199], 0, s[34:35]
	s_mov_b32 m0, s4
	ds_read_b128 v[182:185], v161 offset:49152
	ds_read_b128 v[186:189], v161 offset:50176
	ds_read_b128 v[190:193], v161 offset:51200
	ds_read_b128 v[194:197], v161 offset:52224
	ds_read_b128 v[204:207], v161 offset:53248
	ds_read_b128 v[208:211], v161 offset:54272
	ds_read_b128 v[212:215], v161 offset:55296
	ds_read_b128 v[216:219], v161 offset:56320
	global_load_lds_dwordx4 v[198:199], off
	s_add_i32 m0, s4, 0x2000
	s_add_u32 s4, s52, 0x40080
	v_lshl_add_u64 v[198:199], v[220:221], 0, s[34:35]
	s_addc_u32 s5, s53, 0
	s_add_i32 s52, s76, s16
	global_load_lds_dwordx4 v[198:199], off
	v_lshl_add_u64 v[198:199], s[4:5], 0, v[136:137]
	s_mov_b32 m0, s52
	s_nop 0
	global_load_lds_dwordx4 v[198:199], off
	v_lshl_add_u64 v[198:199], s[4:5], 0, v[132:133]
	s_add_i32 m0, s52, 0x2000
	s_nop 0
	global_load_lds_dwordx4 v[198:199], off
	v_lshl_add_u64 v[198:199], s[12:13], 0, v[138:139]
	s_mov_b32 m0, s61
	s_nop 0
	global_load_lds_dwordx4 v[198:199], off
	v_lshl_add_u64 v[198:199], s[12:13], 0, v[134:135]
	s_mov_b32 m0, s62
	s_nop 0
	global_load_lds_dwordx4 v[198:199], off
	s_waitcnt vmcnt(8)
	s_waitcnt lgkmcnt(0)
	s_barrier
	v_mfma_f32_16x16x32_bf16 v[64:67], v[148:151], v[182:185], v[64:67]
	v_mfma_f32_16x16x32_bf16 v[60:63], v[156:159], v[182:185], v[60:63]
	v_mfma_f32_16x16x32_bf16 v[48:51], v[148:151], v[190:193], v[48:51]
	v_mfma_f32_16x16x32_bf16 v[44:47], v[156:159], v[190:193], v[44:47]
	v_mfma_f32_16x16x32_bf16 v[32:35], v[148:151], v[204:207], v[32:35]
	v_mfma_f32_16x16x32_bf16 v[28:31], v[156:159], v[204:207], v[28:31]
	v_mfma_f32_16x16x32_bf16 v[16:19], v[148:151], v[212:215], v[16:19]
	v_mfma_f32_16x16x32_bf16 v[12:15], v[156:159], v[212:215], v[12:15]
	v_mfma_f32_16x16x32_bf16 v[64:67], v[152:155], v[186:189], v[64:67]
	v_mfma_f32_16x16x32_bf16 v[60:63], v[162:165], v[186:189], v[60:63]
	v_mfma_f32_16x16x32_bf16 v[48:51], v[152:155], v[194:197], v[48:51]
	v_mfma_f32_16x16x32_bf16 v[44:47], v[162:165], v[194:197], v[44:47]
	v_mfma_f32_16x16x32_bf16 v[32:35], v[152:155], v[208:211], v[32:35]
	v_mfma_f32_16x16x32_bf16 v[28:31], v[162:165], v[208:211], v[28:31]
	v_mfma_f32_16x16x32_bf16 v[16:19], v[152:155], v[216:219], v[16:19]
	v_mfma_f32_16x16x32_bf16 v[12:15], v[162:165], v[216:219], v[12:15]
	v_mfma_f32_16x16x32_bf16 v[56:59], v[166:169], v[182:185], v[56:59]
	v_mfma_f32_16x16x32_bf16 v[52:55], v[174:177], v[182:185], v[52:55]
	v_mfma_f32_16x16x32_bf16 v[40:43], v[166:169], v[190:193], v[40:43]
	v_mfma_f32_16x16x32_bf16 v[36:39], v[174:177], v[190:193], v[36:39]
	v_mfma_f32_16x16x32_bf16 v[24:27], v[166:169], v[204:207], v[24:27]
	v_mfma_f32_16x16x32_bf16 v[20:23], v[174:177], v[204:207], v[20:23]
	v_mfma_f32_16x16x32_bf16 v[8:11], v[166:169], v[212:215], v[8:11]
	v_mfma_f32_16x16x32_bf16 v[4:7], v[174:177], v[212:215], v[4:7]
	v_mfma_f32_16x16x32_bf16 v[56:59], v[170:173], v[186:189], v[56:59]
	v_mfma_f32_16x16x32_bf16 v[52:55], v[178:181], v[186:189], v[52:55]
	v_mfma_f32_16x16x32_bf16 v[40:43], v[170:173], v[194:197], v[40:43]
	v_mfma_f32_16x16x32_bf16 v[36:39], v[178:181], v[194:197], v[36:39]
	v_mfma_f32_16x16x32_bf16 v[24:27], v[170:173], v[208:211], v[24:27]
	v_mfma_f32_16x16x32_bf16 v[20:23], v[178:181], v[208:211], v[20:23]
	v_mfma_f32_16x16x32_bf16 v[8:11], v[170:173], v[216:219], v[8:11]
	v_mfma_f32_16x16x32_bf16 v[4:7], v[178:181], v[216:219], v[4:7]
	s_barrier
	s_add_i32 s74, s74, 2
	s_add_u32 s50, s50, 0x100
	s_addc_u32 s51, s51, 0
	s_cmp_gt_u32 s74, 13
	s_cbranch_scc0 .LBB0_1380
	s_and_b64 vcc, exec, s[22:23]
	s_cbranch_vccz .LBB0_1383
	s_barrier

.LBB0_1458:
	s_ashr_i32 s41, s40, 31
	s_lshl_b64 s[4:5], s[40:41], 21
	s_add_u32 s42, s6, s4
	s_addc_u32 s43, s7, s5
	s_and_b64 s[4:5], s[38:39], exec
	s_cselect_b32 s41, s43, s49
	s_cselect_b32 s68, s42, s48
	s_ashr_i32 s37, s36, 31
	s_lshl_b64 s[4:5], s[36:37], 21
	s_add_u32 s44, s8, s4
	s_addc_u32 s45, s9, s5
	s_and_b64 s[4:5], s[38:39], exec
	s_cselect_b32 s37, s45, s51
	s_cselect_b32 s69, s44, s50
	s_add_u32 s70, s68, 0x80
	s_addc_u32 s71, s41, 0
	s_add_u32 s72, s50, 0x100
	s_addc_u32 s73, s51, 0
	s_add_u32 s4, s48, 0x100080
	s_addc_u32 s5, s49, 0
	v_lshl_add_u64 v[112:113], s[4:5], 0, v[210:211]
	v_lshl_add_u64 v[114:115], s[4:5], 0, v[212:213]
	s_mov_b32 s74, -2
	s_mov_b64 s[50:51], 0
	s_waitcnt lgkmcnt(0)
	s_waitcnt vmcnt(0)
	s_add_u32 s4, s48, s50
	s_addc_u32 s5, s49, s51
	s_add_u32 s75, s4, 0x100
	s_addc_u32 s76, s5, 0
	s_add_u32 s52, s72, s50
	s_addc_u32 s53, s73, s51
	s_add_u32 s4, s4, 0x180
	s_addc_u32 s5, s5, 0
	s_add_i32 s77, 0, 0x10000
	s_add_i32 s78, 0, 0x14000
	v_add_u32_e32 v148, s77, v203
	v_add_u32_e32 v164, s78, v203
	ds_read_b128 v[120:123], v148
	ds_read_b128 v[132:135], v148 offset:1024
	ds_read_b128 v[144:147], v148 offset:2048
	ds_read_b128 v[148:151], v148 offset:3072
	ds_read_b128 v[152:155], v164
	ds_read_b128 v[156:159], v164 offset:1024
	ds_read_b128 v[160:163], v164 offset:2048
	ds_read_b128 v[164:167], v164 offset:3072
	s_cmpk_eq_i32 s50, 0x1f00
	s_cselect_b32 s13, s71, s5
	s_cselect_b32 s12, s70, s4
	s_cselect_b32 s53, s37, s53
	s_cselect_b32 s52, s69, s52
	s_cselect_b32 s5, s41, s76
	s_cselect_b32 s4, s68, s75
	v_lshl_add_u64 v[214:215], v[112:113], 0, s[50:51]
	s_add_i32 m0, s17, 0xc000
	ds_read_b128 v[168:171], v233
	ds_read_b128 v[172:175], v233 offset:1024
	ds_read_b128 v[176:179], v233 offset:2048
	ds_read_b128 v[180:183], v233 offset:3072
	ds_read_b128 v[184:187], v233 offset:4096
	ds_read_b128 v[188:191], v233 offset:5120
	ds_read_b128 v[192:195], v233 offset:6144
	ds_read_b128 v[196:199], v233 offset:7168
	global_load_lds_dwordx4 v[214:215], off
	v_lshl_add_u64 v[214:215], v[114:115], 0, s[50:51]
	s_add_i32 m0, s17, 0xe000
	s_nop 0
	global_load_lds_dwordx4 v[214:215], off
	s_waitcnt vmcnt(8)
	s_waitcnt lgkmcnt(0)
	s_barrier
	v_mfma_f32_16x16x32_bf16 v[140:143], v[120:123], v[168:171], 0
	v_mfma_f32_16x16x32_bf16 v[136:139], v[144:147], v[168:171], 0
	v_mfma_f32_16x16x32_bf16 v[116:119], v[120:123], v[176:179], 0
	v_mfma_f32_16x16x32_bf16 v[108:111], v[144:147], v[176:179], 0
	v_mfma_f32_16x16x32_bf16 v[96:99], v[120:123], v[184:187], 0
	v_mfma_f32_16x16x32_bf16 v[92:95], v[144:147], v[184:187], 0
	v_mfma_f32_16x16x32_bf16 v[80:83], v[120:123], v[192:195], 0
	v_mfma_f32_16x16x32_bf16 v[76:79], v[144:147], v[192:195], 0
	v_mfma_f32_16x16x32_bf16 v[140:143], v[132:135], v[172:175], v[140:143]
	v_mfma_f32_16x16x32_bf16 v[136:139], v[148:151], v[172:175], v[136:139]
	v_mfma_f32_16x16x32_bf16 v[116:119], v[132:135], v[180:183], v[116:119]
	v_mfma_f32_16x16x32_bf16 v[108:111], v[148:151], v[180:183], v[108:111]
	v_mfma_f32_16x16x32_bf16 v[96:99], v[132:135], v[188:191], v[96:99]
	v_mfma_f32_16x16x32_bf16 v[92:95], v[148:151], v[188:191], v[92:95]
	v_mfma_f32_16x16x32_bf16 v[80:83], v[132:135], v[196:199], v[80:83]
	v_mfma_f32_16x16x32_bf16 v[76:79], v[148:151], v[196:199], v[76:79]
	v_mfma_f32_16x16x32_bf16 v[128:131], v[152:155], v[168:171], 0
	v_mfma_f32_16x16x32_bf16 v[124:127], v[160:163], v[168:171], 0
	v_mfma_f32_16x16x32_bf16 v[104:107], v[152:155], v[176:179], 0
	v_mfma_f32_16x16x32_bf16 v[100:103], v[160:163], v[176:179], 0
	v_mfma_f32_16x16x32_bf16 v[88:91], v[152:155], v[184:187], 0
	v_mfma_f32_16x16x32_bf16 v[84:87], v[160:163], v[184:187], 0
	v_mfma_f32_16x16x32_bf16 v[72:75], v[152:155], v[192:195], 0
	v_mfma_f32_16x16x32_bf16 v[68:71], v[160:163], v[192:195], 0
	v_mfma_f32_16x16x32_bf16 v[128:131], v[156:159], v[172:175], v[128:131]
	v_mfma_f32_16x16x32_bf16 v[124:127], v[164:167], v[172:175], v[124:127]
	v_mfma_f32_16x16x32_bf16 v[104:107], v[156:159], v[180:183], v[104:107]
	v_mfma_f32_16x16x32_bf16 v[100:103], v[164:167], v[180:183], v[100:103]
	v_mfma_f32_16x16x32_bf16 v[88:91], v[156:159], v[188:191], v[88:91]
	v_mfma_f32_16x16x32_bf16 v[84:87], v[164:167], v[188:191], v[84:87]
	v_mfma_f32_16x16x32_bf16 v[72:75], v[156:159], v[196:199], v[72:75]
	v_mfma_f32_16x16x32_bf16 v[68:71], v[164:167], v[196:199], v[68:71]
	s_barrier
	s_add_i32 s75, s77, s16
	v_lshl_add_u64 v[214:215], s[52:53], 0, v[2:3]
	s_mov_b32 m0, s75
	ds_read_b128 v[168:171], v233 offset:16384
	ds_read_b128 v[172:175], v233 offset:17408
	ds_read_b128 v[176:179], v233 offset:18432
	ds_read_b128 v[180:183], v233 offset:19456
	ds_read_b128 v[184:187], v233 offset:20480
	ds_read_b128 v[188:191], v233 offset:21504
	ds_read_b128 v[192:195], v233 offset:22528
	ds_read_b128 v[196:199], v233 offset:23552
	global_load_lds_dwordx4 v[214:215], off
	s_add_i32 m0, s75, 0x2000
	s_add_u32 s76, s52, 0x100000
	v_lshl_add_u64 v[216:217], s[52:53], 0, v[204:205]
	s_addc_u32 s77, s53, 0
	s_add_i32 s75, s78, s16
	global_load_lds_dwordx4 v[216:217], off
	v_lshl_add_u64 v[218:219], s[76:77], 0, v[2:3]
	s_mov_b32 m0, s75
	s_nop 0
	global_load_lds_dwordx4 v[218:219], off
	v_lshl_add_u64 v[218:219], s[76:77], 0, v[204:205]
	s_add_i32 m0, s75, 0x2000
	s_nop 0
	global_load_lds_dwordx4 v[218:219], off
	v_lshl_add_u64 v[218:219], s[4:5], 0, v[208:209]
	s_mov_b32 m0, s17
	s_nop 0
	global_load_lds_dwordx4 v[218:219], off
	v_lshl_add_u64 v[218:219], s[4:5], 0, v[206:207]
	s_mov_b32 m0, s46
	s_nop 0
	global_load_lds_dwordx4 v[218:219], off
	s_waitcnt vmcnt(8)
	s_waitcnt lgkmcnt(0)
	s_barrier
	v_mfma_f32_16x16x32_bf16 v[64:67], v[120:123], v[168:171], 0
	v_mfma_f32_16x16x32_bf16 v[60:63], v[144:147], v[168:171], 0
	v_mfma_f32_16x16x32_bf16 v[48:51], v[120:123], v[176:179], 0
	v_mfma_f32_16x16x32_bf16 v[44:47], v[144:147], v[176:179], 0
	v_mfma_f32_16x16x32_bf16 v[32:35], v[120:123], v[184:187], 0
	v_mfma_f32_16x16x32_bf16 v[28:31], v[144:147], v[184:187], 0
	v_mfma_f32_16x16x32_bf16 v[16:19], v[120:123], v[192:195], 0
	v_mfma_f32_16x16x32_bf16 v[12:15], v[144:147], v[192:195], 0
	v_mfma_f32_16x16x32_bf16 v[64:67], v[132:135], v[172:175], v[64:67]
	v_mfma_f32_16x16x32_bf16 v[60:63], v[148:151], v[172:175], v[60:63]
	v_mfma_f32_16x16x32_bf16 v[48:51], v[132:135], v[180:183], v[48:51]
	v_mfma_f32_16x16x32_bf16 v[44:47], v[148:151], v[180:183], v[44:47]
	v_mfma_f32_16x16x32_bf16 v[32:35], v[132:135], v[188:191], v[32:35]
	v_mfma_f32_16x16x32_bf16 v[28:31], v[148:151], v[188:191], v[28:31]
	v_mfma_f32_16x16x32_bf16 v[16:19], v[132:135], v[196:199], v[16:19]
	v_mfma_f32_16x16x32_bf16 v[12:15], v[148:151], v[196:199], v[12:15]
	v_mfma_f32_16x16x32_bf16 v[56:59], v[152:155], v[168:171], 0
	v_mfma_f32_16x16x32_bf16 v[52:55], v[160:163], v[168:171], 0
	v_mfma_f32_16x16x32_bf16 v[40:43], v[152:155], v[176:179], 0
	v_mfma_f32_16x16x32_bf16 v[36:39], v[160:163], v[176:179], 0
	v_mfma_f32_16x16x32_bf16 v[24:27], v[152:155], v[184:187], 0
	v_mfma_f32_16x16x32_bf16 v[20:23], v[160:163], v[184:187], 0
	v_mfma_f32_16x16x32_bf16 v[8:11], v[152:155], v[192:195], 0
	v_mfma_f32_16x16x32_bf16 v[4:7], v[160:163], v[192:195], 0
	v_mfma_f32_16x16x32_bf16 v[56:59], v[156:159], v[172:175], v[56:59]
	v_mfma_f32_16x16x32_bf16 v[52:55], v[164:167], v[172:175], v[52:55]
	v_mfma_f32_16x16x32_bf16 v[40:43], v[156:159], v[180:183], v[40:43]
	v_mfma_f32_16x16x32_bf16 v[36:39], v[164:167], v[180:183], v[36:39]
	v_mfma_f32_16x16x32_bf16 v[24:27], v[156:159], v[188:191], v[24:27]
	v_mfma_f32_16x16x32_bf16 v[20:23], v[164:167], v[188:191], v[20:23]
	v_mfma_f32_16x16x32_bf16 v[8:11], v[156:159], v[196:199], v[8:11]
	v_mfma_f32_16x16x32_bf16 v[4:7], v[164:167], v[196:199], v[4:7]
	s_barrier
	s_add_i32 s75, 0, 0x18000
	s_add_i32 s76, 0, 0x1c000
	v_add_u32_e32 v148, s75, v203
	v_add_u32_e32 v164, s76, v203
	ds_read_b128 v[120:123], v148
	ds_read_b128 v[132:135], v148 offset:1024
	ds_read_b128 v[144:147], v148 offset:2048
	ds_read_b128 v[148:151], v148 offset:3072
	ds_read_b128 v[152:155], v164
	ds_read_b128 v[156:159], v164 offset:1024
	ds_read_b128 v[160:163], v164 offset:2048
	ds_read_b128 v[164:167], v164 offset:3072
	s_add_u32 s4, s4, 0x100000
	s_addc_u32 s5, s5, 0
	s_mov_b32 m0, s47
	v_lshl_add_u64 v[218:219], s[4:5], 0, v[208:209]
	ds_read_b128 v[168:171], v233 offset:32768
	ds_read_b128 v[172:175], v233 offset:33792
	ds_read_b128 v[176:179], v233 offset:34816
	ds_read_b128 v[180:183], v233 offset:35840
	ds_read_b128 v[184:187], v233 offset:36864
	ds_read_b128 v[188:191], v233 offset:37888
	ds_read_b128 v[192:195], v233 offset:38912
	ds_read_b128 v[196:199], v233 offset:39936
	global_load_lds_dwordx4 v[218:219], off
	v_lshl_add_u64 v[218:219], s[4:5], 0, v[206:207]
	s_mov_b32 m0, s58
	s_nop 0
	global_load_lds_dwordx4 v[218:219], off
	s_waitcnt vmcnt(8)
	s_waitcnt lgkmcnt(0)
	s_barrier
	v_mfma_f32_16x16x32_bf16 v[140:143], v[120:123], v[168:171], v[140:143]
	v_mfma_f32_16x16x32_bf16 v[136:139], v[144:147], v[168:171], v[136:139]
	v_mfma_f32_16x16x32_bf16 v[116:119], v[120:123], v[176:179], v[116:119]
	v_mfma_f32_16x16x32_bf16 v[108:111], v[144:147], v[176:179], v[108:111]
	v_mfma_f32_16x16x32_bf16 v[96:99], v[120:123], v[184:187], v[96:99]
	v_mfma_f32_16x16x32_bf16 v[92:95], v[144:147], v[184:187], v[92:95]
	v_mfma_f32_16x16x32_bf16 v[80:83], v[120:123], v[192:195], v[80:83]
	v_mfma_f32_16x16x32_bf16 v[76:79], v[144:147], v[192:195], v[76:79]
	v_mfma_f32_16x16x32_bf16 v[140:143], v[132:135], v[172:175], v[140:143]
	v_mfma_f32_16x16x32_bf16 v[136:139], v[148:151], v[172:175], v[136:139]
	v_mfma_f32_16x16x32_bf16 v[116:119], v[132:135], v[180:183], v[116:119]
	v_mfma_f32_16x16x32_bf16 v[108:111], v[148:151], v[180:183], v[108:111]
	v_mfma_f32_16x16x32_bf16 v[96:99], v[132:135], v[188:191], v[96:99]
	v_mfma_f32_16x16x32_bf16 v[92:95], v[148:151], v[188:191], v[92:95]
	v_mfma_f32_16x16x32_bf16 v[80:83], v[132:135], v[196:199], v[80:83]
	v_mfma_f32_16x16x32_bf16 v[76:79], v[148:151], v[196:199], v[76:79]
	v_mfma_f32_16x16x32_bf16 v[128:131], v[152:155], v[168:171], v[128:131]
	v_mfma_f32_16x16x32_bf16 v[124:127], v[160:163], v[168:171], v[124:127]
	v_mfma_f32_16x16x32_bf16 v[104:107], v[152:155], v[176:179], v[104:107]
	v_mfma_f32_16x16x32_bf16 v[100:103], v[160:163], v[176:179], v[100:103]
	v_mfma_f32_16x16x32_bf16 v[88:91], v[152:155], v[184:187], v[88:91]
	v_mfma_f32_16x16x32_bf16 v[84:87], v[160:163], v[184:187], v[84:87]
	v_mfma_f32_16x16x32_bf16 v[72:75], v[152:155], v[192:195], v[72:75]
	v_mfma_f32_16x16x32_bf16 v[68:71], v[160:163], v[192:195], v[68:71]
	v_mfma_f32_16x16x32_bf16 v[128:131], v[156:159], v[172:175], v[128:131]
	v_mfma_f32_16x16x32_bf16 v[124:127], v[164:167], v[172:175], v[124:127]
	v_mfma_f32_16x16x32_bf16 v[104:107], v[156:159], v[180:183], v[104:107]
	v_mfma_f32_16x16x32_bf16 v[100:103], v[164:167], v[180:183], v[100:103]
	v_mfma_f32_16x16x32_bf16 v[88:91], v[156:159], v[188:191], v[88:91]
	v_mfma_f32_16x16x32_bf16 v[84:87], v[164:167], v[188:191], v[84:87]
	v_mfma_f32_16x16x32_bf16 v[72:75], v[156:159], v[196:199], v[72:75]
	v_mfma_f32_16x16x32_bf16 v[68:71], v[164:167], v[196:199], v[68:71]
	s_barrier
	s_add_i32 s4, s75, s16
	v_lshl_add_u64 v[214:215], v[214:215], 0, s[34:35]
	s_mov_b32 m0, s4
	ds_read_b128 v[168:171], v233 offset:49152
	ds_read_b128 v[172:175], v233 offset:50176
	ds_read_b128 v[176:179], v233 offset:51200
	ds_read_b128 v[180:183], v233 offset:52224
	ds_read_b128 v[184:187], v233 offset:53248
	ds_read_b128 v[188:191], v233 offset:54272
	ds_read_b128 v[192:195], v233 offset:55296
	ds_read_b128 v[196:199], v233 offset:56320
	global_load_lds_dwordx4 v[214:215], off
	s_add_i32 m0, s4, 0x2000
	s_add_u32 s4, s52, 0x100080
	v_lshl_add_u64 v[214:215], v[216:217], 0, s[34:35]
	s_addc_u32 s5, s53, 0
	s_add_i32 s52, s76, s16
	global_load_lds_dwordx4 v[214:215], off
	v_lshl_add_u64 v[214:215], s[4:5], 0, v[2:3]
	s_mov_b32 m0, s52
	s_nop 0
	global_load_lds_dwordx4 v[214:215], off
	v_lshl_add_u64 v[214:215], s[4:5], 0, v[204:205]
	s_add_i32 m0, s52, 0x2000
	s_nop 0
	global_load_lds_dwordx4 v[214:215], off
	v_lshl_add_u64 v[214:215], s[12:13], 0, v[208:209]
	s_mov_b32 m0, s62
	s_nop 0
	global_load_lds_dwordx4 v[214:215], off
	v_lshl_add_u64 v[214:215], s[12:13], 0, v[206:207]
	s_mov_b32 m0, s63
	s_nop 0
	global_load_lds_dwordx4 v[214:215], off
	s_waitcnt vmcnt(8)
	s_waitcnt lgkmcnt(0)
	s_barrier
	v_mfma_f32_16x16x32_bf16 v[64:67], v[120:123], v[168:171], v[64:67]
	v_mfma_f32_16x16x32_bf16 v[60:63], v[144:147], v[168:171], v[60:63]
	v_mfma_f32_16x16x32_bf16 v[48:51], v[120:123], v[176:179], v[48:51]
	v_mfma_f32_16x16x32_bf16 v[44:47], v[144:147], v[176:179], v[44:47]
	v_mfma_f32_16x16x32_bf16 v[32:35], v[120:123], v[184:187], v[32:35]
	v_mfma_f32_16x16x32_bf16 v[28:31], v[144:147], v[184:187], v[28:31]
	v_mfma_f32_16x16x32_bf16 v[16:19], v[120:123], v[192:195], v[16:19]
	v_mfma_f32_16x16x32_bf16 v[12:15], v[144:147], v[192:195], v[12:15]
	v_mfma_f32_16x16x32_bf16 v[64:67], v[132:135], v[172:175], v[64:67]
	v_mfma_f32_16x16x32_bf16 v[60:63], v[148:151], v[172:175], v[60:63]
	v_mfma_f32_16x16x32_bf16 v[48:51], v[132:135], v[180:183], v[48:51]
	v_mfma_f32_16x16x32_bf16 v[44:47], v[148:151], v[180:183], v[44:47]
	v_mfma_f32_16x16x32_bf16 v[32:35], v[132:135], v[188:191], v[32:35]
	v_mfma_f32_16x16x32_bf16 v[28:31], v[148:151], v[188:191], v[28:31]
	v_mfma_f32_16x16x32_bf16 v[16:19], v[132:135], v[196:199], v[16:19]
	v_mfma_f32_16x16x32_bf16 v[12:15], v[148:151], v[196:199], v[12:15]
	v_mfma_f32_16x16x32_bf16 v[56:59], v[152:155], v[168:171], v[56:59]
	v_mfma_f32_16x16x32_bf16 v[52:55], v[160:163], v[168:171], v[52:55]
	v_mfma_f32_16x16x32_bf16 v[40:43], v[152:155], v[176:179], v[40:43]
	v_mfma_f32_16x16x32_bf16 v[36:39], v[160:163], v[176:179], v[36:39]
	v_mfma_f32_16x16x32_bf16 v[24:27], v[152:155], v[184:187], v[24:27]
	v_mfma_f32_16x16x32_bf16 v[20:23], v[160:163], v[184:187], v[20:23]
	v_mfma_f32_16x16x32_bf16 v[8:11], v[152:155], v[192:195], v[8:11]
	v_mfma_f32_16x16x32_bf16 v[4:7], v[160:163], v[192:195], v[4:7]
	v_mfma_f32_16x16x32_bf16 v[56:59], v[156:159], v[172:175], v[56:59]
	v_mfma_f32_16x16x32_bf16 v[52:55], v[164:167], v[172:175], v[52:55]
	v_mfma_f32_16x16x32_bf16 v[40:43], v[156:159], v[180:183], v[40:43]
	v_mfma_f32_16x16x32_bf16 v[36:39], v[164:167], v[180:183], v[36:39]
	v_mfma_f32_16x16x32_bf16 v[24:27], v[156:159], v[188:191], v[24:27]
	v_mfma_f32_16x16x32_bf16 v[20:23], v[164:167], v[188:191], v[20:23]
	v_mfma_f32_16x16x32_bf16 v[8:11], v[156:159], v[196:199], v[8:11]
	v_mfma_f32_16x16x32_bf16 v[4:7], v[164:167], v[196:199], v[4:7]
	s_barrier
	s_add_i32 s74, s74, 2
	s_add_u32 s50, s50, 0x100
	s_addc_u32 s51, s51, 0
	s_cmp_gt_u32 s74, 61
.LBB0_1459:
	s_add_u32 s4, s48, s50
	s_addc_u32 s5, s49, s51
	s_add_u32 s75, s4, 0x100
	s_addc_u32 s76, s5, 0
	s_add_u32 s52, s72, s50
	s_addc_u32 s53, s73, s51
	s_add_u32 s4, s4, 0x180
	s_addc_u32 s5, s5, 0
	s_add_i32 s77, 0, 0x10000
	s_add_i32 s78, 0, 0x14000
	v_add_u32_e32 v148, s77, v203
	v_add_u32_e32 v164, s78, v203
	ds_read_b128 v[120:123], v148
	ds_read_b128 v[132:135], v148 offset:1024
	ds_read_b128 v[144:147], v148 offset:2048
	ds_read_b128 v[148:151], v148 offset:3072
	ds_read_b128 v[152:155], v164
	ds_read_b128 v[156:159], v164 offset:1024
	ds_read_b128 v[160:163], v164 offset:2048
	ds_read_b128 v[164:167], v164 offset:3072
	s_cmpk_eq_i32 s50, 0x1f00
	s_cselect_b32 s13, s71, s5
	s_cselect_b32 s12, s70, s4
	s_cselect_b32 s53, s37, s53
	s_cselect_b32 s52, s69, s52
	s_cselect_b32 s5, s41, s76
	s_cselect_b32 s4, s68, s75
	v_lshl_add_u64 v[214:215], v[112:113], 0, s[50:51]
	s_add_i32 m0, s17, 0xc000
	ds_read_b128 v[168:171], v233
	ds_read_b128 v[172:175], v233 offset:1024
	ds_read_b128 v[176:179], v233 offset:2048
	ds_read_b128 v[180:183], v233 offset:3072
	ds_read_b128 v[184:187], v233 offset:4096
	ds_read_b128 v[188:191], v233 offset:5120
	ds_read_b128 v[192:195], v233 offset:6144
	ds_read_b128 v[196:199], v233 offset:7168
	global_load_lds_dwordx4 v[214:215], off
	v_lshl_add_u64 v[214:215], v[114:115], 0, s[50:51]
	s_add_i32 m0, s17, 0xe000
	s_nop 0
	global_load_lds_dwordx4 v[214:215], off
	s_waitcnt vmcnt(8)
	s_waitcnt lgkmcnt(0)
	s_barrier
	v_mfma_f32_16x16x32_bf16 v[140:143], v[120:123], v[168:171], v[140:143]
	v_mfma_f32_16x16x32_bf16 v[136:139], v[144:147], v[168:171], v[136:139]
	v_mfma_f32_16x16x32_bf16 v[116:119], v[120:123], v[176:179], v[116:119]
	v_mfma_f32_16x16x32_bf16 v[108:111], v[144:147], v[176:179], v[108:111]
	v_mfma_f32_16x16x32_bf16 v[96:99], v[120:123], v[184:187], v[96:99]
	v_mfma_f32_16x16x32_bf16 v[92:95], v[144:147], v[184:187], v[92:95]
	v_mfma_f32_16x16x32_bf16 v[80:83], v[120:123], v[192:195], v[80:83]
	v_mfma_f32_16x16x32_bf16 v[76:79], v[144:147], v[192:195], v[76:79]
	v_mfma_f32_16x16x32_bf16 v[140:143], v[132:135], v[172:175], v[140:143]
	v_mfma_f32_16x16x32_bf16 v[136:139], v[148:151], v[172:175], v[136:139]
	v_mfma_f32_16x16x32_bf16 v[116:119], v[132:135], v[180:183], v[116:119]
	v_mfma_f32_16x16x32_bf16 v[108:111], v[148:151], v[180:183], v[108:111]
	v_mfma_f32_16x16x32_bf16 v[96:99], v[132:135], v[188:191], v[96:99]
	v_mfma_f32_16x16x32_bf16 v[92:95], v[148:151], v[188:191], v[92:95]
	v_mfma_f32_16x16x32_bf16 v[80:83], v[132:135], v[196:199], v[80:83]
	v_mfma_f32_16x16x32_bf16 v[76:79], v[148:151], v[196:199], v[76:79]
	v_mfma_f32_16x16x32_bf16 v[128:131], v[152:155], v[168:171], v[128:131]
	v_mfma_f32_16x16x32_bf16 v[124:127], v[160:163], v[168:171], v[124:127]
	v_mfma_f32_16x16x32_bf16 v[104:107], v[152:155], v[176:179], v[104:107]
	v_mfma_f32_16x16x32_bf16 v[100:103], v[160:163], v[176:179], v[100:103]
	v_mfma_f32_16x16x32_bf16 v[88:91], v[152:155], v[184:187], v[88:91]
	v_mfma_f32_16x16x32_bf16 v[84:87], v[160:163], v[184:187], v[84:87]
	v_mfma_f32_16x16x32_bf16 v[72:75], v[152:155], v[192:195], v[72:75]
	v_mfma_f32_16x16x32_bf16 v[68:71], v[160:163], v[192:195], v[68:71]
	v_mfma_f32_16x16x32_bf16 v[128:131], v[156:159], v[172:175], v[128:131]
	v_mfma_f32_16x16x32_bf16 v[124:127], v[164:167], v[172:175], v[124:127]
	v_mfma_f32_16x16x32_bf16 v[104:107], v[156:159], v[180:183], v[104:107]
	v_mfma_f32_16x16x32_bf16 v[100:103], v[164:167], v[180:183], v[100:103]
	v_mfma_f32_16x16x32_bf16 v[88:91], v[156:159], v[188:191], v[88:91]
	v_mfma_f32_16x16x32_bf16 v[84:87], v[164:167], v[188:191], v[84:87]
	v_mfma_f32_16x16x32_bf16 v[72:75], v[156:159], v[196:199], v[72:75]
	v_mfma_f32_16x16x32_bf16 v[68:71], v[164:167], v[196:199], v[68:71]
	s_barrier
	s_add_i32 s75, s77, s16
	v_lshl_add_u64 v[214:215], s[52:53], 0, v[2:3]
	s_mov_b32 m0, s75
	ds_read_b128 v[168:171], v233 offset:16384
	ds_read_b128 v[172:175], v233 offset:17408
	ds_read_b128 v[176:179], v233 offset:18432
	ds_read_b128 v[180:183], v233 offset:19456
	ds_read_b128 v[184:187], v233 offset:20480
	ds_read_b128 v[188:191], v233 offset:21504
	ds_read_b128 v[192:195], v233 offset:22528
	ds_read_b128 v[196:199], v233 offset:23552
	global_load_lds_dwordx4 v[214:215], off
	s_add_i32 m0, s75, 0x2000
	s_add_u32 s76, s52, 0x100000
	v_lshl_add_u64 v[216:217], s[52:53], 0, v[204:205]
	s_addc_u32 s77, s53, 0
	s_add_i32 s75, s78, s16
	global_load_lds_dwordx4 v[216:217], off
	v_lshl_add_u64 v[218:219], s[76:77], 0, v[2:3]
	s_mov_b32 m0, s75
	s_nop 0
	global_load_lds_dwordx4 v[218:219], off
	v_lshl_add_u64 v[218:219], s[76:77], 0, v[204:205]
	s_add_i32 m0, s75, 0x2000
	s_nop 0
	global_load_lds_dwordx4 v[218:219], off
	v_lshl_add_u64 v[218:219], s[4:5], 0, v[208:209]
	s_mov_b32 m0, s17
	s_nop 0
	global_load_lds_dwordx4 v[218:219], off
	v_lshl_add_u64 v[218:219], s[4:5], 0, v[206:207]
	s_mov_b32 m0, s46
	s_nop 0
	global_load_lds_dwordx4 v[218:219], off
	s_waitcnt vmcnt(8)
	s_waitcnt lgkmcnt(0)
	s_barrier
	v_mfma_f32_16x16x32_bf16 v[64:67], v[120:123], v[168:171], v[64:67]
	v_mfma_f32_16x16x32_bf16 v[60:63], v[144:147], v[168:171], v[60:63]
	v_mfma_f32_16x16x32_bf16 v[48:51], v[120:123], v[176:179], v[48:51]
	v_mfma_f32_16x16x32_bf16 v[44:47], v[144:147], v[176:179], v[44:47]
	v_mfma_f32_16x16x32_bf16 v[32:35], v[120:123], v[184:187], v[32:35]
	v_mfma_f32_16x16x32_bf16 v[28:31], v[144:147], v[184:187], v[28:31]
	v_mfma_f32_16x16x32_bf16 v[16:19], v[120:123], v[192:195], v[16:19]
	v_mfma_f32_16x16x32_bf16 v[12:15], v[144:147], v[192:195], v[12:15]
	v_mfma_f32_16x16x32_bf16 v[64:67], v[132:135], v[172:175], v[64:67]
	v_mfma_f32_16x16x32_bf16 v[60:63], v[148:151], v[172:175], v[60:63]
	v_mfma_f32_16x16x32_bf16 v[48:51], v[132:135], v[180:183], v[48:51]
	v_mfma_f32_16x16x32_bf16 v[44:47], v[148:151], v[180:183], v[44:47]
	v_mfma_f32_16x16x32_bf16 v[32:35], v[132:135], v[188:191], v[32:35]
	v_mfma_f32_16x16x32_bf16 v[28:31], v[148:151], v[188:191], v[28:31]
	v_mfma_f32_16x16x32_bf16 v[16:19], v[132:135], v[196:199], v[16:19]
	v_mfma_f32_16x16x32_bf16 v[12:15], v[148:151], v[196:199], v[12:15]
	v_mfma_f32_16x16x32_bf16 v[56:59], v[152:155], v[168:171], v[56:59]
	v_mfma_f32_16x16x32_bf16 v[52:55], v[160:163], v[168:171], v[52:55]
	v_mfma_f32_16x16x32_bf16 v[40:43], v[152:155], v[176:179], v[40:43]
	v_mfma_f32_16x16x32_bf16 v[36:39], v[160:163], v[176:179], v[36:39]
	v_mfma_f32_16x16x32_bf16 v[24:27], v[152:155], v[184:187], v[24:27]
	v_mfma_f32_16x16x32_bf16 v[20:23], v[160:163], v[184:187], v[20:23]
	v_mfma_f32_16x16x32_bf16 v[8:11], v[152:155], v[192:195], v[8:11]
	v_mfma_f32_16x16x32_bf16 v[4:7], v[160:163], v[192:195], v[4:7]
	v_mfma_f32_16x16x32_bf16 v[56:59], v[156:159], v[172:175], v[56:59]
	v_mfma_f32_16x16x32_bf16 v[52:55], v[164:167], v[172:175], v[52:55]
	v_mfma_f32_16x16x32_bf16 v[40:43], v[156:159], v[180:183], v[40:43]
	v_mfma_f32_16x16x32_bf16 v[36:39], v[164:167], v[180:183], v[36:39]
	v_mfma_f32_16x16x32_bf16 v[24:27], v[156:159], v[188:191], v[24:27]
	v_mfma_f32_16x16x32_bf16 v[20:23], v[164:167], v[188:191], v[20:23]
	v_mfma_f32_16x16x32_bf16 v[8:11], v[156:159], v[196:199], v[8:11]
	v_mfma_f32_16x16x32_bf16 v[4:7], v[164:167], v[196:199], v[4:7]
	s_barrier
	s_add_i32 s75, 0, 0x18000
	s_add_i32 s76, 0, 0x1c000
	v_add_u32_e32 v148, s75, v203
	v_add_u32_e32 v164, s76, v203
	ds_read_b128 v[120:123], v148
	ds_read_b128 v[132:135], v148 offset:1024
	ds_read_b128 v[144:147], v148 offset:2048
	ds_read_b128 v[148:151], v148 offset:3072
	ds_read_b128 v[152:155], v164
	ds_read_b128 v[156:159], v164 offset:1024
	ds_read_b128 v[160:163], v164 offset:2048
	ds_read_b128 v[164:167], v164 offset:3072
	s_add_u32 s4, s4, 0x100000
	s_addc_u32 s5, s5, 0
	s_mov_b32 m0, s47
	v_lshl_add_u64 v[218:219], s[4:5], 0, v[208:209]
	ds_read_b128 v[168:171], v233 offset:32768
	ds_read_b128 v[172:175], v233 offset:33792
	ds_read_b128 v[176:179], v233 offset:34816
	ds_read_b128 v[180:183], v233 offset:35840
	ds_read_b128 v[184:187], v233 offset:36864
	ds_read_b128 v[188:191], v233 offset:37888
	ds_read_b128 v[192:195], v233 offset:38912
	ds_read_b128 v[196:199], v233 offset:39936
	global_load_lds_dwordx4 v[218:219], off
	v_lshl_add_u64 v[218:219], s[4:5], 0, v[206:207]
	s_mov_b32 m0, s58
	s_nop 0
	global_load_lds_dwordx4 v[218:219], off
	s_waitcnt vmcnt(8)
	s_waitcnt lgkmcnt(0)
	s_barrier
	v_mfma_f32_16x16x32_bf16 v[140:143], v[120:123], v[168:171], v[140:143]
	v_mfma_f32_16x16x32_bf16 v[136:139], v[144:147], v[168:171], v[136:139]
	v_mfma_f32_16x16x32_bf16 v[116:119], v[120:123], v[176:179], v[116:119]
	v_mfma_f32_16x16x32_bf16 v[108:111], v[144:147], v[176:179], v[108:111]
	v_mfma_f32_16x16x32_bf16 v[96:99], v[120:123], v[184:187], v[96:99]
	v_mfma_f32_16x16x32_bf16 v[92:95], v[144:147], v[184:187], v[92:95]
	v_mfma_f32_16x16x32_bf16 v[80:83], v[120:123], v[192:195], v[80:83]
	v_mfma_f32_16x16x32_bf16 v[76:79], v[144:147], v[192:195], v[76:79]
	v_mfma_f32_16x16x32_bf16 v[140:143], v[132:135], v[172:175], v[140:143]
	v_mfma_f32_16x16x32_bf16 v[136:139], v[148:151], v[172:175], v[136:139]
	v_mfma_f32_16x16x32_bf16 v[116:119], v[132:135], v[180:183], v[116:119]
	v_mfma_f32_16x16x32_bf16 v[108:111], v[148:151], v[180:183], v[108:111]
	v_mfma_f32_16x16x32_bf16 v[96:99], v[132:135], v[188:191], v[96:99]
	v_mfma_f32_16x16x32_bf16 v[92:95], v[148:151], v[188:191], v[92:95]
	v_mfma_f32_16x16x32_bf16 v[80:83], v[132:135], v[196:199], v[80:83]
	v_mfma_f32_16x16x32_bf16 v[76:79], v[148:151], v[196:199], v[76:79]
	v_mfma_f32_16x16x32_bf16 v[128:131], v[152:155], v[168:171], v[128:131]
	v_mfma_f32_16x16x32_bf16 v[124:127], v[160:163], v[168:171], v[124:127]
	v_mfma_f32_16x16x32_bf16 v[104:107], v[152:155], v[176:179], v[104:107]
	v_mfma_f32_16x16x32_bf16 v[100:103], v[160:163], v[176:179], v[100:103]
	v_mfma_f32_16x16x32_bf16 v[88:91], v[152:155], v[184:187], v[88:91]
	v_mfma_f32_16x16x32_bf16 v[84:87], v[160:163], v[184:187], v[84:87]
	v_mfma_f32_16x16x32_bf16 v[72:75], v[152:155], v[192:195], v[72:75]
	v_mfma_f32_16x16x32_bf16 v[68:71], v[160:163], v[192:195], v[68:71]
	v_mfma_f32_16x16x32_bf16 v[128:131], v[156:159], v[172:175], v[128:131]
	v_mfma_f32_16x16x32_bf16 v[124:127], v[164:167], v[172:175], v[124:127]
	v_mfma_f32_16x16x32_bf16 v[104:107], v[156:159], v[180:183], v[104:107]
	v_mfma_f32_16x16x32_bf16 v[100:103], v[164:167], v[180:183], v[100:103]
	v_mfma_f32_16x16x32_bf16 v[88:91], v[156:159], v[188:191], v[88:91]
	v_mfma_f32_16x16x32_bf16 v[84:87], v[164:167], v[188:191], v[84:87]
	v_mfma_f32_16x16x32_bf16 v[72:75], v[156:159], v[196:199], v[72:75]
	v_mfma_f32_16x16x32_bf16 v[68:71], v[164:167], v[196:199], v[68:71]
	s_barrier
	s_add_i32 s4, s75, s16
	v_lshl_add_u64 v[214:215], v[214:215], 0, s[34:35]
	s_mov_b32 m0, s4
	ds_read_b128 v[168:171], v233 offset:49152
	ds_read_b128 v[172:175], v233 offset:50176
	ds_read_b128 v[176:179], v233 offset:51200
	ds_read_b128 v[180:183], v233 offset:52224
	ds_read_b128 v[184:187], v233 offset:53248
	ds_read_b128 v[188:191], v233 offset:54272
	ds_read_b128 v[192:195], v233 offset:55296
	ds_read_b128 v[196:199], v233 offset:56320
	global_load_lds_dwordx4 v[214:215], off
	s_add_i32 m0, s4, 0x2000
	s_add_u32 s4, s52, 0x100080
	v_lshl_add_u64 v[214:215], v[216:217], 0, s[34:35]
	s_addc_u32 s5, s53, 0
	s_add_i32 s52, s76, s16
	global_load_lds_dwordx4 v[214:215], off
	v_lshl_add_u64 v[214:215], s[4:5], 0, v[2:3]
	s_mov_b32 m0, s52
	s_nop 0
	global_load_lds_dwordx4 v[214:215], off
	v_lshl_add_u64 v[214:215], s[4:5], 0, v[204:205]
	s_add_i32 m0, s52, 0x2000
	s_nop 0
	global_load_lds_dwordx4 v[214:215], off
	v_lshl_add_u64 v[214:215], s[12:13], 0, v[208:209]
	s_mov_b32 m0, s62
	s_nop 0
	global_load_lds_dwordx4 v[214:215], off
	v_lshl_add_u64 v[214:215], s[12:13], 0, v[206:207]
	s_mov_b32 m0, s63
	s_nop 0
	global_load_lds_dwordx4 v[214:215], off
	s_waitcnt vmcnt(8)
	s_waitcnt lgkmcnt(0)
	s_barrier
	v_mfma_f32_16x16x32_bf16 v[64:67], v[120:123], v[168:171], v[64:67]
	v_mfma_f32_16x16x32_bf16 v[60:63], v[144:147], v[168:171], v[60:63]
	v_mfma_f32_16x16x32_bf16 v[48:51], v[120:123], v[176:179], v[48:51]
	v_mfma_f32_16x16x32_bf16 v[44:47], v[144:147], v[176:179], v[44:47]
	v_mfma_f32_16x16x32_bf16 v[32:35], v[120:123], v[184:187], v[32:35]
	v_mfma_f32_16x16x32_bf16 v[28:31], v[144:147], v[184:187], v[28:31]
	v_mfma_f32_16x16x32_bf16 v[16:19], v[120:123], v[192:195], v[16:19]
	v_mfma_f32_16x16x32_bf16 v[12:15], v[144:147], v[192:195], v[12:15]
	v_mfma_f32_16x16x32_bf16 v[64:67], v[132:135], v[172:175], v[64:67]
	v_mfma_f32_16x16x32_bf16 v[60:63], v[148:151], v[172:175], v[60:63]
	v_mfma_f32_16x16x32_bf16 v[48:51], v[132:135], v[180:183], v[48:51]
	v_mfma_f32_16x16x32_bf16 v[44:47], v[148:151], v[180:183], v[44:47]
	v_mfma_f32_16x16x32_bf16 v[32:35], v[132:135], v[188:191], v[32:35]
	v_mfma_f32_16x16x32_bf16 v[28:31], v[148:151], v[188:191], v[28:31]
	v_mfma_f32_16x16x32_bf16 v[16:19], v[132:135], v[196:199], v[16:19]
	v_mfma_f32_16x16x32_bf16 v[12:15], v[148:151], v[196:199], v[12:15]
	v_mfma_f32_16x16x32_bf16 v[56:59], v[152:155], v[168:171], v[56:59]
	v_mfma_f32_16x16x32_bf16 v[52:55], v[160:163], v[168:171], v[52:55]
	v_mfma_f32_16x16x32_bf16 v[40:43], v[152:155], v[176:179], v[40:43]
	v_mfma_f32_16x16x32_bf16 v[36:39], v[160:163], v[176:179], v[36:39]
	v_mfma_f32_16x16x32_bf16 v[24:27], v[152:155], v[184:187], v[24:27]
	v_mfma_f32_16x16x32_bf16 v[20:23], v[160:163], v[184:187], v[20:23]
	v_mfma_f32_16x16x32_bf16 v[8:11], v[152:155], v[192:195], v[8:11]
	v_mfma_f32_16x16x32_bf16 v[4:7], v[160:163], v[192:195], v[4:7]
	v_mfma_f32_16x16x32_bf16 v[56:59], v[156:159], v[172:175], v[56:59]
	v_mfma_f32_16x16x32_bf16 v[52:55], v[164:167], v[172:175], v[52:55]
	v_mfma_f32_16x16x32_bf16 v[40:43], v[156:159], v[180:183], v[40:43]
	v_mfma_f32_16x16x32_bf16 v[36:39], v[164:167], v[180:183], v[36:39]
	v_mfma_f32_16x16x32_bf16 v[24:27], v[156:159], v[188:191], v[24:27]
	v_mfma_f32_16x16x32_bf16 v[20:23], v[164:167], v[188:191], v[20:23]
	v_mfma_f32_16x16x32_bf16 v[8:11], v[156:159], v[196:199], v[8:11]
	v_mfma_f32_16x16x32_bf16 v[4:7], v[164:167], v[196:199], v[4:7]
	s_barrier
	s_add_i32 s74, s74, 2
	s_add_u32 s50, s50, 0x100
	s_addc_u32 s51, s51, 0
	s_cmp_gt_u32 s74, 61
	s_cbranch_scc0 .LBB0_1459
	s_and_b64 vcc, exec, s[22:23]
	s_cbranch_vccz .LBB0_1462
	s_barrier
